# topk sort networks: v_cmp_gt+2x v_cndmask compare-exchange replaced by v_max_f32/v_min_f32 on the packed keys; useless s_nops removed
# speedup vs baseline: 1.0102x; 1.0102x over previous
.LBB0_704:
	v_cndmask_b32_e64 v0, 0, 1, s[6:7]
	s_lshl_b32 s36, s8, 8
	v_cmp_ne_u32_e32 vcc, 1, v0
	v_lshl_add_u64 v[0:1], v[178:179], 0, s[36:37]
	global_load_dwordx4 v[44:47], v[0:1], off
	global_load_dwordx4 v[40:43], v[0:1], off offset:32
	global_load_dwordx4 v[36:39], v[0:1], off offset:64
	global_load_dwordx4 v[32:35], v[0:1], off offset:96
	global_load_dwordx4 v[28:31], v[0:1], off offset:128
	global_load_dwordx4 v[24:27], v[0:1], off offset:160
	global_load_dwordx4 v[20:23], v[0:1], off offset:192
	global_load_dwordx4 v[16:19], v[0:1], off offset:224
	v_lshl_or_b32 v180, s8, 7, v209
	v_ashrrev_i32_e32 v181, 31, v180
	v_lshlrev_b64 v[0:1], 8, v[180:181]
	v_lshl_add_u64 v[60:61], v[64:65], 0, v[0:1]
	global_load_dwordx4 v[0:3], v[60:61], off
	global_load_dwordx4 v[48:51], v[60:61], off offset:32
	global_load_dwordx4 v[52:55], v[60:61], off offset:64
	global_load_dwordx4 v[56:59], v[60:61], off offset:96
	s_nop 15
	s_nop 15
	s_waitcnt vmcnt(0)
	v_mfma_f32_32x32x16_bf16 v[0:15], v[0:3], v[44:47], 0
	v_mfma_f32_32x32x16_bf16 v[0:15], v[48:51], v[40:43], v[0:15]
	v_mfma_f32_32x32x16_bf16 v[0:15], v[52:55], v[36:39], v[0:15]
	v_mfma_f32_32x32x16_bf16 v[0:15], v[56:59], v[32:35], v[0:15]
	s_nop 15
	s_nop 15
	global_load_dwordx4 v[48:51], v[60:61], off offset:128
	global_load_dwordx4 v[52:55], v[60:61], off offset:160
	global_load_dwordx4 v[56:59], v[60:61], off offset:192
	s_nop 0
	global_load_dwordx4 v[60:63], v[60:61], off offset:224
	s_nop 15
	s_nop 15
	s_waitcnt vmcnt(3)
	v_mfma_f32_32x32x16_bf16 v[0:15], v[48:51], v[28:31], v[0:15]
	s_waitcnt vmcnt(2)
	v_mfma_f32_32x32x16_bf16 v[0:15], v[52:55], v[24:27], v[0:15]
	s_waitcnt vmcnt(1)
	v_mfma_f32_32x32x16_bf16 v[0:15], v[56:59], v[20:23], v[0:15]
	s_waitcnt vmcnt(0)
	v_mfma_f32_32x32x16_bf16 v[0:15], v[60:63], v[16:19], v[0:15]
	s_nop 15
	s_nop 15
	v_or_b32_e32 v49, 1, v66
	v_xor_b32_e32 v51, 0x7e, v66
	s_nop 9
	v_cmp_gt_i32_e64 s[6:7], 0, v1
	v_xor_b32_e32 v48, 0x7f, v66
	v_and_b32_e32 v1, 0xffffff80, v1
	v_cndmask_b32_e64 v49, v51, v49, s[6:7]
	v_cmp_gt_i32_e64 s[6:7], 0, v0
	v_and_b32_e32 v0, 0xffffff80, v0
	v_or_b32_e32 v210, v49, v1
	v_cndmask_b32_e64 v48, v48, v66, s[6:7]
	v_or_b32_e32 v211, v48, v0
	v_or_b32_e32 v48, 32, v180
	v_ashrrev_i32_e32 v49, 31, v48
	v_lshlrev_b64 v[48:49], 8, v[48:49]
	v_lshl_add_u64 v[182:183], v[64:65], 0, v[48:49]
	global_load_dwordx4 v[60:63], v[182:183], off
	global_load_dwordx4 v[56:59], v[182:183], off offset:32
	global_load_dwordx4 v[52:55], v[182:183], off offset:64
	global_load_dwordx4 v[48:51], v[182:183], off offset:96
	v_or_b32_e32 v1, 3, v66
	v_xor_b32_e32 v173, 0x7c, v66
	v_cmp_gt_i32_e64 s[6:7], 0, v3
	v_or_b32_e32 v0, 2, v66
	v_xor_b32_e32 v190, 0x7d, v66
	v_cndmask_b32_e64 v1, v173, v1, s[6:7]
	v_cmp_gt_i32_e64 s[6:7], 0, v2
	v_and_b32_e32 v3, 0xffffff80, v3
	v_and_b32_e32 v2, 0xffffff80, v2
	v_cndmask_b32_e64 v0, v190, v0, s[6:7]
	v_or_b32_e32 v173, v1, v3
	v_or_b32_e32 v1, 9, v66
	v_xor_b32_e32 v3, 0x76, v66
	v_cmp_gt_i32_e64 s[6:7], 0, v5
	v_or_b32_e32 v212, v0, v2
	v_or_b32_e32 v0, 8, v66
	v_cndmask_b32_e64 v1, v3, v1, s[6:7]
	v_xor_b32_e32 v2, 0x77, v66
	v_cmp_gt_i32_e64 s[6:7], 0, v4
	v_and_b32_e32 v3, 0xffffff80, v4
	s_nop 0
	v_cndmask_b32_e64 v0, v2, v0, s[6:7]
	v_and_b32_e32 v2, 0xffffff80, v5
	v_or_b32_e32 v213, v1, v2
	v_or_b32_e32 v214, v0, v3
	v_or_b32_e32 v1, 11, v66
	v_xor_b32_e32 v3, 0x74, v66
	v_cmp_gt_i32_e64 s[6:7], 0, v7
	v_or_b32_e32 v0, 10, v66
	v_xor_b32_e32 v2, 0x75, v66
	v_cndmask_b32_e64 v1, v3, v1, s[6:7]
	v_cmp_gt_i32_e64 s[6:7], 0, v6
	v_and_b32_e32 v3, 0xffffff80, v6
	s_nop 0
	v_cndmask_b32_e64 v0, v2, v0, s[6:7]
	v_and_b32_e32 v2, 0xffffff80, v7
	v_or_b32_e32 v215, v1, v2
	v_or_b32_e32 v216, v0, v3
	v_or_b32_e32 v1, 17, v66
	v_xor_b32_e32 v3, 0x6e, v66
	v_cmp_gt_i32_e64 s[6:7], 0, v9
	v_or_b32_e32 v0, 16, v66
	v_xor_b32_e32 v2, 0x6f, v66
	v_cndmask_b32_e64 v1, v3, v1, s[6:7]
	v_cmp_gt_i32_e64 s[6:7], 0, v8
	v_and_b32_e32 v3, 0xffffff80, v8
	s_nop 0
	v_cndmask_b32_e64 v0, v2, v0, s[6:7]
	v_and_b32_e32 v2, 0xffffff80, v9
	v_or_b32_e32 v217, v1, v2
	v_or_b32_e32 v218, v0, v3
	v_or_b32_e32 v1, 19, v66
	v_xor_b32_e32 v3, 0x6c, v66
	v_cmp_gt_i32_e64 s[6:7], 0, v11
	v_or_b32_e32 v0, 18, v66
	v_xor_b32_e32 v2, 0x6d, v66
	v_cndmask_b32_e64 v1, v3, v1, s[6:7]
	v_cmp_gt_i32_e64 s[6:7], 0, v10
	v_and_b32_e32 v3, 0xffffff80, v10
	s_nop 0
	v_cndmask_b32_e64 v0, v2, v0, s[6:7]
	v_and_b32_e32 v2, 0xffffff80, v11
	v_or_b32_e32 v219, v1, v2
	v_or_b32_e32 v220, v0, v3
	v_or_b32_e32 v1, 25, v66
	v_xor_b32_e32 v3, 0x66, v66
	v_cmp_gt_i32_e64 s[6:7], 0, v13
	v_or_b32_e32 v0, 24, v66
	v_xor_b32_e32 v2, 0x67, v66
	v_cndmask_b32_e64 v1, v3, v1, s[6:7]
	v_cmp_gt_i32_e64 s[6:7], 0, v12
	v_and_b32_e32 v3, 0xffffff80, v12
	s_nop 0
	v_cndmask_b32_e64 v0, v2, v0, s[6:7]
	v_and_b32_e32 v2, 0xffffff80, v13
	v_or_b32_e32 v221, v1, v2
	v_or_b32_e32 v1, 27, v66
	v_cmp_gt_i32_e64 s[6:7], 0, v15
	v_or_b32_e32 v222, v0, v3
	v_and_b32_e32 v2, 0xffffff80, v15
	v_cndmask_b32_e64 v0, v67, v1, s[6:7]
	v_cmp_gt_i32_e64 s[6:7], 0, v14
	v_and_b32_e32 v3, 0xffffff80, v14
	v_or_b32_e32 v223, v0, v2
	v_cndmask_b32_e64 v1, v70, v68, s[6:7]
	v_or_b32_e32 v224, v1, v3
	s_nop 15
	s_nop 15
	s_waitcnt vmcnt(3)
	v_mfma_f32_32x32x16_bf16 v[0:15], v[60:63], v[44:47], 0
	s_waitcnt vmcnt(2)
	v_mfma_f32_32x32x16_bf16 v[0:15], v[56:59], v[40:43], v[0:15]
	s_waitcnt vmcnt(1)
	v_mfma_f32_32x32x16_bf16 v[0:15], v[52:55], v[36:39], v[0:15]
	s_waitcnt vmcnt(0)
	v_mfma_f32_32x32x16_bf16 v[0:15], v[48:51], v[32:35], v[0:15]
	s_nop 15
	s_nop 15
	global_load_dwordx4 v[48:51], v[182:183], off offset:128
	global_load_dwordx4 v[52:55], v[182:183], off offset:160
	global_load_dwordx4 v[56:59], v[182:183], off offset:192
	global_load_dwordx4 v[60:63], v[182:183], off offset:224
	s_nop 15
	s_nop 15
	s_waitcnt vmcnt(3)
	v_mfma_f32_32x32x16_bf16 v[0:15], v[48:51], v[28:31], v[0:15]
	s_waitcnt vmcnt(2)
	v_mfma_f32_32x32x16_bf16 v[0:15], v[52:55], v[24:27], v[0:15]
	s_waitcnt vmcnt(1)
	v_mfma_f32_32x32x16_bf16 v[0:15], v[56:59], v[20:23], v[0:15]
	s_waitcnt vmcnt(0)
	v_mfma_f32_32x32x16_bf16 v[0:15], v[60:63], v[16:19], v[0:15]
	s_nop 15
	s_nop 15
	v_or_b32_e32 v48, 64, v180
	v_ashrrev_i32_e32 v49, 31, v48
	v_lshlrev_b64 v[48:49], 8, v[48:49]
	v_lshl_add_u64 v[182:183], v[64:65], 0, v[48:49]
	global_load_dwordx4 v[60:63], v[182:183], off
	global_load_dwordx4 v[56:59], v[182:183], off offset:32
	global_load_dwordx4 v[52:55], v[182:183], off offset:64
	global_load_dwordx4 v[48:51], v[182:183], off offset:96
	s_nop 3
	v_cmp_gt_i32_e64 s[6:7], 0, v1
	v_and_b32_e32 v1, 0xffffff80, v1
	s_nop 0
	v_cndmask_b32_e64 v181, v71, v69, s[6:7]
	v_cmp_gt_i32_e64 s[6:7], 0, v0
	v_and_b32_e32 v0, 0xffffff80, v0
	v_or_b32_e32 v225, v181, v1
	v_cndmask_b32_e64 v190, v74, v72, s[6:7]
	v_cmp_gt_i32_e64 s[6:7], 0, v3
	v_or_b32_e32 v226, v190, v0
	v_and_b32_e32 v3, 0xffffff80, v3
	v_cndmask_b32_e64 v0, v75, v73, s[6:7]
	v_cmp_gt_i32_e64 s[6:7], 0, v2
	v_and_b32_e32 v2, 0xffffff80, v2
	v_or_b32_e32 v227, v0, v3
	v_cndmask_b32_e64 v1, v78, v76, s[6:7]
	v_cmp_gt_i32_e64 s[6:7], 0, v5
	v_or_b32_e32 v228, v1, v2
	v_and_b32_e32 v2, 0xffffff80, v5
	v_cndmask_b32_e64 v0, v79, v77, s[6:7]
	v_cmp_gt_i32_e64 s[6:7], 0, v4
	v_and_b32_e32 v3, 0xffffff80, v4
	v_or_b32_e32 v229, v0, v2
	v_cndmask_b32_e64 v1, v82, v80, s[6:7]
	v_cmp_gt_i32_e64 s[6:7], 0, v7
	v_or_b32_e32 v230, v1, v3
	v_and_b32_e32 v2, 0xffffff80, v7
	v_cndmask_b32_e64 v0, v83, v81, s[6:7]
	v_cmp_gt_i32_e64 s[6:7], 0, v6
	v_and_b32_e32 v3, 0xffffff80, v6
	v_or_b32_e32 v231, v0, v2
	v_cndmask_b32_e64 v1, v86, v84, s[6:7]
	v_cmp_gt_i32_e64 s[6:7], 0, v9
	v_or_b32_e32 v232, v1, v3
	v_and_b32_e32 v2, 0xffffff80, v9
	v_cndmask_b32_e64 v0, v87, v85, s[6:7]
	v_cmp_gt_i32_e64 s[6:7], 0, v8
	v_and_b32_e32 v3, 0xffffff80, v8
	v_or_b32_e32 v233, v0, v2
	v_cndmask_b32_e64 v1, v90, v88, s[6:7]
	v_cmp_gt_i32_e64 s[6:7], 0, v11
	v_or_b32_e32 v234, v1, v3
	v_and_b32_e32 v2, 0xffffff80, v11
	v_cndmask_b32_e64 v0, v91, v89, s[6:7]
	v_cmp_gt_i32_e64 s[6:7], 0, v10
	v_and_b32_e32 v3, 0xffffff80, v10
	v_or_b32_e32 v235, v0, v2
	v_cndmask_b32_e64 v1, v94, v92, s[6:7]
	v_cmp_gt_i32_e64 s[6:7], 0, v13
	v_or_b32_e32 v236, v1, v3
	v_and_b32_e32 v2, 0xffffff80, v13
	v_cndmask_b32_e64 v0, v95, v93, s[6:7]
	v_cmp_gt_i32_e64 s[6:7], 0, v12
	v_and_b32_e32 v3, 0xffffff80, v12
	v_or_b32_e32 v237, v0, v2
	v_cndmask_b32_e64 v1, v98, v96, s[6:7]
	v_cmp_gt_i32_e64 s[6:7], 0, v15
	v_or_b32_e32 v238, v1, v3
	v_and_b32_e32 v2, 0xffffff80, v15
	v_cndmask_b32_e64 v0, v99, v97, s[6:7]
	v_cmp_gt_i32_e64 s[6:7], 0, v14
	v_and_b32_e32 v3, 0xffffff80, v14
	v_or_b32_e32 v239, v0, v2
	v_cndmask_b32_e64 v1, v102, v100, s[6:7]
	v_or_b32_e32 v240, v1, v3
	s_nop 15
	s_nop 15
	s_waitcnt vmcnt(3)
	v_mfma_f32_32x32x16_bf16 v[0:15], v[60:63], v[44:47], 0
	s_waitcnt vmcnt(2)
	v_mfma_f32_32x32x16_bf16 v[0:15], v[56:59], v[40:43], v[0:15]
	s_waitcnt vmcnt(1)
	v_mfma_f32_32x32x16_bf16 v[0:15], v[52:55], v[36:39], v[0:15]
	s_waitcnt vmcnt(0)
	v_mfma_f32_32x32x16_bf16 v[0:15], v[48:51], v[32:35], v[0:15]
	s_nop 15
	s_nop 15
	global_load_dwordx4 v[48:51], v[182:183], off offset:128
	global_load_dwordx4 v[52:55], v[182:183], off offset:160
	global_load_dwordx4 v[56:59], v[182:183], off offset:192
	global_load_dwordx4 v[60:63], v[182:183], off offset:224
	s_nop 15
	s_nop 15
	s_waitcnt vmcnt(3)
	v_mfma_f32_32x32x16_bf16 v[0:15], v[48:51], v[28:31], v[0:15]
	s_waitcnt vmcnt(2)
	v_mfma_f32_32x32x16_bf16 v[0:15], v[52:55], v[24:27], v[0:15]
	s_waitcnt vmcnt(1)
	v_mfma_f32_32x32x16_bf16 v[0:15], v[56:59], v[20:23], v[0:15]
	s_waitcnt vmcnt(0)
	v_mfma_f32_32x32x16_bf16 v[0:15], v[60:63], v[16:19], v[0:15]
	s_nop 15
	s_nop 15
	v_or_b32_e32 v48, 0x60, v180
	v_ashrrev_i32_e32 v49, 31, v48
	v_lshlrev_b64 v[48:49], 8, v[48:49]
	v_lshl_add_u64 v[180:181], v[64:65], 0, v[48:49]
	global_load_dwordx4 v[60:63], v[180:181], off
	global_load_dwordx4 v[56:59], v[180:181], off offset:32
	global_load_dwordx4 v[52:55], v[180:181], off offset:64
	global_load_dwordx4 v[48:51], v[180:181], off offset:96
	s_nop 3
	v_cmp_gt_i32_e64 s[6:7], 0, v1
	v_and_b32_e32 v1, 0xffffff80, v1
	s_nop 0
	v_cndmask_b32_e64 v182, v103, v101, s[6:7]
	v_cmp_gt_i32_e64 s[6:7], 0, v0
	v_and_b32_e32 v0, 0xffffff80, v0
	v_or_b32_e32 v182, v182, v1
	v_cndmask_b32_e64 v183, v106, v104, s[6:7]
	v_cmp_gt_i32_e64 s[6:7], 0, v3
	v_or_b32_e32 v183, v183, v0
	v_and_b32_e32 v3, 0xffffff80, v3
	v_cndmask_b32_e64 v0, v107, v105, s[6:7]
	v_cmp_gt_i32_e64 s[6:7], 0, v2
	v_and_b32_e32 v2, 0xffffff80, v2
	v_or_b32_e32 v241, v0, v3
	v_cndmask_b32_e64 v1, v110, v108, s[6:7]
	v_cmp_gt_i32_e64 s[6:7], 0, v5
	v_or_b32_e32 v242, v1, v2
	v_and_b32_e32 v2, 0xffffff80, v5
	v_cndmask_b32_e64 v0, v111, v109, s[6:7]
	v_cmp_gt_i32_e64 s[6:7], 0, v4
	v_and_b32_e32 v3, 0xffffff80, v4
	v_or_b32_e32 v243, v0, v2
	v_cndmask_b32_e64 v1, v114, v112, s[6:7]
	v_cmp_gt_i32_e64 s[6:7], 0, v7
	v_or_b32_e32 v244, v1, v3
	v_and_b32_e32 v2, 0xffffff80, v7
	v_cndmask_b32_e64 v0, v115, v113, s[6:7]
	v_cmp_gt_i32_e64 s[6:7], 0, v6
	v_and_b32_e32 v3, 0xffffff80, v6
	v_or_b32_e32 v245, v0, v2
	v_cndmask_b32_e64 v1, v118, v116, s[6:7]
	v_cmp_gt_i32_e64 s[6:7], 0, v9
	v_or_b32_e32 v246, v1, v3
	v_and_b32_e32 v2, 0xffffff80, v9
	v_cndmask_b32_e64 v0, v119, v117, s[6:7]
	v_cmp_gt_i32_e64 s[6:7], 0, v8
	v_and_b32_e32 v3, 0xffffff80, v8
	v_or_b32_e32 v247, v0, v2
	v_cndmask_b32_e64 v1, v122, v120, s[6:7]
	v_cmp_gt_i32_e64 s[6:7], 0, v11
	v_or_b32_e32 v248, v1, v3
	v_and_b32_e32 v2, 0xffffff80, v11
	v_cndmask_b32_e64 v0, v123, v121, s[6:7]
	v_cmp_gt_i32_e64 s[6:7], 0, v10
	v_and_b32_e32 v3, 0xffffff80, v10
	v_or_b32_e32 v249, v0, v2
	v_cndmask_b32_e64 v1, v126, v124, s[6:7]
	v_cmp_gt_i32_e64 s[6:7], 0, v13
	v_or_b32_e32 v250, v1, v3
	v_and_b32_e32 v2, 0xffffff80, v13
	v_cndmask_b32_e64 v0, v127, v125, s[6:7]
	v_cmp_gt_i32_e64 s[6:7], 0, v12
	v_and_b32_e32 v3, 0xffffff80, v12
	v_or_b32_e32 v251, v0, v2
	v_cndmask_b32_e64 v1, v130, v128, s[6:7]
	v_cmp_gt_i32_e64 s[6:7], 0, v15
	v_or_b32_e32 v252, v1, v3
	v_and_b32_e32 v2, 0xffffff80, v15
	v_cndmask_b32_e64 v0, v131, v129, s[6:7]
	v_cmp_gt_i32_e64 s[6:7], 0, v14
	v_and_b32_e32 v3, 0xffffff80, v14
	v_or_b32_e32 v190, v0, v2
	v_cndmask_b32_e64 v1, v134, v132, s[6:7]
	v_or_b32_e32 v195, v1, v3
	s_nop 15
	s_nop 15
	s_waitcnt vmcnt(3)
	v_mfma_f32_32x32x16_bf16 v[0:15], v[60:63], v[44:47], 0
	s_waitcnt vmcnt(2)
	v_mfma_f32_32x32x16_bf16 v[0:15], v[56:59], v[40:43], v[0:15]
	s_waitcnt vmcnt(1)
	v_mfma_f32_32x32x16_bf16 v[0:15], v[52:55], v[36:39], v[0:15]
	s_waitcnt vmcnt(0)
	v_mfma_f32_32x32x16_bf16 v[0:15], v[48:51], v[32:35], v[0:15]
	s_nop 15
	s_nop 15
	global_load_dwordx4 v[32:35], v[180:181], off offset:128
	global_load_dwordx4 v[36:39], v[180:181], off offset:160
	global_load_dwordx4 v[40:43], v[180:181], off offset:192
	global_load_dwordx4 v[44:47], v[180:181], off offset:224
	s_nop 15
	s_nop 15
	s_waitcnt vmcnt(3)
	v_mfma_f32_32x32x16_bf16 v[0:15], v[32:35], v[28:31], v[0:15]
	s_waitcnt vmcnt(2)
	v_mfma_f32_32x32x16_bf16 v[0:15], v[36:39], v[24:27], v[0:15]
	s_waitcnt vmcnt(1)
	v_mfma_f32_32x32x16_bf16 v[0:15], v[40:43], v[20:23], v[0:15]
	s_waitcnt vmcnt(0)
	v_mfma_f32_32x32x16_bf16 v[0:15], v[44:47], v[16:19], v[0:15]
	s_nop 15
	s_nop 15
	s_nop 11
	v_cmp_gt_i32_e64 s[6:7], 0, v1
	v_and_b32_e32 v1, 0xffffff80, v1
	v_and_b32_e32 v18, 0xffffff80, v0
	v_cndmask_b32_e64 v16, v135, v133, s[6:7]
	v_cmp_gt_i32_e64 s[6:7], 0, v0
	v_or_b32_e32 v0, v16, v1
	s_nop 0
	v_cndmask_b32_e64 v17, v138, v136, s[6:7]
	v_cmp_gt_i32_e64 s[6:7], 0, v3
	v_or_b32_e32 v1, v17, v18
	v_and_b32_e32 v3, 0xffffff80, v3
	v_cndmask_b32_e64 v16, v139, v137, s[6:7]
	v_cmp_gt_i32_e64 s[6:7], 0, v2
	v_and_b32_e32 v18, 0xffffff80, v2
	v_or_b32_e32 v2, v16, v3
	v_cndmask_b32_e64 v17, v142, v140, s[6:7]
	v_cmp_gt_i32_e64 s[6:7], 0, v5
	v_or_b32_e32 v3, v17, v18
	v_and_b32_e32 v5, 0xffffff80, v5
	v_cndmask_b32_e64 v16, v143, v141, s[6:7]
	v_cmp_gt_i32_e64 s[6:7], 0, v4
	v_and_b32_e32 v18, 0xffffff80, v4
	v_or_b32_e32 v4, v16, v5
	v_cndmask_b32_e64 v17, v154, v152, s[6:7]
	v_cmp_gt_i32_e64 s[6:7], 0, v7
	v_or_b32_e32 v5, v17, v18
	v_and_b32_e32 v7, 0xffffff80, v7
	v_cndmask_b32_e64 v16, v155, v153, s[6:7]
	v_cmp_gt_i32_e64 s[6:7], 0, v6
	v_and_b32_e32 v18, 0xffffff80, v6
	v_or_b32_e32 v6, v16, v7
	v_cndmask_b32_e64 v17, v158, v156, s[6:7]
	v_cmp_gt_i32_e64 s[6:7], 0, v9
	v_or_b32_e32 v7, v17, v18
	v_and_b32_e32 v9, 0xffffff80, v9
	v_cndmask_b32_e64 v16, v159, v157, s[6:7]
	v_cmp_gt_i32_e64 s[6:7], 0, v8
	v_and_b32_e32 v18, 0xffffff80, v8
	v_or_b32_e32 v8, v16, v9
	v_cndmask_b32_e64 v17, v162, v160, s[6:7]
	v_cmp_gt_i32_e64 s[6:7], 0, v11
	v_or_b32_e32 v9, v17, v18
	v_and_b32_e32 v11, 0xffffff80, v11
	v_cndmask_b32_e64 v16, v163, v161, s[6:7]
	v_cmp_gt_i32_e64 s[6:7], 0, v10
	v_and_b32_e32 v18, 0xffffff80, v10
	v_or_b32_e32 v10, v16, v11
	v_cndmask_b32_e64 v17, v166, v164, s[6:7]
	v_cmp_gt_i32_e64 s[6:7], 0, v13
	v_or_b32_e32 v11, v17, v18
	v_and_b32_e32 v13, 0xffffff80, v13
	v_cndmask_b32_e64 v16, v167, v165, s[6:7]
	v_cmp_gt_i32_e64 s[6:7], 0, v12
	v_and_b32_e32 v18, 0xffffff80, v12
	v_or_b32_e32 v12, v16, v13
	v_cndmask_b32_e64 v17, v170, v168, s[6:7]
	v_cmp_gt_i32_e64 s[6:7], 0, v15
	v_or_b32_e32 v16, v17, v18
	v_and_b32_e32 v15, 0xffffff80, v15
	v_cndmask_b32_e64 v13, v171, v169, s[6:7]
	v_cmp_gt_i32_e64 s[6:7], 0, v14
	v_and_b32_e32 v14, 0xffffff80, v14
	v_or_b32_e32 v25, v13, v15
	v_cndmask_b32_e64 v17, v174, v172, s[6:7]
	v_or_b32_e32 v28, v17, v14
	v_max_f32_e32 v13, v211, v210
	v_min_f32_e32 v14, v211, v210
	v_min_f32_e32 v15, v212, v173
	v_max_f32_e32 v17, v212, v173
	v_max_f32_e32 v18, v214, v213
	v_min_f32_e32 v19, v214, v213
	v_min_f32_e32 v20, v216, v215
	v_max_f32_e32 v21, v216, v215
	v_max_f32_e32 v22, v218, v217
	v_min_f32_e32 v23, v218, v217
	v_min_f32_e32 v24, v220, v219
	v_max_f32_e32 v26, v220, v219
	v_max_f32_e32 v27, v222, v221
	v_min_f32_e32 v29, v222, v221
	v_min_f32_e32 v30, v224, v223
	v_max_f32_e32 v31, v224, v223
	v_max_f32_e32 v32, v13, v15
	v_min_f32_e32 v13, v13, v15
	v_max_f32_e32 v15, v14, v17
	v_min_f32_e32 v14, v14, v17
	v_min_f32_e32 v17, v18, v20
	v_max_f32_e32 v18, v18, v20
	v_min_f32_e32 v20, v19, v21
	v_max_f32_e32 v19, v19, v21
	v_max_f32_e32 v21, v22, v24
	v_min_f32_e32 v22, v22, v24
	v_max_f32_e32 v24, v23, v26
	v_min_f32_e32 v23, v23, v26
	v_min_f32_e32 v26, v27, v30
	v_max_f32_e32 v27, v27, v30
	v_min_f32_e32 v30, v29, v31
	v_max_f32_e32 v29, v29, v31
	v_max_f32_e32 v31, v32, v15
	v_min_f32_e32 v15, v32, v15
	v_max_f32_e32 v32, v13, v14
	v_min_f32_e32 v13, v13, v14
	v_min_f32_e32 v14, v17, v20
	v_max_f32_e32 v17, v17, v20
	v_min_f32_e32 v20, v18, v19
	v_max_f32_e32 v18, v18, v19
	v_max_f32_e32 v19, v21, v24
	v_min_f32_e32 v21, v21, v24
	v_max_f32_e32 v24, v22, v23
	v_min_f32_e32 v22, v22, v23
	v_min_f32_e32 v23, v26, v30
	v_max_f32_e32 v26, v26, v30
	v_min_f32_e32 v30, v27, v29
	v_max_f32_e32 v27, v27, v29
	v_max_f32_e32 v29, v31, v14
	v_min_f32_e32 v14, v31, v14
	v_max_f32_e32 v31, v15, v17
	v_min_f32_e32 v15, v15, v17
	v_max_f32_e32 v17, v32, v20
	v_min_f32_e32 v20, v32, v20
	v_max_f32_e32 v32, v13, v18
	v_min_f32_e32 v13, v13, v18
	v_min_f32_e32 v18, v19, v23
	v_max_f32_e32 v19, v19, v23
	v_min_f32_e32 v23, v21, v26
	v_max_f32_e32 v21, v21, v26
	v_min_f32_e32 v26, v24, v30
	v_max_f32_e32 v24, v24, v30
	v_min_f32_e32 v30, v22, v27
	v_max_f32_e32 v22, v22, v27
	v_max_f32_e32 v27, v29, v17
	v_min_f32_e32 v17, v29, v17
	v_max_f32_e32 v29, v31, v32
	v_min_f32_e32 v31, v31, v32
	v_max_f32_e32 v32, v14, v20
	v_min_f32_e32 v14, v14, v20
	v_max_f32_e32 v20, v15, v13
	v_min_f32_e32 v13, v15, v13
	v_min_f32_e32 v15, v18, v26
	v_max_f32_e32 v18, v18, v26
	v_min_f32_e32 v26, v23, v30
	v_max_f32_e32 v23, v23, v30
	v_min_f32_e32 v30, v19, v24
	v_max_f32_e32 v19, v19, v24
	v_min_f32_e32 v24, v21, v22
	v_max_f32_e32 v21, v21, v22
	v_max_f32_e32 v22, v27, v29
	v_min_f32_e32 v27, v27, v29
	v_max_f32_e32 v29, v17, v31
	v_min_f32_e32 v17, v17, v31
	v_max_f32_e32 v31, v32, v20
	v_min_f32_e32 v20, v32, v20
	v_max_f32_e32 v32, v14, v13
	v_min_f32_e32 v13, v14, v13
	v_min_f32_e32 v14, v15, v26
	v_max_f32_e32 v15, v15, v26
	v_min_f32_e32 v26, v18, v23
	v_max_f32_e32 v18, v18, v23
	v_min_f32_e32 v23, v30, v24
	v_max_f32_e32 v24, v30, v24
	v_min_f32_e32 v30, v19, v21
	v_max_f32_e32 v19, v19, v21
	v_max_f32_e32 v21, v22, v14
	v_min_f32_e32 v14, v22, v14
	v_max_f32_e32 v22, v27, v15
	v_min_f32_e32 v15, v27, v15
	v_max_f32_e32 v27, v29, v26
	v_min_f32_e32 v26, v29, v26
	v_max_f32_e32 v29, v17, v18
	v_min_f32_e32 v17, v17, v18
	v_max_f32_e32 v18, v31, v23
	v_min_f32_e32 v23, v31, v23
	v_max_f32_e32 v31, v20, v24
	v_min_f32_e32 v20, v20, v24
	v_max_f32_e32 v24, v32, v30
	v_min_f32_e32 v30, v32, v30
	v_max_f32_e32 v32, v13, v19
	v_min_f32_e32 v13, v13, v19
	v_max_f32_e32 v19, v21, v18
	v_min_f32_e32 v18, v21, v18
	v_max_f32_e32 v21, v22, v31
	v_min_f32_e32 v22, v22, v31
	v_max_f32_e32 v31, v27, v24
	v_min_f32_e32 v24, v27, v24
	v_max_f32_e32 v27, v29, v32
	v_min_f32_e32 v29, v29, v32
	v_max_f32_e32 v32, v14, v23
	v_min_f32_e32 v14, v14, v23
	v_max_f32_e32 v23, v15, v20
	v_min_f32_e32 v15, v15, v20
	v_max_f32_e32 v20, v26, v30
	v_min_f32_e32 v26, v26, v30
	v_max_f32_e32 v30, v17, v13
	v_min_f32_e32 v13, v17, v13
	v_max_f32_e32 v17, v19, v31
	v_min_f32_e32 v19, v19, v31
	v_max_f32_e32 v33, v21, v27
	v_min_f32_e32 v21, v21, v27
	v_max_f32_e32 v34, v18, v24
	v_min_f32_e32 v18, v18, v24
	v_max_f32_e32 v24, v22, v29
	v_min_f32_e32 v22, v22, v29
	v_max_f32_e32 v35, v32, v20
	v_min_f32_e32 v32, v32, v20
	v_max_f32_e32 v20, v23, v30
	v_min_f32_e32 v36, v23, v30
	v_max_f32_e32 v37, v14, v26
	v_min_f32_e32 v38, v14, v26
	v_max_f32_e32 v14, v15, v13
	v_min_f32_e32 v13, v15, v13
	v_max_f32_e32 v31, v17, v33
	v_min_f32_e32 v29, v17, v33
	v_max_f32_e32 v30, v19, v21
	v_min_f32_e32 v26, v19, v21
	v_max_f32_e32 v27, v34, v24
	v_min_f32_e32 v23, v34, v24
	v_max_f32_e32 v24, v18, v22
	v_min_f32_e32 v21, v18, v22
	v_max_f32_e32 v22, v35, v20
	v_min_f32_e32 v19, v35, v20
	v_max_f32_e32 v20, v32, v36
	v_min_f32_e32 v17, v32, v36
	v_max_f32_e32 v18, v37, v14
	v_min_f32_e32 v14, v37, v14
	v_max_f32_e32 v15, v38, v13
	v_min_f32_e32 v13, v38, v13
	v_max_f32_e32 v32, v226, v225
	v_min_f32_e32 v33, v226, v225
	v_min_f32_e32 v34, v228, v227
	v_max_f32_e32 v35, v228, v227
	v_max_f32_e32 v36, v230, v229
	v_min_f32_e32 v37, v230, v229
	v_min_f32_e32 v38, v232, v231
	v_max_f32_e32 v39, v232, v231
	v_max_f32_e32 v40, v234, v233
	v_min_f32_e32 v41, v234, v233
	v_min_f32_e32 v42, v236, v235
	v_max_f32_e32 v43, v236, v235
	v_max_f32_e32 v44, v238, v237
	v_min_f32_e32 v45, v238, v237
	v_min_f32_e32 v46, v240, v239
	v_max_f32_e32 v47, v240, v239
	v_max_f32_e32 v48, v32, v34
	v_min_f32_e32 v32, v32, v34
	v_max_f32_e32 v34, v33, v35
	v_min_f32_e32 v33, v33, v35
	v_min_f32_e32 v35, v36, v38
	v_max_f32_e32 v36, v36, v38
	v_min_f32_e32 v38, v37, v39
	v_max_f32_e32 v37, v37, v39
	v_max_f32_e32 v39, v40, v42
	v_min_f32_e32 v40, v40, v42
	v_max_f32_e32 v42, v41, v43
	v_min_f32_e32 v41, v41, v43
	v_min_f32_e32 v43, v44, v46
	v_max_f32_e32 v44, v44, v46
	v_min_f32_e32 v46, v45, v47
	v_max_f32_e32 v45, v45, v47
	v_max_f32_e32 v47, v48, v34
	v_min_f32_e32 v34, v48, v34
	v_max_f32_e32 v48, v32, v33
	v_min_f32_e32 v32, v32, v33
	v_min_f32_e32 v33, v35, v38
	v_max_f32_e32 v35, v35, v38
	v_min_f32_e32 v38, v36, v37
	v_max_f32_e32 v36, v36, v37
	v_max_f32_e32 v37, v39, v42
	v_min_f32_e32 v39, v39, v42
	v_max_f32_e32 v42, v40, v41
	v_min_f32_e32 v40, v40, v41
	v_min_f32_e32 v41, v43, v46
	v_max_f32_e32 v43, v43, v46
	v_min_f32_e32 v46, v44, v45
	v_max_f32_e32 v44, v44, v45
	v_max_f32_e32 v45, v47, v33
	v_min_f32_e32 v33, v47, v33
	v_max_f32_e32 v47, v34, v35
	v_min_f32_e32 v34, v34, v35
	v_max_f32_e32 v35, v48, v38
	v_min_f32_e32 v38, v48, v38
	v_max_f32_e32 v48, v32, v36
	v_min_f32_e32 v32, v32, v36
	v_min_f32_e32 v36, v37, v41
	v_max_f32_e32 v37, v37, v41
	v_min_f32_e32 v41, v39, v43
	v_max_f32_e32 v39, v39, v43
	v_min_f32_e32 v43, v42, v46
	v_max_f32_e32 v42, v42, v46
	v_min_f32_e32 v46, v40, v44
	v_max_f32_e32 v40, v40, v44
	v_max_f32_e32 v44, v45, v35
	v_min_f32_e32 v35, v45, v35
	v_max_f32_e32 v45, v47, v48
	v_min_f32_e32 v47, v47, v48
	v_max_f32_e32 v48, v33, v38
	v_min_f32_e32 v33, v33, v38
	v_max_f32_e32 v38, v34, v32
	v_min_f32_e32 v32, v34, v32
	v_min_f32_e32 v34, v36, v43
	v_max_f32_e32 v36, v36, v43
	v_min_f32_e32 v43, v41, v46
	v_max_f32_e32 v41, v41, v46
	v_min_f32_e32 v46, v37, v42
	v_max_f32_e32 v37, v37, v42
	v_min_f32_e32 v42, v39, v40
	v_max_f32_e32 v39, v39, v40
	v_max_f32_e32 v40, v44, v45
	v_min_f32_e32 v44, v44, v45
	v_max_f32_e32 v45, v35, v47
	v_min_f32_e32 v35, v35, v47
	v_max_f32_e32 v47, v48, v38
	v_min_f32_e32 v38, v48, v38
	v_max_f32_e32 v48, v33, v32
	v_min_f32_e32 v32, v33, v32
	v_min_f32_e32 v33, v34, v43
	v_max_f32_e32 v34, v34, v43
	v_min_f32_e32 v43, v36, v41
	v_max_f32_e32 v36, v36, v41
	v_min_f32_e32 v41, v46, v42
	v_max_f32_e32 v42, v46, v42
	v_min_f32_e32 v46, v37, v39
	v_max_f32_e32 v37, v37, v39
	v_max_f32_e32 v39, v40, v33
	v_min_f32_e32 v33, v40, v33
	v_max_f32_e32 v40, v44, v34
	v_min_f32_e32 v34, v44, v34
	v_max_f32_e32 v44, v45, v43
	v_min_f32_e32 v43, v45, v43
	v_max_f32_e32 v45, v35, v36
	v_min_f32_e32 v35, v35, v36
	v_max_f32_e32 v36, v47, v41
	v_min_f32_e32 v41, v47, v41
	v_max_f32_e32 v47, v38, v42
	v_min_f32_e32 v38, v38, v42
	v_max_f32_e32 v42, v48, v46
	v_min_f32_e32 v46, v48, v46
	v_max_f32_e32 v48, v32, v37
	v_min_f32_e32 v32, v32, v37
	v_max_f32_e32 v37, v39, v36
	v_min_f32_e32 v36, v39, v36
	v_max_f32_e32 v39, v40, v47
	v_min_f32_e32 v40, v40, v47
	v_max_f32_e32 v47, v44, v42
	v_min_f32_e32 v42, v44, v42
	v_max_f32_e32 v44, v45, v48
	v_min_f32_e32 v45, v45, v48
	v_max_f32_e32 v48, v33, v41
	v_min_f32_e32 v33, v33, v41
	v_max_f32_e32 v41, v34, v38
	v_min_f32_e32 v34, v34, v38
	v_max_f32_e32 v38, v43, v46
	v_min_f32_e32 v43, v43, v46
	v_max_f32_e32 v46, v35, v32
	v_min_f32_e32 v32, v35, v32
	v_max_f32_e32 v35, v37, v47
	v_min_f32_e32 v37, v37, v47
	v_max_f32_e32 v47, v39, v44
	v_min_f32_e32 v39, v39, v44
	v_max_f32_e32 v44, v36, v42
	v_min_f32_e32 v42, v36, v42
	v_max_f32_e32 v49, v40, v45
	v_min_f32_e32 v40, v40, v45
	v_max_f32_e32 v45, v48, v38
	v_min_f32_e32 v48, v48, v38
	v_max_f32_e32 v50, v41, v46
	v_min_f32_e32 v41, v41, v46
	v_max_f32_e32 v46, v33, v43
	v_min_f32_e32 v43, v33, v43
	v_max_f32_e32 v51, v34, v32
	v_min_f32_e32 v52, v34, v32
	v_max_f32_e32 v32, v35, v47
	v_min_f32_e32 v33, v35, v47
	v_max_f32_e32 v34, v37, v39
	v_min_f32_e32 v35, v37, v39
	v_max_f32_e32 v36, v44, v49
	v_min_f32_e32 v37, v44, v49
	v_max_f32_e32 v38, v42, v40
	v_min_f32_e32 v39, v42, v40
	v_max_f32_e32 v40, v45, v50
	v_min_f32_e32 v42, v45, v50
	v_max_f32_e32 v44, v48, v41
	v_min_f32_e32 v41, v48, v41
	v_max_f32_e32 v45, v46, v51
	v_min_f32_e32 v46, v46, v51
	v_max_f32_e32 v47, v43, v52
	v_min_f32_e32 v43, v43, v52
	v_max_f32_e32 v48, v183, v182
	v_min_f32_e32 v49, v183, v182
	v_min_f32_e32 v50, v242, v241
	v_max_f32_e32 v51, v242, v241
	v_max_f32_e32 v52, v244, v243
	v_min_f32_e32 v53, v244, v243
	v_min_f32_e32 v54, v246, v245
	v_max_f32_e32 v55, v246, v245
	v_max_f32_e32 v56, v248, v247
	v_min_f32_e32 v57, v248, v247
	v_min_f32_e32 v58, v250, v249
	v_max_f32_e32 v59, v250, v249
	v_max_f32_e32 v60, v252, v251
	v_min_f32_e32 v61, v252, v251
	v_min_f32_e32 v62, v195, v190
	v_max_f32_e32 v63, v195, v190
	v_max_f32_e32 v173, v48, v50
	v_min_f32_e32 v48, v48, v50
	v_max_f32_e32 v50, v49, v51
	v_min_f32_e32 v49, v49, v51
	v_min_f32_e32 v51, v52, v54
	v_max_f32_e32 v52, v52, v54
	v_min_f32_e32 v54, v53, v55
	v_max_f32_e32 v53, v53, v55
	v_max_f32_e32 v55, v56, v58
	v_min_f32_e32 v56, v56, v58
	v_max_f32_e32 v58, v57, v59
	v_min_f32_e32 v57, v57, v59
	v_min_f32_e32 v59, v60, v62
	v_max_f32_e32 v60, v60, v62
	v_min_f32_e32 v62, v61, v63
	v_max_f32_e32 v61, v61, v63
	v_max_f32_e32 v63, v173, v50
	v_min_f32_e32 v50, v173, v50
	v_max_f32_e32 v173, v48, v49
	v_min_f32_e32 v48, v48, v49
	v_min_f32_e32 v49, v51, v54
	v_max_f32_e32 v51, v51, v54
	v_min_f32_e32 v54, v52, v53
	v_max_f32_e32 v52, v52, v53
	v_max_f32_e32 v53, v55, v58
	v_min_f32_e32 v55, v55, v58
	v_max_f32_e32 v58, v56, v57
	v_min_f32_e32 v56, v56, v57
	v_min_f32_e32 v57, v59, v62
	v_max_f32_e32 v59, v59, v62
	v_min_f32_e32 v62, v60, v61
	v_max_f32_e32 v60, v60, v61
	v_max_f32_e32 v61, v63, v49
	v_min_f32_e32 v49, v63, v49
	v_max_f32_e32 v63, v50, v51
	v_min_f32_e32 v50, v50, v51
	v_max_f32_e32 v51, v173, v54
	v_min_f32_e32 v54, v173, v54
	v_max_f32_e32 v173, v48, v52
	v_min_f32_e32 v48, v48, v52
	v_min_f32_e32 v52, v53, v57
	v_max_f32_e32 v53, v53, v57
	v_min_f32_e32 v57, v55, v59
	v_max_f32_e32 v55, v55, v59
	v_min_f32_e32 v59, v58, v62
	v_max_f32_e32 v58, v58, v62
	v_min_f32_e32 v62, v56, v60
	v_max_f32_e32 v56, v56, v60
	v_max_f32_e32 v60, v61, v51
	v_min_f32_e32 v51, v61, v51
	v_max_f32_e32 v61, v63, v173
	v_min_f32_e32 v63, v63, v173
	v_max_f32_e32 v173, v49, v54
	v_min_f32_e32 v49, v49, v54
	v_max_f32_e32 v54, v50, v48
	v_min_f32_e32 v48, v50, v48
	v_min_f32_e32 v50, v52, v59
	v_max_f32_e32 v52, v52, v59
	v_min_f32_e32 v59, v57, v62
	v_max_f32_e32 v57, v57, v62
	v_min_f32_e32 v62, v53, v58
	v_max_f32_e32 v53, v53, v58
	v_min_f32_e32 v58, v55, v56
	v_max_f32_e32 v55, v55, v56
	v_max_f32_e32 v56, v60, v61
	v_min_f32_e32 v60, v60, v61
	v_max_f32_e32 v61, v51, v63
	v_min_f32_e32 v51, v51, v63
	v_max_f32_e32 v63, v173, v54
	v_min_f32_e32 v54, v173, v54
	v_max_f32_e32 v173, v49, v48
	v_min_f32_e32 v48, v49, v48
	v_min_f32_e32 v49, v50, v59
	v_max_f32_e32 v50, v50, v59
	v_min_f32_e32 v59, v52, v57
	v_max_f32_e32 v52, v52, v57
	v_min_f32_e32 v57, v62, v58
	v_max_f32_e32 v58, v62, v58
	v_min_f32_e32 v62, v53, v55
	v_max_f32_e32 v53, v53, v55
	v_max_f32_e32 v55, v56, v49
	v_min_f32_e32 v49, v56, v49
	v_max_f32_e32 v56, v60, v50
	v_min_f32_e32 v50, v60, v50
	v_max_f32_e32 v60, v61, v59
	v_min_f32_e32 v59, v61, v59
	v_max_f32_e32 v61, v51, v52
	v_min_f32_e32 v51, v51, v52
	v_max_f32_e32 v52, v63, v57
	v_min_f32_e32 v57, v63, v57
	v_max_f32_e32 v63, v54, v58
	v_min_f32_e32 v54, v54, v58
	v_max_f32_e32 v58, v173, v62
	v_min_f32_e32 v62, v173, v62
	v_max_f32_e32 v173, v48, v53
	v_min_f32_e32 v48, v48, v53
	v_max_f32_e32 v53, v55, v52
	v_min_f32_e32 v52, v55, v52
	v_max_f32_e32 v55, v56, v63
	v_min_f32_e32 v56, v56, v63
	v_max_f32_e32 v63, v60, v58
	v_min_f32_e32 v58, v60, v58
	v_max_f32_e32 v60, v61, v173
	v_min_f32_e32 v61, v61, v173
	v_max_f32_e32 v173, v49, v57
	v_min_f32_e32 v49, v49, v57
	v_max_f32_e32 v57, v50, v54
	v_min_f32_e32 v50, v50, v54
	v_max_f32_e32 v54, v59, v62
	v_min_f32_e32 v59, v59, v62
	v_max_f32_e32 v62, v51, v48
	v_min_f32_e32 v48, v51, v48
	v_max_f32_e32 v51, v53, v63
	v_min_f32_e32 v53, v53, v63
	v_max_f32_e32 v63, v55, v60
	v_min_f32_e32 v55, v55, v60
	v_max_f32_e32 v60, v52, v58
	v_min_f32_e32 v52, v52, v58
	v_max_f32_e32 v58, v56, v61
	v_min_f32_e32 v56, v56, v61
	v_max_f32_e32 v61, v173, v54
	v_min_f32_e32 v54, v173, v54
	v_max_f32_e32 v173, v57, v62
	v_min_f32_e32 v57, v57, v62
	v_max_f32_e32 v62, v49, v59
	v_min_f32_e32 v49, v49, v59
	v_max_f32_e32 v59, v50, v48
	v_min_f32_e32 v48, v50, v48
	v_max_f32_e32 v50, v51, v63
	v_min_f32_e32 v51, v51, v63
	v_max_f32_e32 v63, v53, v55
	v_min_f32_e32 v53, v53, v55
	v_max_f32_e32 v55, v60, v58
	v_min_f32_e32 v58, v60, v58
	v_max_f32_e32 v60, v52, v56
	v_min_f32_e32 v52, v52, v56
	v_max_f32_e32 v56, v61, v173
	v_min_f32_e32 v61, v61, v173
	v_max_f32_e32 v173, v54, v57
	v_min_f32_e32 v54, v54, v57
	v_max_f32_e32 v57, v62, v59
	v_min_f32_e32 v59, v62, v59
	v_max_f32_e32 v62, v49, v48
	v_min_f32_e32 v48, v49, v48
	v_max_f32_e32 v49, v1, v0
	v_min_f32_e32 v0, v1, v0
	v_min_f32_e32 v1, v3, v2
	v_max_f32_e32 v2, v3, v2
	v_max_f32_e32 v3, v5, v4
	v_min_f32_e32 v4, v5, v4
	v_min_f32_e32 v5, v7, v6
	v_max_f32_e32 v6, v7, v6
	v_max_f32_e32 v7, v9, v8
	v_min_f32_e32 v8, v9, v8
	v_min_f32_e32 v9, v11, v10
	v_max_f32_e32 v10, v11, v10
	v_max_f32_e32 v11, v16, v12
	v_min_f32_e32 v12, v16, v12
	v_min_f32_e32 v16, v28, v25
	v_max_f32_e32 v25, v28, v25
	v_max_f32_e32 v28, v49, v1
	v_min_f32_e32 v1, v49, v1
	v_max_f32_e32 v49, v0, v2
	v_min_f32_e32 v0, v0, v2
	v_min_f32_e32 v2, v3, v5
	v_max_f32_e32 v3, v3, v5
	v_min_f32_e32 v5, v4, v6
	v_max_f32_e32 v4, v4, v6
	v_max_f32_e32 v6, v7, v9
	v_min_f32_e32 v7, v7, v9
	v_max_f32_e32 v9, v8, v10
	v_min_f32_e32 v8, v8, v10
	v_min_f32_e32 v10, v11, v16
	v_max_f32_e32 v11, v11, v16
	v_min_f32_e32 v16, v12, v25
	v_max_f32_e32 v12, v12, v25
	v_max_f32_e32 v25, v28, v49
	v_min_f32_e32 v28, v28, v49
	v_max_f32_e32 v49, v1, v0
	v_min_f32_e32 v0, v1, v0
	v_min_f32_e32 v1, v2, v5
	v_max_f32_e32 v2, v2, v5
	v_min_f32_e32 v5, v3, v4
	v_max_f32_e32 v3, v3, v4
	v_max_f32_e32 v4, v6, v9
	v_min_f32_e32 v6, v6, v9
	v_max_f32_e32 v9, v7, v8
	v_min_f32_e32 v7, v7, v8
	v_min_f32_e32 v8, v10, v16
	v_max_f32_e32 v10, v10, v16
	v_min_f32_e32 v16, v11, v12
	v_max_f32_e32 v11, v11, v12
	v_max_f32_e32 v12, v25, v1
	v_min_f32_e32 v1, v25, v1
	v_max_f32_e32 v25, v28, v2
	v_min_f32_e32 v2, v28, v2
	v_max_f32_e32 v28, v49, v5
	v_min_f32_e32 v5, v49, v5
	v_max_f32_e32 v49, v0, v3
	v_min_f32_e32 v0, v0, v3
	v_min_f32_e32 v3, v4, v8
	v_max_f32_e32 v4, v4, v8
	v_min_f32_e32 v8, v6, v10
	v_max_f32_e32 v6, v6, v10
	v_min_f32_e32 v10, v9, v16
	v_max_f32_e32 v9, v9, v16
	v_min_f32_e32 v16, v7, v11
	v_max_f32_e32 v7, v7, v11
	v_max_f32_e32 v11, v12, v28
	v_min_f32_e32 v12, v12, v28
	v_max_f32_e32 v28, v25, v49
	v_min_f32_e32 v25, v25, v49
	v_max_f32_e32 v49, v1, v5
	v_min_f32_e32 v1, v1, v5
	v_max_f32_e32 v5, v2, v0
	v_min_f32_e32 v0, v2, v0
	v_min_f32_e32 v2, v3, v10
	v_max_f32_e32 v3, v3, v10
	v_min_f32_e32 v10, v8, v16
	v_max_f32_e32 v8, v8, v16
	v_min_f32_e32 v16, v4, v9
	v_max_f32_e32 v4, v4, v9
	v_min_f32_e32 v9, v6, v7
	v_max_f32_e32 v6, v6, v7
	v_max_f32_e32 v7, v11, v28
	v_min_f32_e32 v11, v11, v28
	v_max_f32_e32 v28, v12, v25
	v_min_f32_e32 v12, v12, v25
	v_max_f32_e32 v25, v49, v5
	v_min_f32_e32 v5, v49, v5
	v_max_f32_e32 v49, v1, v0
	v_min_f32_e32 v0, v1, v0
	v_min_f32_e32 v1, v2, v10
	v_max_f32_e32 v2, v2, v10
	v_min_f32_e32 v10, v3, v8
	v_max_f32_e32 v3, v3, v8
	v_min_f32_e32 v8, v16, v9
	v_max_f32_e32 v9, v16, v9
	v_min_f32_e32 v16, v4, v6
	v_max_f32_e32 v4, v4, v6
	v_max_f32_e32 v6, v7, v1
	v_min_f32_e32 v1, v7, v1
	v_max_f32_e32 v7, v11, v2
	v_min_f32_e32 v2, v11, v2
	v_max_f32_e32 v11, v28, v10
	v_min_f32_e32 v10, v28, v10
	v_max_f32_e32 v28, v12, v3
	v_min_f32_e32 v3, v12, v3
	v_max_f32_e32 v12, v25, v8
	v_min_f32_e32 v8, v25, v8
	v_max_f32_e32 v25, v5, v9
	v_min_f32_e32 v5, v5, v9
	v_max_f32_e32 v9, v49, v16
	v_min_f32_e32 v16, v49, v16
	v_max_f32_e32 v49, v0, v4
	v_min_f32_e32 v0, v0, v4
	v_max_f32_e32 v4, v6, v12
	v_min_f32_e32 v6, v6, v12
	v_max_f32_e32 v12, v7, v25
	v_min_f32_e32 v7, v7, v25
	v_max_f32_e32 v25, v11, v9
	v_min_f32_e32 v9, v11, v9
	v_max_f32_e32 v11, v28, v49
	v_min_f32_e32 v28, v28, v49
	v_max_f32_e32 v49, v1, v8
	v_min_f32_e32 v1, v1, v8
	v_max_f32_e32 v8, v2, v5
	v_min_f32_e32 v2, v2, v5
	v_max_f32_e32 v5, v10, v16
	v_min_f32_e32 v10, v10, v16
	v_max_f32_e32 v16, v3, v0
	v_min_f32_e32 v0, v3, v0
	v_max_f32_e32 v3, v4, v25
	v_min_f32_e32 v4, v4, v25
	v_max_f32_e32 v25, v12, v11
	v_min_f32_e32 v11, v12, v11
	v_max_f32_e32 v12, v6, v9
	v_min_f32_e32 v6, v6, v9
	v_max_f32_e32 v9, v7, v28
	v_min_f32_e32 v7, v7, v28
	v_max_f32_e32 v28, v49, v5
	v_min_f32_e32 v5, v49, v5
	v_max_f32_e32 v49, v8, v16
	v_min_f32_e32 v8, v8, v16
	v_max_f32_e32 v16, v1, v10
	v_min_f32_e32 v1, v1, v10
	v_max_f32_e32 v10, v2, v0
	v_min_f32_e32 v0, v2, v0
	v_max_f32_e32 v2, v3, v25
	v_min_f32_e32 v3, v3, v25
	v_max_f32_e32 v25, v4, v11
	v_min_f32_e32 v4, v4, v11
	v_max_f32_e32 v11, v12, v9
	v_min_f32_e32 v9, v12, v9
	v_max_f32_e32 v12, v6, v7
	v_min_f32_e32 v6, v6, v7
	v_max_f32_e32 v7, v28, v49
	v_min_f32_e32 v28, v28, v49
	v_max_f32_e32 v49, v5, v8
	v_min_f32_e32 v5, v5, v8
	v_max_f32_e32 v8, v16, v10
	v_min_f32_e32 v10, v16, v10
	v_max_f32_e32 v16, v1, v0
	v_min_f32_e32 v0, v1, v0
	v_max_f32_e32 v1, v31, v43
	v_max_f32_e32 v29, v29, v47
	v_max_f32_e32 v30, v30, v46
	v_max_f32_e32 v26, v26, v45
	v_max_f32_e32 v27, v27, v41
	v_max_f32_e32 v23, v23, v44
	v_max_f32_e32 v24, v24, v42
	v_max_f32_e32 v21, v21, v40
	v_max_f32_e32 v22, v22, v39
	v_max_f32_e32 v19, v19, v38
	v_max_f32_e32 v20, v20, v37
	v_max_f32_e32 v17, v17, v36
	v_max_f32_e32 v18, v18, v35
	v_max_f32_e32 v14, v14, v34
	v_max_f32_e32 v15, v15, v33
	v_max_f32_e32 v13, v13, v32
	v_max_f32_e32 v31, v1, v22
	v_min_f32_e32 v1, v1, v22
	v_max_f32_e32 v22, v29, v19
	v_min_f32_e32 v19, v29, v19
	v_max_f32_e32 v29, v30, v20
	v_min_f32_e32 v20, v30, v20
	v_max_f32_e32 v30, v26, v17
	v_min_f32_e32 v17, v26, v17
	v_max_f32_e32 v26, v27, v18
	v_min_f32_e32 v18, v27, v18
	v_max_f32_e32 v27, v23, v14
	v_min_f32_e32 v14, v23, v14
	v_max_f32_e32 v23, v24, v15
	v_min_f32_e32 v15, v24, v15
	v_max_f32_e32 v24, v21, v13
	v_min_f32_e32 v13, v21, v13
	v_max_f32_e32 v21, v31, v26
	v_min_f32_e32 v26, v31, v26
	v_max_f32_e32 v31, v22, v27
	v_min_f32_e32 v22, v22, v27
	v_max_f32_e32 v27, v29, v23
	v_min_f32_e32 v23, v29, v23
	v_max_f32_e32 v29, v30, v24
	v_min_f32_e32 v24, v30, v24
	v_max_f32_e32 v30, v1, v18
	v_min_f32_e32 v1, v1, v18
	v_max_f32_e32 v18, v19, v14
	v_min_f32_e32 v14, v19, v14
	v_max_f32_e32 v19, v20, v15
	v_min_f32_e32 v15, v20, v15
	v_max_f32_e32 v20, v17, v13
	v_min_f32_e32 v13, v17, v13
	v_max_f32_e32 v17, v21, v27
	v_min_f32_e32 v21, v21, v27
	v_max_f32_e32 v27, v31, v29
	v_min_f32_e32 v29, v31, v29
	v_max_f32_e32 v31, v26, v23
	v_min_f32_e32 v23, v26, v23
	v_max_f32_e32 v26, v22, v24
	v_min_f32_e32 v22, v22, v24
	v_max_f32_e32 v24, v30, v19
	v_min_f32_e32 v19, v30, v19
	v_max_f32_e32 v30, v18, v20
	v_min_f32_e32 v18, v18, v20
	v_max_f32_e32 v20, v1, v15
	v_min_f32_e32 v1, v1, v15
	v_max_f32_e32 v15, v14, v13
	v_min_f32_e32 v13, v14, v13
	v_max_f32_e32 v14, v17, v27
	v_min_f32_e32 v17, v17, v27
	v_max_f32_e32 v27, v21, v29
	v_min_f32_e32 v21, v21, v29
	v_max_f32_e32 v29, v31, v26
	v_min_f32_e32 v26, v31, v26
	v_max_f32_e32 v31, v23, v22
	v_min_f32_e32 v22, v23, v22
	v_max_f32_e32 v23, v24, v30
	v_min_f32_e32 v24, v24, v30
	v_max_f32_e32 v30, v19, v18
	v_min_f32_e32 v18, v19, v18
	v_max_f32_e32 v19, v20, v15
	v_min_f32_e32 v15, v20, v15
	v_max_f32_e32 v20, v1, v13
	v_min_f32_e32 v1, v1, v13
	v_max_f32_e32 v0, v50, v0
	v_max_f32_e32 v13, v51, v16
	v_max_f32_e32 v10, v63, v10
	v_max_f32_e32 v8, v53, v8
	v_max_f32_e32 v5, v55, v5
	v_max_f32_e32 v16, v58, v49
	v_max_f32_e32 v28, v60, v28
	v_max_f32_e32 v7, v52, v7
	v_max_f32_e32 v6, v56, v6
	v_max_f32_e32 v12, v61, v12
	v_max_f32_e32 v9, v173, v9
	v_max_f32_e32 v11, v54, v11
	v_max_f32_e32 v4, v57, v4
	v_max_f32_e32 v25, v59, v25
	v_max_f32_e32 v3, v62, v3
	v_max_f32_e32 v2, v48, v2
	v_max_f32_e32 v32, v0, v6
	v_min_f32_e32 v0, v0, v6
	v_max_f32_e32 v6, v13, v12
	v_min_f32_e32 v12, v13, v12
	v_max_f32_e32 v13, v10, v9
	v_min_f32_e32 v9, v10, v9
	v_max_f32_e32 v10, v8, v11
	v_min_f32_e32 v8, v8, v11
	v_max_f32_e32 v11, v5, v4
	v_min_f32_e32 v4, v5, v4
	v_max_f32_e32 v5, v16, v25
	v_min_f32_e32 v16, v16, v25
	v_max_f32_e32 v25, v28, v3
	v_min_f32_e32 v3, v28, v3
	v_max_f32_e32 v28, v7, v2
	v_min_f32_e32 v2, v7, v2
	v_max_f32_e32 v7, v32, v11
	v_min_f32_e32 v11, v32, v11
	v_max_f32_e32 v32, v6, v5
	v_min_f32_e32 v5, v6, v5
	v_max_f32_e32 v6, v13, v25
	v_min_f32_e32 v13, v13, v25
	v_max_f32_e32 v25, v10, v28
	v_min_f32_e32 v10, v10, v28
	v_max_f32_e32 v28, v0, v4
	v_min_f32_e32 v0, v0, v4
	v_max_f32_e32 v4, v12, v16
	v_min_f32_e32 v12, v12, v16
	v_max_f32_e32 v16, v9, v3
	v_min_f32_e32 v3, v9, v3
	v_max_f32_e32 v9, v8, v2
	v_min_f32_e32 v2, v8, v2
	v_max_f32_e32 v8, v7, v6
	v_min_f32_e32 v6, v7, v6
	v_max_f32_e32 v7, v32, v25
	v_min_f32_e32 v25, v32, v25
	v_max_f32_e32 v32, v11, v13
	v_min_f32_e32 v11, v11, v13
	v_max_f32_e32 v13, v5, v10
	v_min_f32_e32 v5, v5, v10
	v_max_f32_e32 v10, v28, v16
	v_min_f32_e32 v16, v28, v16
	v_max_f32_e32 v28, v4, v9
	v_min_f32_e32 v4, v4, v9
	v_max_f32_e32 v9, v0, v3
	v_min_f32_e32 v0, v0, v3
	v_max_f32_e32 v3, v12, v2
	v_min_f32_e32 v2, v12, v2
	v_max_f32_e32 v12, v8, v7
	v_min_f32_e32 v7, v8, v7
	v_max_f32_e32 v8, v6, v25
	v_min_f32_e32 v6, v6, v25
	v_max_f32_e32 v25, v32, v13
	v_min_f32_e32 v13, v32, v13
	v_max_f32_e32 v32, v11, v5
	v_min_f32_e32 v5, v11, v5
	v_max_f32_e32 v11, v10, v28
	v_min_f32_e32 v10, v10, v28
	v_max_f32_e32 v28, v16, v4
	v_min_f32_e32 v4, v16, v4
	v_max_f32_e32 v16, v9, v3
	v_min_f32_e32 v3, v9, v3
	v_max_f32_e32 v9, v0, v2
	v_min_f32_e32 v0, v0, v2
	v_max_f32_e32 v0, v14, v0
	v_max_f32_e32 v2, v17, v9
	v_max_f32_e32 v3, v27, v3
	v_max_f32_e32 v9, v21, v16
	v_max_f32_e32 v4, v29, v4
	v_max_f32_e32 v14, v26, v28
	v_max_f32_e32 v10, v31, v10
	v_max_f32_e32 v11, v22, v11
	v_max_f32_e32 v5, v23, v5
	v_max_f32_e32 v16, v24, v32
	v_max_f32_e32 v13, v30, v13
	v_max_f32_e32 v17, v18, v25
	v_max_f32_e32 v6, v19, v6
	v_max_f32_e32 v8, v15, v8
	v_max_f32_e32 v7, v20, v7
	v_max_f32_e32 v1, v1, v12
	v_max_f32_e32 v12, v0, v5
	v_min_f32_e32 v0, v0, v5
	v_max_f32_e32 v5, v2, v16
	v_min_f32_e32 v2, v2, v16
	v_max_f32_e32 v15, v3, v13
	v_min_f32_e32 v3, v3, v13
	v_max_f32_e32 v13, v9, v17
	v_min_f32_e32 v9, v9, v17
	v_max_f32_e32 v16, v4, v6
	v_min_f32_e32 v4, v4, v6
	v_max_f32_e32 v6, v14, v8
	v_min_f32_e32 v8, v14, v8
	v_max_f32_e32 v14, v10, v7
	v_min_f32_e32 v7, v10, v7
	v_max_f32_e32 v10, v11, v1
	v_min_f32_e32 v1, v11, v1
	v_max_f32_e32 v11, v12, v16
	v_min_f32_e32 v12, v12, v16
	v_max_f32_e32 v16, v5, v6
	v_min_f32_e32 v5, v5, v6
	v_max_f32_e32 v6, v15, v14
	v_min_f32_e32 v14, v15, v14
	v_max_f32_e32 v15, v13, v10
	v_min_f32_e32 v10, v13, v10
	v_max_f32_e32 v13, v0, v4
	v_min_f32_e32 v0, v0, v4
	v_max_f32_e32 v4, v2, v8
	v_min_f32_e32 v2, v2, v8
	v_max_f32_e32 v8, v3, v7
	v_min_f32_e32 v3, v3, v7
	v_max_f32_e32 v7, v9, v1
	v_min_f32_e32 v1, v9, v1
	v_max_f32_e32 v9, v11, v6
	v_min_f32_e32 v6, v11, v6
	v_max_f32_e32 v11, v16, v15
	v_min_f32_e32 v15, v16, v15
	v_max_f32_e32 v16, v12, v14
	v_min_f32_e32 v12, v12, v14
	v_max_f32_e32 v14, v5, v10
	v_min_f32_e32 v5, v5, v10
	v_max_f32_e32 v10, v13, v8
	v_min_f32_e32 v8, v13, v8
	v_max_f32_e32 v13, v4, v7
	v_min_f32_e32 v4, v4, v7
	v_max_f32_e32 v7, v0, v3
	v_min_f32_e32 v0, v0, v3
	v_max_f32_e32 v3, v2, v1
	v_min_f32_e32 v1, v2, v1
	v_max_f32_e32 v2, v9, v11
	v_min_f32_e32 v9, v9, v11
	v_max_f32_e32 v11, v6, v15
	v_min_f32_e32 v6, v6, v15
	v_max_f32_e32 v15, v16, v14
	v_min_f32_e32 v14, v16, v14
	v_max_f32_e32 v16, v12, v5
	v_min_f32_e32 v5, v12, v5
	v_max_f32_e32 v12, v10, v13
	v_min_f32_e32 v10, v10, v13
	v_max_f32_e32 v13, v8, v4
	v_min_f32_e32 v4, v8, v4
	v_max_f32_e32 v8, v7, v3
	v_min_f32_e32 v3, v7, v3
	v_max_f32_e32 v7, v0, v1
	v_min_f32_e32 v0, v0, v1
	ds_bpermute_b32 v27, v184, v0
	ds_bpermute_b32 v29, v184, v7
	ds_bpermute_b32 v31, v184, v3
	ds_bpermute_b32 v30, v184, v8
	ds_bpermute_b32 v28, v184, v4
	ds_bpermute_b32 v26, v184, v13
	s_waitcnt lgkmcnt(5)
	ds_bpermute_b32 v1, v184, v2
	ds_bpermute_b32 v25, v184, v10
	v_max_f32_e32 v2, v2, v27
	s_waitcnt lgkmcnt(6)
	ds_bpermute_b32 v17, v184, v9
	ds_bpermute_b32 v24, v184, v12
	v_max_f32_e32 v9, v9, v29
	s_waitcnt lgkmcnt(7)
	ds_bpermute_b32 v18, v184, v11
	ds_bpermute_b32 v23, v184, v5
	v_max_f32_e32 v11, v11, v31
	s_waitcnt lgkmcnt(8)
	ds_bpermute_b32 v19, v184, v6
	ds_bpermute_b32 v22, v184, v16
	v_max_f32_e32 v6, v6, v30
	s_waitcnt lgkmcnt(9)
	ds_bpermute_b32 v20, v184, v15
	ds_bpermute_b32 v21, v184, v14
	v_max_f32_e32 v15, v15, v28
	s_waitcnt lgkmcnt(10)
	v_max_f32_e32 v14, v14, v26
	s_waitcnt lgkmcnt(8)
	v_max_f32_e32 v16, v16, v25
	s_waitcnt lgkmcnt(6)
	v_max_f32_e32 v5, v5, v24
	s_waitcnt lgkmcnt(4)
	v_max_f32_e32 v12, v12, v23
	s_waitcnt lgkmcnt(2)
	v_max_f32_e32 v10, v10, v22
	s_waitcnt lgkmcnt(0)
	v_max_f32_e32 v13, v13, v21
	v_max_f32_e32 v4, v4, v20
	v_max_f32_e32 v8, v8, v19
	v_max_f32_e32 v3, v3, v18
	v_max_f32_e32 v7, v7, v17
	v_max_f32_e32 v0, v0, v1
	v_max_f32_e32 v1, v2, v12
	v_min_f32_e32 v2, v2, v12
	v_max_f32_e32 v12, v9, v10
	v_min_f32_e32 v9, v9, v10
	v_max_f32_e32 v10, v11, v13
	v_min_f32_e32 v11, v11, v13
	v_max_f32_e32 v13, v6, v4
	v_min_f32_e32 v4, v6, v4
	v_max_f32_e32 v6, v15, v8
	v_min_f32_e32 v8, v15, v8
	v_max_f32_e32 v15, v14, v3
	v_min_f32_e32 v3, v14, v3
	v_max_f32_e32 v14, v16, v7
	v_min_f32_e32 v7, v16, v7
	v_max_f32_e32 v16, v5, v0
	v_min_f32_e32 v0, v5, v0
	v_max_f32_e32 v5, v1, v6
	v_min_f32_e32 v1, v1, v6
	v_max_f32_e32 v6, v12, v15
	v_min_f32_e32 v12, v12, v15
	v_max_f32_e32 v15, v10, v14
	v_min_f32_e32 v10, v10, v14
	v_max_f32_e32 v14, v13, v16
	v_min_f32_e32 v13, v13, v16
	v_max_f32_e32 v16, v2, v8
	v_min_f32_e32 v2, v2, v8
	v_max_f32_e32 v8, v9, v3
	v_min_f32_e32 v3, v9, v3
	v_max_f32_e32 v9, v11, v7
	v_min_f32_e32 v7, v11, v7
	v_max_f32_e32 v11, v4, v0
	v_min_f32_e32 v0, v4, v0
	v_max_f32_e32 v4, v5, v15
	v_min_f32_e32 v5, v5, v15
	v_max_f32_e32 v15, v6, v14
	v_min_f32_e32 v6, v6, v14
	v_max_f32_e32 v14, v1, v10
	v_min_f32_e32 v1, v1, v10
	v_max_f32_e32 v10, v12, v13
	v_min_f32_e32 v12, v12, v13
	v_max_f32_e32 v13, v16, v9
	v_min_f32_e32 v9, v16, v9
	v_max_f32_e32 v16, v8, v11
	v_min_f32_e32 v8, v8, v11
	v_max_f32_e32 v11, v2, v7
	v_min_f32_e32 v2, v2, v7
	v_max_f32_e32 v7, v3, v0
	v_min_f32_e32 v0, v3, v0
	v_max_f32_e32 v3, v4, v15
	v_min_f32_e32 v4, v4, v15
	v_max_f32_e32 v15, v5, v6
	v_min_f32_e32 v5, v5, v6
	v_max_f32_e32 v6, v14, v10
	v_min_f32_e32 v10, v14, v10
	v_max_f32_e32 v14, v1, v12
	v_min_f32_e32 v1, v1, v12
	v_max_f32_e32 v12, v13, v16
	v_min_f32_e32 v13, v13, v16
	v_max_f32_e32 v16, v9, v8
	v_min_f32_e32 v8, v9, v8
	v_max_f32_e32 v9, v11, v7
	v_min_f32_e32 v7, v11, v7
	v_max_f32_e32 v11, v2, v0
	v_min_f32_e32 v0, v2, v0
	v_lshl_add_u32 v2, s8, 12, v207
	ds_write2st64_b32 v2, v3, v4 offset1:1
	ds_write2st64_b32 v2, v15, v5 offset0:2 offset1:3
	ds_write2st64_b32 v2, v6, v10 offset0:4 offset1:5
	ds_write2st64_b32 v2, v14, v1 offset0:6 offset1:7
	ds_write2st64_b32 v2, v12, v13 offset0:8 offset1:9
	ds_write2st64_b32 v2, v16, v8 offset0:10 offset1:11
	ds_write2st64_b32 v2, v9, v7 offset0:12 offset1:13
	ds_write2st64_b32 v2, v11, v0 offset0:14 offset1:15
	s_mov_b64 s[6:7], 0
	s_mov_b32 s8, 1
	s_cbranch_vccz .LBB0_704
	ds_read2st64_b32 v[0:1], v207 offset1:1
	ds_read2st64_b32 v[2:3], v207 offset0:2 offset1:3
	ds_read2st64_b32 v[4:5], v207 offset0:4 offset1:5
	ds_read2st64_b32 v[6:7], v207 offset0:6 offset1:7
	ds_read2st64_b32 v[16:17], v207 offset0:16 offset1:17
	ds_read2st64_b32 v[18:19], v207 offset0:18 offset1:19
	ds_read2st64_b32 v[20:21], v207 offset0:20 offset1:21
	ds_read2st64_b32 v[22:23], v207 offset0:22 offset1:23
	ds_read2st64_b32 v[8:9], v207 offset0:8 offset1:9
	ds_read2st64_b32 v[10:11], v207 offset0:10 offset1:11
	ds_read2st64_b32 v[12:13], v207 offset0:12 offset1:13
	ds_read2st64_b32 v[14:15], v207 offset0:14 offset1:15
	ds_read2st64_b32 v[24:25], v207 offset0:24 offset1:25
	ds_read2st64_b32 v[26:27], v207 offset0:26 offset1:27
	ds_read2st64_b32 v[28:29], v207 offset0:28 offset1:29
	ds_read2st64_b32 v[30:31], v207 offset0:30 offset1:31
	s_and_saveexec_b64 s[8:9], s[38:39]
	s_cbranch_execz .LBB0_696
	s_waitcnt lgkmcnt(0)
	v_and_b32_e32 v49, 0xffffff80, v30
	v_and_b32_e32 v48, 0xffffff80, v0
	v_and_b32_e32 v39, 0xffffff80, v19
	v_and_b32_e32 v38, 0xffffff80, v20
	v_pk_add_f32 v[52:53], v[38:39], v[48:49] op_sel:[1,0] op_sel_hi:[0,1]
	v_cmp_gt_i32_e32 vcc, 0, v52
	v_bfrev_b32_e32 v43, 0.5
	s_movk_i32 s12, 0xff00
	v_cndmask_b32_e64 v43, v43, 3, vcc
	v_and_b32_e32 v42, 0xffffff80, v23
	v_and_or_b32 v56, v52, s12, v43
	v_mov_b32_e32 v43, v38
	v_pk_add_f32 v[52:53], v[48:49], v[42:43] op_sel_hi:[0,1]
	v_cmp_gt_i32_e32 vcc, 0, v53
	v_mov_b32_e32 v54, 0xfb
	v_and_b32_e32 v41, 0xffffff80, v22
	v_cndmask_b32_e64 v54, v54, 4, vcc
	v_and_b32_e32 v40, 0xffffff80, v21
	v_and_or_b32 v53, v53, s12, v54
	v_cmp_gt_i32_e32 vcc, 0, v52
	v_mov_b32_e32 v54, 0xf8
	v_mov_b32_e32 v58, 0xf9
	v_cndmask_b32_e64 v57, v54, 7, vcc
	v_pk_add_f32 v[54:55], v[48:49], v[40:41] op_sel_hi:[0,1]
	v_cmp_gt_i32_e32 vcc, 0, v55
	v_mov_b32_e32 v59, 0xfa
	v_and_b32_e32 v55, 0xffffff00, v55
	v_cndmask_b32_e64 v58, v58, 6, vcc
	v_cmp_gt_i32_e32 vcc, 0, v54
	v_and_b32_e32 v54, 0xffffff00, v54
	v_and_b32_e32 v52, 0xffffff00, v52
	v_cndmask_b32_e64 v59, v59, 5, vcc
	v_or_b32_e32 v55, v58, v55
	v_or_b32_e32 v54, v59, v54
	v_or_b32_e32 v52, v57, v52
	v_writelane_b32 v255, s8, 44
	v_min_f32_e32 v57, v55, v52
	v_max_f32_e32 v58, v53, v54
	v_min_f32_e32 v53, v53, v54
	v_max_f32_e32 v52, v55, v52
	v_writelane_b32 v255, s9, 45
	v_and_b32_e32 v45, 0xffffff80, v24
	v_and_b32_e32 v44, 0xffffff80, v27
	v_min_f32_e32 v59, v58, v57
	v_min_f32_e32 v54, v53, v52
	v_max_f32_e32 v57, v58, v57
	v_max_f32_e32 v52, v53, v52
	v_pk_add_f32 v[44:45], v[48:49], v[44:45] op_sel_hi:[0,1]
	v_and_b32_e32 v47, 0xffffff80, v26
	v_min_f32_e32 v58, v57, v52
	v_max_f32_e32 v57, v57, v52
	v_cmp_gt_i32_e32 vcc, 0, v45
	v_mov_b32_e32 v52, 0xf7
	v_and_b32_e32 v46, 0xffffff80, v25
	v_cndmask_b32_e64 v52, v52, 8, vcc
	v_and_or_b32 v45, v45, s12, v52
	v_cmp_gt_i32_e32 vcc, 0, v44
	v_mov_b32_e32 v52, 0xf4
	v_pk_add_f32 v[46:47], v[48:49], v[46:47] op_sel_hi:[0,1]
	v_cndmask_b32_e64 v52, v52, 11, vcc
	v_cmp_gt_i32_e32 vcc, 0, v47
	v_mov_b32_e32 v53, 0xf5
	v_min_f32_e32 v55, v59, v54
	v_max_f32_e32 v59, v59, v54
	v_cndmask_b32_e64 v53, v53, 10, vcc
	v_cmp_gt_i32_e32 vcc, 0, v46
	v_mov_b32_e32 v54, 0xf6
	v_and_b32_e32 v47, 0xffffff00, v47
	v_cndmask_b32_e64 v54, v54, 9, vcc
	v_and_b32_e32 v46, 0xffffff00, v46
	v_and_b32_e32 v44, 0xffffff00, v44
	v_or_b32_e32 v47, v53, v47
	v_or_b32_e32 v46, v54, v46
	v_or_b32_e32 v44, v52, v44
	v_and_b32_e32 v51, 0xffffff80, v29
	v_and_b32_e32 v50, 0xffffff80, v28
	v_writelane_b32 v255, s11, 46
	v_min_f32_e32 v52, v47, v44
	v_max_f32_e32 v53, v45, v46
	v_min_f32_e32 v46, v45, v46
	v_max_f32_e32 v47, v47, v44
	v_pk_add_f32 v[44:45], v[48:49], v[50:51] op_sel_hi:[0,1]
	v_cmp_gt_i32_e64 s[10:11], 0, v45
	v_mov_b32_e32 v50, 0xf2
	v_mov_b32_e32 v51, 0xf3
	v_cndmask_b32_e64 v50, v50, 13, s[10:11]
	v_cmp_gt_i32_e64 s[10:11], 0, v44
	v_and_b32_e32 v45, 0xffffff00, v45
	v_and_b32_e32 v44, 0xffffff00, v44
	v_cndmask_b32_e64 v51, v51, 12, s[10:11]
	v_or_b32_e32 v50, v50, v45
	v_or_b32_e32 v51, v51, v44
	v_and_b32_e32 v45, 0xffffff80, v31
	v_mov_b32_e32 v44, v49
	v_pk_add_f32 v[44:45], v[48:49], v[44:45] op_sel_hi:[0,1]
	v_cmp_gt_i32_e64 s[42:43], 0, v45
	v_mov_b32_e32 v249, 0xf0
	v_mov_b32_e32 v173, 0xf1
	v_cndmask_b32_e64 v63, v249, 15, s[42:43]
	v_cmp_gt_i32_e64 s[42:43], 0, v44
	v_and_b32_e32 v45, 0xffffff00, v45
	v_and_b32_e32 v44, 0xffffff00, v44
	v_cndmask_b32_e64 v173, v173, 14, s[42:43]
	v_or_b32_e32 v45, v63, v45
	v_or_b32_e32 v44, v173, v44
	v_max_f32_e32 v62, v51, v50
	v_min_f32_e32 v63, v44, v45
	v_min_f32_e32 v50, v51, v50
	v_max_f32_e32 v44, v44, v45
	v_max_f32_e32 v54, v53, v52
	v_max_f32_e32 v60, v46, v47
	v_min_f32_e32 v173, v62, v63
	v_min_f32_e32 v45, v50, v44
	v_min_f32_e32 v51, v53, v52
	v_min_f32_e32 v46, v46, v47
	v_max_f32_e32 v52, v62, v63
	v_max_f32_e32 v44, v50, v44
	v_max_f32_e32 v61, v54, v60
	v_min_f32_e32 v178, v173, v45
	v_max_f32_e32 v47, v51, v46
	v_min_f32_e32 v50, v52, v44
	v_min_f32_e32 v54, v54, v60
	v_max_f32_e32 v45, v173, v45
	v_min_f32_e32 v46, v51, v46
	v_max_f32_e32 v44, v52, v44
	v_min_f32_e32 v179, v61, v178
	v_min_f32_e32 v53, v47, v50
	v_min_f32_e32 v60, v54, v45
	v_min_f32_e32 v52, v46, v44
	v_max_f32_e32 v61, v61, v178
	v_max_f32_e32 v47, v47, v50
	v_max_f32_e32 v45, v54, v45
	v_max_f32_e32 v44, v46, v44
	v_min_f32_e32 v62, v179, v53
	v_min_f32_e32 v63, v60, v52
	v_min_f32_e32 v50, v61, v47
	v_min_f32_e32 v46, v45, v44
	v_max_f32_e32 v53, v179, v53
	v_max_f32_e32 v52, v60, v52
	v_max_f32_e32 v47, v61, v47
	v_max_f32_e32 v44, v45, v44
	v_min_f32_e32 v60, v53, v52
	v_min_f32_e32 v61, v47, v44
	v_max_f32_e32 v52, v53, v52
	v_max_f32_e32 v53, v47, v44
	v_and_b32_e32 v44, 0xffffff80, v1
	v_add_f32_e32 v45, v39, v44
	v_min_f32_e32 v51, v62, v63
	v_min_f32_e32 v173, v50, v46
	v_max_f32_e32 v62, v62, v63
	v_max_f32_e32 v63, v50, v46
	v_cmp_gt_i32_e32 vcc, 0, v45
	v_mov_b32_e32 v46, 0xec
	v_mov_b32_e32 v47, 0xe9
	v_cndmask_b32_e64 v46, v46, 19, vcc
	v_and_or_b32 v45, v45, s12, v46
	v_pk_add_f32 v[42:43], v[44:45], v[42:43] op_sel_hi:[0,1]
	v_cmp_gt_i32_e32 vcc, 0, v43
	v_mov_b32_e32 v46, 0xeb
	v_pk_add_f32 v[40:41], v[44:45], v[40:41] op_sel_hi:[0,1]
	v_cndmask_b32_e64 v46, v46, 20, vcc
	v_and_or_b32 v43, v43, s12, v46
	v_cmp_gt_i32_e32 vcc, 0, v42
	v_mov_b32_e32 v46, 0xe8
	v_mov_b32_e32 v50, 0xea
	v_cndmask_b32_e64 v46, v46, 23, vcc
	v_cmp_gt_i32_e32 vcc, 0, v41
	v_and_b32_e32 v41, 0xffffff00, v41
	v_and_b32_e32 v42, 0xffffff00, v42
	v_cndmask_b32_e64 v47, v47, 22, vcc
	v_cmp_gt_i32_e32 vcc, 0, v40
	v_and_b32_e32 v40, 0xffffff00, v40
	v_or_b32_e32 v41, v47, v41
	v_cndmask_b32_e64 v50, v50, 21, vcc
	v_or_b32_e32 v40, v50, v40
	v_or_b32_e32 v42, v46, v42
	v_and_b32_e32 v182, 0xffffff80, v3
	v_min_f32_e32 v46, v41, v42
	v_max_f32_e32 v47, v43, v40
	v_min_f32_e32 v40, v43, v40
	v_max_f32_e32 v41, v41, v42
	v_and_b32_e32 v37, 0xffffff80, v4
	v_max_f32_e32 v43, v47, v46
	v_min_f32_e32 v42, v40, v41
	v_max_f32_e32 v40, v40, v41
	v_min_f32_e32 v50, v47, v46
	v_and_b32_e32 v46, 0xffffff80, v2
	v_and_b32_e32 v36, 0xffffff80, v18
	v_min_f32_e32 v179, v43, v40
	v_max_f32_e32 v180, v43, v40
	v_pk_add_f32 v[40:41], v[46:47], v[38:39] op_sel_hi:[0,1]
	v_cmp_gt_i32_e32 vcc, 0, v41
	v_mov_b32_e32 v38, 0xdc
	v_and_b32_e32 v35, 0xffffff80, v7
	v_cndmask_b32_e64 v38, v38, 35, vcc
	v_and_or_b32 v41, v41, s12, v38
	v_cmp_gt_i32_e32 vcc, 0, v40
	v_mov_b32_e32 v38, 0xdb
	v_and_b32_e32 v34, 0xffffff80, v17
	v_cndmask_b32_e64 v38, v38, 36, vcc
	v_and_or_b32 v181, v40, s12, v38
	v_add_f32_e32 v38, v39, v182
	v_cmp_gt_i32_e32 vcc, 0, v38
	v_mov_b32_e32 v39, 0xcc
	s_nop 0
	v_cndmask_b32_e64 v39, v39, 51, vcc
	v_and_or_b32 v54, v38, s12, v39
	v_pk_add_f32 v[38:39], v[48:49], v[36:37]
	v_min_f32_e32 v178, v50, v42
	v_cmp_gt_i32_e32 vcc, 0, v38
	v_bfrev_b32_e32 v39, -0.5
	v_max_f32_e32 v50, v50, v42
	v_cndmask_b32_e64 v39, v39, 2, vcc
	v_and_or_b32 v38, v38, s12, v39
	v_mov_b32_e32 v39, 0xed
	v_and_b32_e32 v43, 0xffffff80, v6
	v_min_f32_e32 v183, v38, v56
	v_max_f32_e32 v56, v38, v56
	v_add_f32_e32 v38, v36, v44
	v_cmp_gt_i32_e32 vcc, 0, v38
	v_and_b32_e32 v42, 0xffffff80, v5
	v_and_b32_e32 v33, 0xffffff80, v14
	v_cndmask_b32_e64 v39, v39, 18, vcc
	v_and_or_b32 v38, v38, s12, v39
	v_mov_b32_e32 v39, 0xdd
	v_and_b32_e32 v32, 0xffffff80, v16
	v_min_f32_e32 v190, v38, v45
	v_max_f32_e32 v195, v38, v45
	v_add_f32_e32 v38, v36, v46
	v_cmp_gt_i32_e32 vcc, 0, v38
	v_mov_b32_e32 v45, 0x61
	v_mov_b32_e32 v234, 0xef
	v_cndmask_b32_e64 v39, v39, 34, vcc
	v_and_or_b32 v38, v38, s12, v39
	v_mov_b32_e32 v39, 0xcd
	v_mov_b32_e32 v241, 0xdf
	v_min_f32_e32 v209, v38, v41
	v_max_f32_e32 v210, v38, v41
	v_add_f32_e32 v38, v36, v182
	v_cmp_gt_i32_e32 vcc, 0, v38
	v_mov_b32_e32 v41, 0x42
	v_mov_b32_e32 v244, 0xcf
	v_cndmask_b32_e64 v39, v39, 50, vcc
	v_and_or_b32 v40, v38, s12, v39
	v_pk_add_f32 v[38:39], v[36:37], v[36:37] op_sel:[1,0] op_sel_hi:[0,1]
	v_cmp_gt_i32_e32 vcc, 0, v38
	v_mov_b32_e32 v39, 0xbd
	v_and_b32_e32 v47, 0xffffff80, v8
	v_cndmask_b32_e32 v39, v39, v41, vcc
	v_and_or_b32 v41, v38, s12, v39
	v_pk_add_f32 v[38:39], v[48:49], v[34:35]
	v_pk_add_f32 v[48:49], v[48:49], v[32:33]
	v_cmp_gt_i32_e32 vcc, 0, v38
	v_mov_b32_e32 v39, 0xfe
	s_mov_b32 s28, 0xff61b1e6
	v_cndmask_b32_e64 v39, v39, 1, vcc
	v_and_or_b32 v211, v38, s12, v39
	v_add_f32_e32 v38, v34, v44
	v_cmp_gt_i32_e32 vcc, 0, v38
	v_mov_b32_e32 v39, 0xee
	v_add_f32_e32 v44, v32, v44
	v_cndmask_b32_e64 v39, v39, 17, vcc
	v_and_or_b32 v212, v38, s12, v39
	v_add_f32_e32 v38, v34, v46
	v_cmp_gt_i32_e32 vcc, 0, v38
	v_mov_b32_e32 v39, 0xde
	v_add_f32_e32 v46, v32, v46
	v_cndmask_b32_e64 v39, v39, 33, vcc
	v_and_or_b32 v213, v38, s12, v39
	v_add_f32_e32 v38, v34, v182
	v_cmp_gt_i32_e32 vcc, 0, v38
	v_mov_b32_e32 v39, 0xce
	v_add_f32_e32 v182, v32, v182
	v_cndmask_b32_e64 v39, v39, 49, vcc
	v_and_or_b32 v38, v38, s12, v39
	v_cmp_gt_i32_e64 s[74:75], 0, v46
	v_cmp_gt_i32_e64 s[84:85], 0, v182
	v_min_f32_e32 v219, v38, v40
	v_max_f32_e32 v220, v38, v40
	v_pk_add_f32 v[38:39], v[36:37], v[34:35] op_sel:[1,0] op_sel_hi:[0,1]
	v_cmp_gt_i32_e32 vcc, 0, v38
	v_mov_b32_e32 v39, 0xbe
	v_mov_b32_e32 v40, 0x41
	v_cndmask_b32_e32 v39, v39, v40, vcc
	v_and_or_b32 v38, v38, s12, v39
	v_mov_b32_e32 v40, v35
	v_cndmask_b32_e64 v241, v241, 32, s[74:75]
	v_min_f32_e32 v215, v38, v41
	v_max_f32_e32 v216, v38, v41
	v_pk_add_f32 v[38:39], v[34:35], v[42:43]
	v_mov_b32_e32 v41, v43
	v_pk_add_f32 v[40:41], v[34:35], v[40:41] op_sel_hi:[0,1]
	v_cmp_gt_i32_e32 vcc, 0, v38
	v_mov_b32_e32 v34, 0xae
	v_mov_b32_e32 v39, 0x51
	v_cndmask_b32_e32 v34, v34, v39, vcc
	v_cmp_gt_i32_e32 vcc, 0, v41
	v_mov_b32_e32 v39, 0x9e
	v_and_b32_e32 v38, 0xffffff00, v38
	v_cndmask_b32_e32 v39, v39, v45, vcc
	v_or_b32_e32 v218, v34, v38
	v_cmp_gt_i32_e32 vcc, 0, v40
	v_mov_b32_e32 v34, 0x8e
	v_mov_b32_e32 v38, 0x71
	v_cndmask_b32_e32 v34, v34, v38, vcc
	v_and_or_b32 v214, v40, s12, v34
	v_cmp_gt_i32_e32 vcc, 0, v48
	v_mov_b32_e32 v34, 0xff
	v_cndmask_b32_e64 v244, v244, 48, s[84:85]
	v_cndmask_b32_e64 v34, v34, 0, vcc
	v_and_or_b32 v34, v48, s12, v34
	v_and_or_b32 v46, v46, s12, v241
	v_and_or_b32 v182, v182, s12, v244
	v_max_f32_e32 v48, v34, v211
	v_min_f32_e32 v34, v34, v211
	v_max_f32_e32 v49, v48, v183
	v_max_f32_e32 v211, v34, v56
	v_min_f32_e32 v48, v48, v183
	v_min_f32_e32 v34, v34, v56
	v_max_f32_e32 v221, v49, v211
	v_max_f32_e32 v56, v48, v34
	v_min_f32_e32 v49, v49, v211
	v_min_f32_e32 v34, v48, v34
	v_max_f32_e32 v222, v221, v55
	v_max_f32_e32 v183, v56, v58
	v_max_f32_e32 v211, v49, v59
	v_max_f32_e32 v48, v34, v57
	v_min_f32_e32 v55, v221, v55
	v_min_f32_e32 v56, v56, v58
	v_min_f32_e32 v49, v49, v59
	v_min_f32_e32 v34, v34, v57
	v_max_f32_e32 v241, v46, v213
	v_max_f32_e32 v58, v55, v56
	v_max_f32_e32 v57, v49, v34
	v_min_f32_e32 v55, v55, v56
	v_min_f32_e32 v34, v49, v34
	v_min_f32_e32 v46, v46, v213
	v_max_f32_e32 v244, v181, v182
	v_max_f32_e32 v49, v55, v34
	v_min_f32_e32 v34, v55, v34
	v_cmp_gt_i32_e64 s[6:7], 0, v44
	v_min_f32_e32 v181, v181, v182
	s_nop 0
	v_cndmask_b32_e64 v234, v234, 16, s[6:7]
	v_and_or_b32 v44, v44, s12, v234
	v_max_f32_e32 v234, v44, v212
	v_min_f32_e32 v44, v44, v212
	v_max_f32_e32 v235, v234, v190
	v_max_f32_e32 v212, v44, v195
	v_min_f32_e32 v190, v234, v190
	v_min_f32_e32 v44, v44, v195
	v_max_f32_e32 v242, v241, v209
	v_max_f32_e32 v213, v46, v210
	v_min_f32_e32 v245, v244, v219
	v_min_f32_e32 v182, v181, v220
	v_min_f32_e32 v209, v241, v209
	v_min_f32_e32 v46, v46, v210
	v_max_f32_e32 v219, v244, v219
	v_max_f32_e32 v181, v181, v220
	v_max_f32_e32 v59, v58, v57
	v_min_f32_e32 v57, v58, v57
	v_max_f32_e32 v236, v235, v212
	v_max_f32_e32 v195, v190, v44
	v_min_f32_e32 v212, v235, v212
	v_min_f32_e32 v44, v190, v44
	v_max_f32_e32 v243, v242, v213
	v_min_f32_e32 v246, v245, v182
	v_max_f32_e32 v210, v209, v46
	v_min_f32_e32 v220, v219, v181
	v_min_f32_e32 v213, v242, v213
	v_max_f32_e32 v182, v245, v182
	v_min_f32_e32 v46, v209, v46
	v_max_f32_e32 v181, v219, v181
	v_max_f32_e32 v237, v236, v178
	v_max_f32_e32 v234, v195, v179
	v_max_f32_e32 v235, v212, v50
	v_max_f32_e32 v190, v44, v180
	v_min_f32_e32 v247, v243, v246
	v_min_f32_e32 v241, v210, v220
	v_min_f32_e32 v242, v213, v182
	v_min_f32_e32 v209, v46, v181
	v_min_f32_e32 v178, v236, v178
	v_min_f32_e32 v179, v195, v179
	v_min_f32_e32 v50, v212, v50
	v_min_f32_e32 v44, v44, v180
	v_max_f32_e32 v236, v243, v246
	v_max_f32_e32 v210, v210, v220
	v_max_f32_e32 v182, v213, v182
	v_max_f32_e32 v46, v46, v181
	v_max_f32_e32 v223, v222, v183
	v_max_f32_e32 v224, v211, v48
	v_min_f32_e32 v183, v222, v183
	v_min_f32_e32 v48, v211, v48
	v_max_f32_e32 v238, v237, v234
	v_max_f32_e32 v239, v235, v190
	v_min_f32_e32 v244, v247, v241
	v_min_f32_e32 v219, v242, v209
	v_max_f32_e32 v195, v178, v179
	v_max_f32_e32 v180, v50, v44
	v_min_f32_e32 v220, v236, v210
	v_min_f32_e32 v181, v182, v46
	v_min_f32_e32 v234, v237, v234
	v_min_f32_e32 v190, v235, v190
	v_max_f32_e32 v237, v247, v241
	v_max_f32_e32 v209, v242, v209
	v_min_f32_e32 v178, v178, v179
	v_min_f32_e32 v44, v50, v44
	v_max_f32_e32 v50, v236, v210
	v_max_f32_e32 v46, v182, v46
	v_max_f32_e32 v225, v223, v224
	v_max_f32_e32 v211, v183, v48
	v_min_f32_e32 v223, v223, v224
	v_min_f32_e32 v48, v183, v48
	v_max_f32_e32 v240, v238, v239
	v_min_f32_e32 v245, v244, v219
	v_max_f32_e32 v212, v195, v180
	v_min_f32_e32 v213, v220, v181
	v_max_f32_e32 v235, v234, v190
	v_min_f32_e32 v241, v237, v209
	v_max_f32_e32 v179, v178, v44
	v_min_f32_e32 v182, v50, v46
	v_min_f32_e32 v238, v238, v239
	v_max_f32_e32 v219, v244, v219
	v_min_f32_e32 v180, v195, v180
	v_max_f32_e32 v181, v220, v181
	v_min_f32_e32 v190, v234, v190
	v_max_f32_e32 v209, v237, v209
	v_min_f32_e32 v44, v178, v44
	v_max_f32_e32 v46, v50, v46
	v_max_f32_e32 v226, v225, v51
	v_max_f32_e32 v221, v59, v173
	v_max_f32_e32 v222, v211, v60
	v_max_f32_e32 v56, v49, v61
	v_max_f32_e32 v224, v223, v62
	v_max_f32_e32 v58, v57, v63
	v_max_f32_e32 v183, v48, v52
	v_max_f32_e32 v55, v34, v53
	v_min_f32_e32 v248, v240, v245
	v_min_f32_e32 v243, v212, v213
	v_min_f32_e32 v242, v235, v241
	v_min_f32_e32 v210, v179, v182
	v_min_f32_e32 v239, v238, v219
	v_min_f32_e32 v195, v180, v181
	v_min_f32_e32 v234, v190, v209
	v_min_f32_e32 v178, v44, v46
	v_max_f32_e32 v227, v226, v221
	v_max_f32_e32 v228, v222, v56
	v_max_f32_e32 v230, v224, v58
	v_max_f32_e32 v231, v183, v55
	v_min_f32_e32 v246, v248, v243
	v_min_f32_e32 v236, v242, v210
	v_min_f32_e32 v220, v239, v195
	v_min_f32_e32 v237, v234, v178
	v_max_f32_e32 v229, v227, v228
	v_max_f32_e32 v232, v230, v231
	v_min_f32_e32 v247, v246, v236
	v_min_f32_e32 v244, v220, v237
	v_min_f32_e32 v51, v225, v51
	v_min_f32_e32 v59, v59, v173
	v_min_f32_e32 v60, v211, v60
	v_min_f32_e32 v61, v49, v61
	v_min_f32_e32 v62, v223, v62
	v_min_f32_e32 v57, v57, v63
	v_min_f32_e32 v48, v48, v52
	v_min_f32_e32 v34, v34, v53
	v_max_f32_e32 v63, v240, v245
	v_max_f32_e32 v212, v212, v213
	v_max_f32_e32 v235, v235, v241
	v_max_f32_e32 v179, v179, v182
	v_max_f32_e32 v219, v238, v219
	v_max_f32_e32 v180, v180, v181
	v_max_f32_e32 v190, v190, v209
	v_max_f32_e32 v44, v44, v46
	v_max_f32_e32 v233, v229, v232
	v_min_f32_e32 v50, v247, v244
	v_max_f32_e32 v173, v51, v59
	v_max_f32_e32 v211, v60, v61
	v_max_f32_e32 v223, v62, v57
	v_max_f32_e32 v53, v48, v34
	v_min_f32_e32 v213, v63, v212
	v_min_f32_e32 v182, v235, v179
	v_min_f32_e32 v181, v219, v180
	v_min_f32_e32 v46, v190, v44
	v_min_f32_e32 v227, v227, v228
	v_min_f32_e32 v228, v230, v231
	v_max_f32_e32 v230, v246, v236
	v_max_f32_e32 v220, v220, v237
	v_max_f32_e32 v50, v233, v50
	v_max_f32_e32 v44, v190, v44
	v_max_f32_e32 v225, v173, v211
	v_max_f32_e32 v233, v223, v53
	v_min_f32_e32 v240, v213, v182
	v_min_f32_e32 v209, v181, v46
	v_min_f32_e32 v221, v226, v221
	v_min_f32_e32 v222, v222, v56
	v_min_f32_e32 v224, v224, v58
	v_min_f32_e32 v183, v183, v55
	v_max_f32_e32 v241, v248, v243
	v_max_f32_e32 v210, v242, v210
	v_max_f32_e32 v195, v239, v195
	v_max_f32_e32 v234, v234, v178
	v_min_f32_e32 v51, v51, v59
	v_min_f32_e32 v59, v60, v61
	v_min_f32_e32 v57, v62, v57
	v_min_f32_e32 v34, v48, v34
	v_max_f32_e32 v60, v63, v212
	v_max_f32_e32 v62, v235, v179
	v_max_f32_e32 v58, v227, v228
	v_min_f32_e32 v63, v230, v220
	v_min_f32_e32 v211, v173, v211
	v_min_f32_e32 v223, v223, v53
	v_max_f32_e32 v213, v213, v182
	v_max_f32_e32 v46, v181, v46
	v_max_f32_e32 v226, v221, v222
	v_max_f32_e32 v238, v224, v183
	v_max_f32_e32 v243, v51, v59
	v_max_f32_e32 v245, v57, v34
	v_min_f32_e32 v179, v60, v62
	v_max_f32_e32 v63, v58, v63
	v_max_f32_e32 v53, v211, v223
	v_min_f32_e32 v58, v213, v46
	v_min_f32_e32 v181, v221, v222
	v_min_f32_e32 v221, v224, v183
	v_max_f32_e32 v222, v241, v210
	v_max_f32_e32 v224, v195, v234
	v_min_f32_e32 v51, v51, v59
	v_min_f32_e32 v59, v57, v34
	v_max_f32_e32 v231, v60, v62
	v_min_f32_e32 v57, v229, v232
	v_max_f32_e32 v62, v247, v244
	v_min_f32_e32 v239, v195, v234
	v_min_f32_e32 v242, v241, v210
	v_max_f32_e32 v212, v219, v180
	v_max_f32_e32 v178, v53, v58
	v_max_f32_e32 v53, v181, v221
	v_min_f32_e32 v173, v222, v224
	v_max_f32_e32 v183, v57, v62
	v_min_f32_e32 v57, v225, v233
	v_max_f32_e32 v62, v240, v209
	v_min_f32_e32 v219, v212, v44
	v_max_f32_e32 v180, v53, v173
	v_max_f32_e32 v190, v57, v62
	v_min_f32_e32 v57, v226, v238
	v_max_f32_e32 v173, v242, v239
	v_max_f32_e32 v55, v226, v238
	v_min_f32_e32 v56, v242, v239
	v_max_f32_e32 v210, v230, v220
	v_max_f32_e32 v195, v57, v173
	v_min_f32_e32 v57, v243, v245
	v_max_f32_e32 v173, v179, v219
	v_max_f32_e32 v55, v55, v56
	v_min_f32_e32 v56, v179, v219
	v_min_f32_e32 v179, v227, v228
	v_min_f32_e32 v52, v240, v209
	v_max_f32_e32 v209, v57, v173
	v_max_f32_e32 v46, v213, v46
	v_max_f32_e32 v44, v212, v44
	v_max_f32_e32 v210, v179, v210
	v_min_f32_e32 v179, v211, v223
	v_max_f32_e32 v211, v179, v46
	v_min_f32_e32 v46, v181, v221
	v_max_f32_e32 v181, v222, v224
	v_min_f32_e32 v53, v231, v44
	v_max_f32_e32 v44, v231, v44
	v_max_f32_e32 v212, v46, v181
	v_min_f32_e32 v46, v51, v59
	v_max_f32_e32 v34, v51, v59
	v_pk_add_f32 v[36:37], v[36:37], v[32:33] op_sel:[1,0] op_sel_hi:[0,1]
	v_mov_b32_e32 v37, 0xbf
	v_max_f32_e32 v213, v46, v44
	v_cmp_gt_i32_e32 vcc, 0, v36
	v_mov_b32_e32 v221, 0x50
	v_and_b32_e32 v41, 0xffffff00, v41
	v_cndmask_b32_e64 v37, v37, 64, vcc
	v_and_or_b32 v36, v36, s12, v37
	v_or_b32_e32 v217, v39, v41
	v_max_f32_e32 v49, v225, v233
	v_max_f32_e32 v44, v54, v36
	v_min_f32_e32 v54, v54, v36
	v_pk_add_f32 v[36:37], v[32:33], v[42:43] op_sel_hi:[0,1]
	v_cmp_gt_i32_e64 s[68:69], 0, v37
	v_mov_b32_e32 v42, 0x9f
	v_mov_b32_e32 v43, 0x60
	v_cndmask_b32_e64 v42, v42, v43, s[68:69]
	v_cmp_gt_i32_e64 s[68:69], 0, v36
	v_mov_b32_e32 v43, 0xaf
	v_and_b32_e32 v37, 0xffffff00, v37
	v_cndmask_b32_e64 v43, v43, v221, s[68:69]
	v_and_b32_e32 v36, 0xffffff00, v36
	v_or_b32_e32 v37, v42, v37
	v_or_b32_e32 v36, v43, v36
	v_min_f32_e32 v42, v37, v217
	v_max_f32_e32 v43, v36, v218
	v_max_f32_e32 v37, v37, v217
	v_min_f32_e32 v36, v36, v218
	v_max_f32_e32 v46, v44, v215
	v_max_f32_e32 v219, v54, v216
	v_min_f32_e32 v221, v43, v42
	v_min_f32_e32 v217, v36, v37
	v_max_f32_e32 v42, v43, v42
	v_max_f32_e32 v36, v36, v37
	v_max_f32_e32 v220, v46, v219
	v_min_f32_e32 v44, v44, v215
	v_min_f32_e32 v54, v54, v216
	v_min_f32_e32 v219, v46, v219
	v_mov_b32_e32 v46, v35
	v_min_f32_e32 v216, v42, v36
	v_max_f32_e32 v225, v42, v36
	v_pk_add_f32 v[36:37], v[32:33], v[46:47] op_sel_hi:[0,1]
	v_and_b32_e32 v45, 0xffffff80, v9
	v_max_f32_e32 v215, v44, v54
	v_min_f32_e32 v54, v44, v54
	v_mov_b32_e32 v44, v35
	v_cmp_gt_i32_e32 vcc, 0, v37
	v_mov_b32_e32 v35, 0x7f
	v_pk_add_f32 v[42:43], v[32:33], v[44:45] op_sel_hi:[0,1]
	v_cndmask_b32_e32 v35, v35, v196, vcc
	v_cmp_gt_i32_e32 vcc, 0, v36
	v_mov_b32_e32 v47, 0x8f
	v_mov_b32_e32 v45, 0x6f
	v_cndmask_b32_e32 v44, v47, v198, vcc
	v_cmp_gt_i32_e32 vcc, 0, v43
	v_mov_b32_e32 v46, 0x90
	v_and_b32_e32 v37, 0xffffff00, v37
	v_and_b32_e32 v36, 0xffffff00, v36
	v_cndmask_b32_e32 v45, v45, v46, vcc
	v_and_b32_e32 v43, 0xffffff00, v43
	v_cmp_gt_i32_e32 vcc, 0, v42
	v_or_b32_e32 v35, v35, v37
	v_or_b32_e32 v36, v44, v36
	v_or_b32_e32 v37, v45, v43
	v_and_b32_e32 v41, 0xffffff80, v10
	v_and_b32_e32 v40, 0xffffff80, v13
	v_cndmask_b32_e32 v46, v47, v198, vcc
	v_cmp_lt_f32_e32 vcc, v37, v35
	v_cmp_lt_f32_e64 s[8:9], v214, v36
	v_and_b32_e32 v39, 0xffffff80, v12
	v_cndmask_b32_e32 v43, v35, v37, vcc
	v_cndmask_b32_e64 v45, v36, v214, s[8:9]
	v_cndmask_b32_e32 v35, v37, v35, vcc
	v_pk_add_f32 v[36:37], v[32:33], v[40:41] op_sel_hi:[0,1]
	v_cmp_gt_i32_e64 s[80:81], 0, v37
	v_mov_b32_e32 v40, 0x5f
	v_mov_b32_e32 v41, 0xa0
	v_and_b32_e32 v38, 0xffffff80, v11
	v_cndmask_b32_e64 v40, v40, v41, s[80:81]
	v_and_b32_e32 v42, 0xffffff00, v42
	v_and_or_b32 v37, v37, s12, v40
	v_cmp_gt_i32_e64 s[80:81], 0, v36
	v_mov_b32_e32 v40, 0xd0
	v_pk_add_f32 v[38:39], v[32:33], v[38:39] op_sel_hi:[0,1]
	v_or_b32_e32 v42, v46, v42
	v_cndmask_b32_e64 v40, 47, v40, s[80:81]
	v_cmp_gt_i32_e64 s[80:81], 0, v39
	v_mov_b32_e32 v41, 0xc0
	v_cndmask_b32_e64 v42, v214, v42, s[8:9]
	v_cndmask_b32_e64 v41, 63, v41, s[80:81]
	v_cmp_gt_i32_e64 s[80:81], 0, v38
	v_mov_b32_e32 v214, 0x4f
	v_mov_b32_e32 v229, 0xb0
	v_cndmask_b32_e64 v214, v214, v229, s[80:81]
	v_and_b32_e32 v39, 0xffffff00, v39
	v_and_b32_e32 v38, 0xffffff00, v38
	v_and_b32_e32 v36, 0xffffff00, v36
	v_or_b32_e32 v39, v41, v39
	v_or_b32_e32 v38, v214, v38
	v_or_b32_e32 v36, v40, v36
	v_min_f32_e32 v40, v39, v36
	v_max_f32_e32 v41, v37, v38
	v_min_f32_e32 v37, v37, v38
	v_max_f32_e32 v36, v39, v36
	v_max_f32_e32 v44, v42, v43
	v_max_f32_e32 v46, v45, v35
	v_min_f32_e32 v214, v41, v40
	v_min_f32_e32 v38, v37, v36
	v_min_f32_e32 v42, v42, v43
	v_min_f32_e32 v35, v45, v35
	v_max_f32_e32 v40, v41, v40
	v_max_f32_e32 v36, v37, v36
	v_max_f32_e32 v47, v44, v46
	v_min_f32_e32 v39, v214, v38
	v_max_f32_e32 v43, v42, v35
	v_min_f32_e32 v37, v40, v36
	v_min_f32_e32 v44, v44, v46
	v_max_f32_e32 v38, v214, v38
	v_min_f32_e32 v35, v42, v35
	v_max_f32_e32 v36, v40, v36
	v_min_f32_e32 v218, v221, v217
	v_max_f32_e32 v217, v221, v217
	v_min_f32_e32 v229, v47, v39
	v_min_f32_e32 v41, v43, v37
	v_min_f32_e32 v46, v44, v38
	v_min_f32_e32 v40, v35, v36
	v_max_f32_e32 v39, v47, v39
	v_max_f32_e32 v37, v43, v37
	v_max_f32_e32 v38, v44, v38
	v_max_f32_e32 v35, v35, v36
	v_max_f32_e32 v222, v220, v218
	v_max_f32_e32 v223, v215, v216
	v_max_f32_e32 v221, v219, v217
	v_max_f32_e32 v226, v54, v225
	v_min_f32_e32 v218, v220, v218
	v_min_f32_e32 v215, v215, v216
	v_min_f32_e32 v217, v219, v217
	v_min_f32_e32 v54, v54, v225
	v_min_f32_e32 v43, v39, v37
	v_min_f32_e32 v36, v38, v35
	v_max_f32_e32 v37, v39, v37
	v_max_f32_e32 v35, v38, v35
	v_max_f32_e32 v216, v218, v215
	v_max_f32_e32 v219, v217, v54
	v_min_f32_e32 v44, v43, v36
	v_min_f32_e32 v215, v218, v215
	v_min_f32_e32 v54, v217, v54
	v_min_f32_e32 v38, v37, v35
	v_max_f32_e32 v43, v43, v36
	v_max_f32_e32 v35, v37, v35
	v_and_b32_e32 v37, 0xffffff80, v15
	v_mov_b32_e32 v36, v33
	v_pk_add_f32 v[32:33], v[32:33], v[36:37] op_sel_hi:[0,1]
	v_mov_b32_e32 v37, 0xe0
	v_max_f32_e32 v217, v215, v54
	v_min_f32_e32 v54, v215, v54
	v_cmp_gt_i32_e64 s[76:77], 0, v33
	v_and_b32_e32 v33, 0xffffff00, v33
	s_nop 0
	v_cndmask_b32_e64 v36, 15, v249, s[76:77]
	v_cmp_gt_i32_e64 s[76:77], 0, v32
	v_and_b32_e32 v32, 0xffffff00, v32
	v_or_b32_e32 v33, v36, v33
	v_cndmask_b32_e64 v37, 31, v37, s[76:77]
	v_or_b32_e32 v32, v37, v32
	v_max_f32_e32 v36, v32, v33
	v_min_f32_e32 v32, v32, v33
	v_max_f32_e32 v37, v36, v36
	v_max_f32_e32 v33, v32, v32
	v_max_f32_e32 v37, 0xff61b1e6, v37
	v_max_f32_e32 v33, 0xff61b1e6, v33
	v_max_f32_e32 v224, v222, v223
	v_max_f32_e32 v233, v37, v33
	v_min_f32_e32 v33, v37, v33
	v_max_f32_e32 v234, 0xff61b1e6, v233
	v_max_f32_e32 v37, 0xff61b1e6, v33
	v_cmp_nlt_f32_e32 vcc, s28, v33
	v_max_f32_e32 v227, v221, v226
	v_max_f32_e32 v235, v234, v37
	v_cmp_nlt_f32_e64 s[88:89], s28, v235
	v_cndmask_b32_e32 v33, v199, v33, vcc
	v_min_f32_e32 v45, v229, v41
	v_cndmask_b32_e64 v236, v199, v235, s[88:89]
	v_cmp_nlt_f32_e64 s[88:89], s28, v233
	v_min_f32_e32 v42, v46, v40
	v_min_f32_e32 v222, v222, v223
	v_cndmask_b32_e64 v233, v199, v233, s[88:89]
	v_cmp_nlt_f32_e64 s[88:89], s28, v36
	v_min_f32_e32 v221, v221, v226
	v_max_f32_e32 v41, v229, v41
	v_cndmask_b32_e64 v36, v199, v36, s[88:89]
	v_cmp_nlt_f32_e64 s[88:89], s28, v32
	v_max_f32_e32 v40, v46, v40
	s_nop 0
	v_cndmask_b32_e64 v32, v199, v32, s[88:89]
	v_max_f32_e32 v237, v36, v32
	v_min_f32_e32 v32, v36, v32
	v_max_f32_e32 v238, v233, v237
	v_max_f32_e32 v36, v33, v32
	v_max_f32_e32 v228, v224, v227
	v_min_f32_e32 v214, v45, v42
	v_max_f32_e32 v220, v216, v219
	v_max_f32_e32 v223, v222, v221
	v_min_f32_e32 v46, v41, v40
	v_min_f32_e32 v224, v224, v227
	v_max_f32_e32 v42, v45, v42
	v_min_f32_e32 v216, v216, v219
	v_min_f32_e32 v221, v222, v221
	v_max_f32_e32 v40, v41, v40
	v_max_f32_e32 v239, v238, v36
	v_min_f32_e32 v233, v233, v237
	v_min_f32_e32 v32, v33, v32
	v_min_f32_e32 v37, v234, v37
	v_min_f32_e32 v36, v238, v36
	v_max_f32_e32 v52, v49, v52
	s_mov_b64 s[6:7], s[96:97]
	v_cmp_nlt_f32_e64 s[88:89], s28, v239
	v_cmp_nlt_f32_e64 s[76:77], s28, v37
	v_cmp_nlt_f32_e64 s[14:15], s28, v36
	v_max_f32_e32 v230, v228, v214
	v_max_f32_e32 v47, v220, v44
	v_max_f32_e32 v226, v223, v46
	v_max_f32_e32 v39, v217, v38
	v_max_f32_e32 v45, v224, v42
	v_max_f32_e32 v219, v216, v43
	v_max_f32_e32 v41, v221, v40
	v_max_f32_e32 v215, v54, v35
	v_cndmask_b32_e64 v240, v199, v239, s[88:89]
	v_max_f32_e32 v33, v233, v32
	v_cndmask_b32_e64 v234, v199, v37, s[76:77]
	v_cndmask_b32_e64 v238, v199, v36, s[14:15]
	v_min_f32_e32 v32, v233, v32
	v_cmp_nlt_f32_e64 s[88:89], s28, v33
	v_cmp_nlt_f32_e32 vcc, s28, v32
	v_max_f32_e32 v48, v243, v245
	v_max_f32_e32 v225, v230, v47
	v_max_f32_e32 v218, v226, v39
	v_max_f32_e32 v227, v45, v219
	v_max_f32_e32 v222, v41, v215
	v_min_f32_e32 v241, v236, v240
	v_cndmask_b32_e64 v237, v199, v33, s[88:89]
	v_min_f32_e32 v243, v234, v238
	v_cndmask_b32_e32 v233, v199, v32, vcc
	v_max_f32_e32 v229, v225, v218
	v_max_f32_e32 v231, v227, v222
	v_min_f32_e32 v242, v241, v237
	v_min_f32_e32 v244, v243, v233
	v_min_f32_e32 v214, v228, v214
	v_max_f32_e32 v232, v229, v231
	v_min_f32_e32 v245, v242, v244
	v_max_f32_e32 v228, 0xff61b1e6, v235
	v_max_f32_e32 v235, v239, v239
	v_max_f32_e32 v36, v36, v36
	v_min_f32_e32 v44, v220, v44
	v_min_f32_e32 v46, v223, v46
	v_min_f32_e32 v38, v217, v38
	v_min_f32_e32 v42, v224, v42
	v_min_f32_e32 v43, v216, v43
	v_min_f32_e32 v40, v221, v40
	v_min_f32_e32 v35, v54, v35
	v_max_f32_e32 v235, 0xff61b1e6, v235
	v_max_f32_e32 v33, v33, v33
	v_max_f32_e32 v37, 0xff61b1e6, v37
	v_max_f32_e32 v36, 0xff61b1e6, v36
	v_max_f32_e32 v32, v32, v32
	v_max_f32_e32 v232, v232, v245
	s_mov_b32 s36, s18
	v_max_f32_e32 v33, 0xff61b1e6, v33
	v_max_f32_e32 v32, 0xff61b1e6, v32
	v_max_f32_e32 v220, v214, v44
	v_max_f32_e32 v217, v46, v38
	v_max_f32_e32 v216, v42, v43
	v_max_f32_e32 v54, v40, v35
	v_min_f32_e32 v239, v228, v235
	v_min_f32_e32 v245, 0xff61b1e6, v33
	v_min_f32_e32 v247, v37, v36
	v_min_f32_e32 v248, 0xff61b1e6, v32
	v_max_f32_e32 v223, v220, v217
	v_max_f32_e32 v221, v216, v54
	v_min_f32_e32 v246, v239, v245
	v_min_f32_e32 v249, v247, v248
	v_min_f32_e32 v47, v230, v47
	v_max_f32_e32 v230, v236, v240
	v_cmp_ngt_f32_e64 s[16:17], s28, v237
	v_max_f32_e32 v234, v234, v238
	v_cmp_ngt_f32_e64 s[14:15], s28, v233
	v_min_f32_e32 v44, v214, v44
	v_min_f32_e32 v38, v46, v38
	v_min_f32_e32 v42, v42, v43
	v_min_f32_e32 v35, v40, v35
	v_max_f32_e32 v214, v228, v235
	v_max_f32_e32 v36, v37, v36
	v_max_f32_e32 v224, v223, v221
	v_min_f32_e32 v250, v246, v249
	v_min_f32_e32 v39, v226, v39
	v_min_f32_e32 v45, v45, v219
	v_min_f32_e32 v41, v41, v215
	v_cndmask_b32_e64 v236, v199, v237, s[16:17]
	v_cndmask_b32_e64 v238, v199, v233, s[14:15]
	v_max_f32_e32 v46, v44, v38
	v_max_f32_e32 v40, v42, v35
	v_min_f32_e32 v228, v214, v33
	v_min_f32_e32 v37, v36, v32
	v_max_f32_e32 v224, v224, v250
	v_max_f32_e32 v226, v47, v39
	v_max_f32_e32 v215, v45, v41
	v_min_f32_e32 v240, v230, v236
	v_min_f32_e32 v250, v234, v238
	v_min_f32_e32 v218, v225, v218
	v_min_f32_e32 v222, v227, v222
	v_max_f32_e32 v237, v241, v237
	v_max_f32_e32 v233, v243, v233
	v_min_f32_e32 v39, v47, v39
	v_min_f32_e32 v41, v45, v41
	v_max_f32_e32 v47, v230, v236
	v_max_f32_e32 v230, v234, v238
	v_max_f32_e32 v43, v46, v40
	v_min_f32_e32 v235, v228, v37
	v_min_f32_e32 v217, v220, v217
	v_min_f32_e32 v54, v216, v54
	v_max_f32_e32 v239, v239, v245
	v_max_f32_e32 v243, v247, v248
	v_min_f32_e32 v38, v44, v38
	v_min_f32_e32 v35, v42, v35
	v_max_f32_e32 v33, v214, v33
	v_max_f32_e32 v32, v36, v32
	v_max_f32_e32 v219, v226, v215
	v_max_f32_e32 v227, v218, v222
	v_min_f32_e32 v241, v237, v233
	v_max_f32_e32 v45, v39, v41
	v_min_f32_e32 v234, v47, v230
	v_min_f32_e32 v229, v229, v231
	v_max_f32_e32 v231, v242, v244
	v_min_f32_e32 v215, v226, v215
	v_max_f32_e32 v226, v240, v250
	v_min_f32_e32 v251, v240, v250
	v_max_f32_e32 v43, v43, v235
	v_max_f32_e32 v216, v217, v54
	v_min_f32_e32 v245, v239, v243
	v_max_f32_e32 v42, v38, v35
	v_min_f32_e32 v36, v33, v32
	v_min_f32_e32 v221, v223, v221
	v_max_f32_e32 v223, v246, v249
	v_min_f32_e32 v40, v46, v40
	v_max_f32_e32 v37, v228, v37
	v_min_f32_e32 v218, v218, v222
	v_max_f32_e32 v222, v237, v233
	v_min_f32_e32 v54, v217, v54
	v_max_f32_e32 v217, v239, v243
	v_min_f32_e32 v39, v39, v41
	v_max_f32_e32 v41, v47, v230
	v_min_f32_e32 v35, v38, v35
	v_max_f32_e32 v32, v33, v32
	v_max_f32_e32 v227, v227, v241
	v_max_f32_e32 v45, v45, v234
	v_max_f32_e32 v229, v229, v231
	v_max_f32_e32 v215, v215, v226
	v_max_f32_e32 v61, v48, v56
	v_max_f32_e32 v182, v34, v53
	v_max_f32_e32 v219, v219, v251
	v_max_f32_e32 v216, v216, v245
	v_max_f32_e32 v36, v42, v36
	v_max_f32_e32 v221, v221, v223
	v_max_f32_e32 v37, v40, v37
	v_max_f32_e32 v218, v218, v222
	v_max_f32_e32 v217, v54, v217
	v_max_f32_e32 v39, v39, v41
	v_max_f32_e32 v32, v35, v32
	v_max_f32_e32 v49, v50, v52
	v_max_f32_e32 v56, v55, v61
	v_max_f32_e32 v58, v63, v178
	v_max_f32_e32 v60, v180, v182
	v_max_f32_e32 v62, v183, v190
	v_max_f32_e32 v173, v195, v209
	v_max_f32_e32 v179, v210, v211
	v_max_f32_e32 v181, v212, v213
	v_min_f32_e32 v225, v232, v224
	v_min_f32_e32 v241, v219, v43
	v_min_f32_e32 v245, v227, v216
	v_min_f32_e32 v42, v45, v36
	v_min_f32_e32 v223, v229, v221
	v_min_f32_e32 v40, v215, v37
	v_min_f32_e32 v222, v218, v217
	v_min_f32_e32 v33, v39, v32
	v_max_f32_e32 v48, v49, v56
	v_max_f32_e32 v53, v58, v60
	v_max_f32_e32 v57, v62, v173
	v_max_f32_e32 v59, v179, v181
	v_min_f32_e32 v220, v225, v241
	v_min_f32_e32 v44, v245, v42
	v_min_f32_e32 v46, v223, v40
	v_min_f32_e32 v35, v222, v33
	v_max_f32_e32 v34, v48, v53
	v_max_f32_e32 v51, v57, v59
	v_min_f32_e32 v214, v220, v44
	v_min_f32_e32 v38, v46, v35
	v_min_f32_e32 v47, v55, v61
	v_max_f32_e32 v235, v34, v51
	v_min_f32_e32 v41, v214, v38
	v_min_f32_e32 v61, v63, v178
	v_min_f32_e32 v63, v180, v182
	v_max_f32_e32 v54, v235, v41
	v_min_f32_e32 v41, v50, v52
	v_min_f32_e32 v182, v183, v190
	v_min_f32_e32 v183, v195, v209
	v_min_f32_e32 v190, v210, v211
	v_min_f32_e32 v209, v212, v213
	v_max_f32_e32 v212, v232, v224
	v_max_f32_e32 v43, v219, v43
	v_max_f32_e32 v216, v227, v216
	v_max_f32_e32 v36, v45, v36
	v_max_f32_e32 v221, v229, v221
	v_max_f32_e32 v37, v215, v37
	v_max_f32_e32 v217, v218, v217
	v_max_f32_e32 v32, v39, v32
	v_min_f32_e32 v49, v49, v56
	v_min_f32_e32 v224, v58, v60
	v_min_f32_e32 v62, v62, v173
	v_min_f32_e32 v173, v179, v181
	v_max_f32_e32 v181, v225, v241
	v_max_f32_e32 v42, v245, v42
	v_max_f32_e32 v40, v223, v40
	v_max_f32_e32 v33, v222, v33
	v_max_f32_e32 v50, v41, v47
	v_max_f32_e32 v178, v61, v63
	v_max_f32_e32 v195, v182, v183
	v_min_f32_e32 v213, v212, v43
	v_min_f32_e32 v45, v216, v36
	v_min_f32_e32 v215, v221, v37
	v_min_f32_e32 v39, v217, v32
	v_max_f32_e32 v226, v49, v224
	v_max_f32_e32 v179, v62, v173
	v_min_f32_e32 v225, v181, v42
	v_min_f32_e32 v222, v40, v33
	v_min_f32_e32 v41, v41, v47
	v_min_f32_e32 v47, v61, v63
	v_min_f32_e32 v63, v182, v183
	v_min_f32_e32 v182, v190, v209
	v_max_f32_e32 v43, v212, v43
	v_max_f32_e32 v36, v216, v36
	v_max_f32_e32 v37, v221, v37
	v_max_f32_e32 v32, v217, v32
	v_cmp_gt_f32_e64 s[24:25], v63, v182
	v_max_f32_e32 v210, v190, v209
	v_max_f32_e32 v56, v226, v179
	v_min_f32_e32 v58, v225, v222
	v_max_f32_e32 v223, v41, v47
	v_cndmask_b32_e64 v183, v182, v63, s[24:25]
	v_min_f32_e32 v209, v43, v36
	v_min_f32_e32 v212, v37, v32
	v_max_f32_e32 v56, v56, v58
	v_max_f32_e32 v58, v223, v183
	v_min_f32_e32 v60, v209, v212
	v_min_f32_e32 v48, v48, v53
	v_min_f32_e32 v217, v57, v59
	v_max_f32_e32 v44, v220, v44
	v_max_f32_e32 v35, v46, v35
	v_max_f32_e32 v58, v58, v60
	v_max_f32_e32 v53, v48, v217
	v_min_f32_e32 v46, v44, v35
	v_max_f32_e32 v180, v50, v178
	v_min_f32_e32 v219, v213, v45
	v_min_f32_e32 v218, v215, v39
	v_max_f32_e32 v59, v53, v46
	v_min_f32_e32 v46, v50, v178
	v_min_f32_e32 v50, v195, v210
	v_max_f32_e32 v45, v213, v45
	v_max_f32_e32 v39, v215, v39
	v_min_f32_e32 v49, v49, v224
	v_max_f32_e32 v53, v46, v50
	v_min_f32_e32 v57, v45, v39
	v_min_f32_e32 v213, v62, v173
	v_max_f32_e32 v42, v181, v42
	v_max_f32_e32 v33, v40, v33
	v_max_f32_e32 v60, v53, v57
	v_cmp_gt_f32_e64 s[20:21], v49, v213
	v_max_f32_e32 v211, v195, v210
	s_nop 0
	v_cndmask_b32_e64 v57, v213, v49, s[20:21]
	v_min_f32_e32 v40, v42, v33
	v_max_f32_e32 v36, v43, v36
	v_max_f32_e32 v32, v37, v32
	v_max_f32_e32 v61, v57, v40
	v_min_f32_e32 v40, v41, v47
	v_cndmask_b32_e64 v41, v63, v182, s[24:25]
	v_cmp_gt_f32_e64 s[14:15], v40, v41
	v_min_f32_e32 v34, v34, v51
	s_nop 0
	v_cndmask_b32_e64 v47, v41, v40, s[14:15]
	v_min_f32_e32 v37, v36, v32
	s_mov_b64 s[96:97], s[6:7]
	v_max_f32_e32 v62, v47, v37
	v_max_f32_e32 v37, v214, v38
	v_max_f32_e32 v35, v44, v35
	v_min_f32_e32 v55, v219, v218
	v_max_f32_e32 v63, v34, v37
	v_min_f32_e32 v34, v180, v211
	v_max_f32_e32 v37, v219, v218
	v_max_f32_e32 v52, v180, v211
	v_max_f32_e32 v33, v42, v33
	v_max_f32_e32 v173, v34, v37
	v_min_f32_e32 v34, v226, v179
	v_max_f32_e32 v37, v225, v222
	v_max_f32_e32 v32, v36, v32
	v_max_f32_e32 v178, v34, v37
	v_min_f32_e32 v34, v223, v183
	v_max_f32_e32 v37, v209, v212
	v_max_f32_e32 v55, v52, v55
	v_max_f32_e32 v179, v34, v37
	v_min_f32_e32 v34, v48, v217
	v_max_f32_e32 v180, v34, v35
	v_min_f32_e32 v34, v46, v50
	v_max_f32_e32 v35, v45, v39
	v_max_f32_e32 v181, v34, v35
	v_cndmask_b32_e64 v34, v49, v213, s[20:21]
	v_max_f32_e32 v182, v34, v33
	v_cndmask_b32_e64 v33, v40, v41, s[14:15]
	v_min_f32_e32 v52, v54, v55
	v_min_f32_e32 v190, v56, v58
	v_max_f32_e32 v183, v33, v32
	v_min_f32_e32 v53, v59, v60
	v_min_f32_e32 v57, v61, v62
	v_min_f32_e32 v195, v63, v173
	v_min_f32_e32 v209, v178, v179
	v_min_f32_e32 v210, v180, v181
	v_min_f32_e32 v211, v182, v183
	v_min_f32_e32 v216, v52, v190
	v_min_f32_e32 v215, v53, v57
	v_min_f32_e32 v51, v195, v209
	v_min_f32_e32 v50, v210, v211
	s_movk_i32 s10, 0xff
	v_min_f32_e32 v220, v216, v215
	v_min_f32_e32 v212, v51, v50
	s_movk_i32 s8, 0x7f
	v_bitop3_b32 v35, v31, s8, v31 bitop3:0xc
	v_min_f32_e32 v32, v220, v212
	v_and_b32_e32 v33, 0xff, v32
	v_bitop3_b32 v34, v32, s10, v32 bitop3:0xc
	v_cmp_gt_i32_e64 s[6:7], 0, v32
	v_readlane_b32 s94, v255, 39
	v_readlane_b32 s95, v255, 40
	v_cndmask_b32_e64 v213, v34, v33, s[6:7]
	v_and_b32_e32 v33, 0x7f, v31
	v_cmp_gt_i32_e64 s[6:7], 0, v31
	v_and_b32_e32 v34, 15, v213
	v_lshrrev_b32_e32 v214, 4, v213
	v_cndmask_b32_e64 v31, v35, v33, s[6:7]
	v_and_b32_e32 v33, 0x7f, v30
	v_bitop3_b32 v35, v30, s8, v30 bitop3:0xc
	v_cmp_gt_i32_e64 s[6:7], 0, v30
	v_readlane_b32 s86, v255, 31
	v_readlane_b32 s82, v255, 33
	v_cndmask_b32_e64 v30, v35, v33, s[6:7]
	v_and_b32_e32 v33, 0x7f, v29
	v_bitop3_b32 v35, v29, s8, v29 bitop3:0xc
	v_cmp_gt_i32_e64 s[6:7], 0, v29
	v_readlane_b32 s84, v255, 25
	v_readlane_b32 s87, v255, 32
	v_cndmask_b32_e64 v29, v35, v33, s[6:7]
	v_and_b32_e32 v33, 0x7f, v28
	v_bitop3_b32 v35, v28, s8, v28 bitop3:0xc
	v_cmp_gt_i32_e64 s[6:7], 0, v28
	v_readlane_b32 s92, v255, 35
	v_readlane_b32 s88, v255, 29
	v_cndmask_b32_e64 v28, v35, v33, s[6:7]
	v_and_b32_e32 v33, 0x7f, v27
	v_bitop3_b32 v35, v27, s8, v27 bitop3:0xc
	v_cmp_gt_i32_e64 s[6:7], 0, v27
	v_readlane_b32 s90, v255, 27
	v_readlane_b32 s78, v255, 13
	v_cndmask_b32_e64 v27, v35, v33, s[6:7]
	v_and_b32_e32 v33, 0x7f, v26
	v_bitop3_b32 v35, v26, s8, v26 bitop3:0xc
	v_cmp_gt_i32_e64 s[6:7], 0, v26
	v_readlane_b32 s83, v255, 34
	v_readlane_b32 s74, v255, 9
	v_cndmask_b32_e64 v26, v35, v33, s[6:7]
	v_and_b32_e32 v33, 0x7f, v25
	v_bitop3_b32 v35, v25, s8, v25 bitop3:0xc
	v_cmp_gt_i32_e64 s[6:7], 0, v25
	v_readlane_b32 s85, v255, 26
	v_readlane_b32 s76, v255, 11
	v_cndmask_b32_e64 v25, v35, v33, s[6:7]
	v_and_b32_e32 v33, 0x7f, v24
	v_bitop3_b32 v35, v24, s8, v24 bitop3:0xc
	v_cmp_gt_i32_e64 s[6:7], 0, v24
	v_readlane_b32 s22, v255, 23
	v_readlane_b32 s34, v255, 17
	v_cndmask_b32_e64 v24, v35, v33, s[6:7]
	v_and_b32_e32 v33, 0x7f, v23
	v_bitop3_b32 v35, v23, s8, v23 bitop3:0xc
	v_cmp_gt_i32_e64 s[6:7], 0, v23
	v_readlane_b32 s30, v255, 15
	v_readlane_b32 s81, v255, 41
	v_cndmask_b32_e64 v23, v35, v33, s[6:7]
	v_and_b32_e32 v33, 0x7f, v22
	v_bitop3_b32 v35, v22, s8, v22 bitop3:0xc
	v_cmp_gt_i32_e64 s[6:7], 0, v22
	s_movk_i32 s87, 0x4000
	v_readlane_b32 s93, v255, 36
	v_cndmask_b32_e64 v22, v35, v33, s[6:7]
	v_and_b32_e32 v33, 0x7f, v21
	v_bitop3_b32 v35, v21, s8, v21 bitop3:0xc
	v_cmp_gt_i32_e64 s[6:7], 0, v21
	v_readlane_b32 s89, v255, 30
	v_readlane_b32 s91, v255, 28
	v_cndmask_b32_e64 v21, v35, v33, s[6:7]
	v_and_b32_e32 v33, 0x7f, v20
	v_bitop3_b32 v35, v20, s8, v20 bitop3:0xc
	v_cmp_gt_i32_e64 s[6:7], 0, v20
	v_readlane_b32 s79, v255, 14
	v_readlane_b32 s83, v255, 37
	v_cndmask_b32_e64 v20, v35, v33, s[6:7]
	v_and_b32_e32 v33, 0x7f, v19
	v_bitop3_b32 v35, v19, s8, v19 bitop3:0xc
	v_cmp_gt_i32_e64 s[6:7], 0, v19
	v_readlane_b32 s75, v255, 10
	v_readlane_b32 s85, v255, 38
	v_cndmask_b32_e64 v19, v35, v33, s[6:7]
	v_and_b32_e32 v33, 0x7f, v18
	v_bitop3_b32 v35, v18, s8, v18 bitop3:0xc
	v_cmp_gt_i32_e64 s[6:7], 0, v18
	v_readlane_b32 s77, v255, 12
	v_readlane_b32 s23, v255, 24
	v_cndmask_b32_e64 v18, v35, v33, s[6:7]
	v_and_b32_e32 v33, 0x7f, v17
	v_bitop3_b32 v35, v17, s8, v17 bitop3:0xc
	v_cmp_gt_i32_e64 s[6:7], 0, v17
	s_mov_b32 s18, s36
	s_movk_i32 s27, 0x1200
	v_cndmask_b32_e64 v17, v35, v33, s[6:7]
	v_and_b32_e32 v33, 0x7f, v16
	v_bitop3_b32 v35, v16, s8, v16 bitop3:0xc
	v_cmp_gt_i32_e64 s[6:7], 0, v16
	v_readlane_b32 s35, v255, 18
	v_readlane_b32 s31, v255, 16
	v_cndmask_b32_e64 v33, v35, v33, s[6:7]
	v_cmp_eq_u32_e64 s[6:7], 0, v34
	v_bitop3_b32 v35, v15, s8, v15 bitop3:0xc
	s_nop 0
	v_cndmask_b32_e64 v16, 0, v33, s[6:7]
	v_cmp_eq_u32_e64 s[6:7], 1, v34
	s_nop 1
	v_cndmask_b32_e64 v16, v16, v17, s[6:7]
	v_cmp_eq_u32_e64 s[6:7], 2, v34
	s_nop 1
	v_cndmask_b32_e64 v16, v16, v18, s[6:7]
	v_cmp_eq_u32_e64 s[6:7], 3, v34
	s_nop 1
	v_cndmask_b32_e64 v16, v16, v19, s[6:7]
	v_cmp_eq_u32_e64 s[6:7], 4, v34
	s_nop 1
	v_cndmask_b32_e64 v16, v16, v20, s[6:7]
	v_cmp_eq_u32_e64 s[6:7], 5, v34
	s_nop 1
	v_cndmask_b32_e64 v16, v16, v21, s[6:7]
	v_cmp_eq_u32_e64 s[6:7], 6, v34
	s_nop 1
	v_cndmask_b32_e64 v16, v16, v22, s[6:7]
	v_cmp_eq_u32_e64 s[6:7], 7, v34
	s_nop 1
	v_cndmask_b32_e64 v16, v16, v23, s[6:7]
	v_cmp_eq_u32_e64 s[6:7], 8, v34
	s_nop 1
	v_cndmask_b32_e64 v16, v16, v24, s[6:7]
	v_cmp_eq_u32_e64 s[6:7], 9, v34
	s_nop 1
	v_cndmask_b32_e64 v16, v16, v25, s[6:7]
	v_cmp_eq_u32_e64 s[6:7], 10, v34
	s_nop 1
	v_cndmask_b32_e64 v16, v16, v26, s[6:7]
	v_cmp_eq_u32_e64 s[6:7], 11, v34
	s_nop 1
	v_cndmask_b32_e64 v16, v16, v27, s[6:7]
	v_cmp_eq_u32_e64 s[6:7], 12, v34
	s_nop 1
	v_cndmask_b32_e64 v16, v16, v28, s[6:7]
	v_cmp_eq_u32_e64 s[6:7], 13, v34
	s_nop 1
	v_cndmask_b32_e64 v16, v16, v29, s[6:7]
	v_cmp_eq_u32_e64 s[6:7], 14, v34
	s_nop 1
	v_cndmask_b32_e64 v16, v16, v30, s[6:7]
	v_cmp_eq_u32_e64 s[6:7], 15, v34
	v_and_b32_e32 v34, 0x7f, v15
	s_nop 0
	v_cndmask_b32_e64 v16, v16, v31, s[6:7]
	v_cmp_gt_i32_e64 s[6:7], 0, v15
	v_and_b32_e32 v15, 0x7f, v14
	s_nop 0
	v_cndmask_b32_e64 v34, v35, v34, s[6:7]
	v_bitop3_b32 v35, v14, s8, v14 bitop3:0xc
	v_cmp_gt_i32_e64 s[6:7], 0, v14
	v_and_b32_e32 v14, 0x7f, v13
	s_nop 0
	v_cndmask_b32_e64 v35, v35, v15, s[6:7]
	v_bitop3_b32 v15, v13, s8, v13 bitop3:0xc
	v_cmp_gt_i32_e64 s[6:7], 0, v13
	v_and_b32_e32 v13, 0x7f, v12
	s_nop 0
	v_cndmask_b32_e64 v36, v15, v14, s[6:7]
	v_bitop3_b32 v14, v12, s8, v12 bitop3:0xc
	v_cmp_gt_i32_e64 s[6:7], 0, v12
	v_and_b32_e32 v12, 0x7f, v11
	v_max_f32_e32 v15, v59, v60
	v_cndmask_b32_e64 v37, v14, v13, s[6:7]
	v_bitop3_b32 v13, v11, s8, v11 bitop3:0xc
	v_cmp_gt_i32_e64 s[6:7], 0, v11
	v_and_b32_e32 v11, 0x7f, v10
	v_max_f32_e32 v14, v56, v58
	v_cndmask_b32_e64 v38, v13, v12, s[6:7]
	v_bitop3_b32 v12, v10, s8, v10 bitop3:0xc
	v_cmp_gt_i32_e64 s[6:7], 0, v10
	v_and_b32_e32 v10, 0x7f, v9
	v_max_f32_e32 v59, v61, v62
	v_cndmask_b32_e64 v39, v12, v11, s[6:7]
	v_bitop3_b32 v11, v9, s8, v9 bitop3:0xc
	v_cmp_gt_i32_e64 s[6:7], 0, v9
	v_and_b32_e32 v9, 0x7f, v8
	v_max_f32_e32 v60, v63, v173
	v_cndmask_b32_e64 v40, v11, v10, s[6:7]
	v_bitop3_b32 v10, v8, s8, v8 bitop3:0xc
	v_cmp_gt_i32_e64 s[6:7], 0, v8
	v_and_b32_e32 v8, 0x7f, v7
	v_max_f32_e32 v61, v178, v179
	v_cndmask_b32_e64 v41, v10, v9, s[6:7]
	v_bitop3_b32 v9, v7, s8, v7 bitop3:0xc
	v_cmp_gt_i32_e64 s[6:7], 0, v7
	v_and_b32_e32 v7, 0x7f, v6
	v_max_f32_e32 v62, v180, v181
	v_cndmask_b32_e64 v42, v9, v8, s[6:7]
	v_bitop3_b32 v8, v6, s8, v6 bitop3:0xc
	v_cmp_gt_i32_e64 s[6:7], 0, v6
	v_and_b32_e32 v6, 0x7f, v5
	v_max_f32_e32 v9, v210, v211
	v_cndmask_b32_e64 v43, v8, v7, s[6:7]
	v_bitop3_b32 v7, v5, s8, v5 bitop3:0xc
	v_cmp_gt_i32_e64 s[6:7], 0, v5
	v_and_b32_e32 v5, 0x7f, v4
	v_max_f32_e32 v8, v195, v209
	v_cndmask_b32_e64 v44, v7, v6, s[6:7]
	v_bitop3_b32 v6, v4, s8, v4 bitop3:0xc
	v_cmp_gt_i32_e64 s[6:7], 0, v4
	v_and_b32_e32 v4, 0x7f, v3
	v_max_f32_e32 v63, v182, v183
	v_cndmask_b32_e64 v45, v6, v5, s[6:7]
	v_bitop3_b32 v5, v3, s8, v3 bitop3:0xc
	v_cmp_gt_i32_e64 s[6:7], 0, v3
	v_and_b32_e32 v3, 0x7f, v2
	s_nop 0
	v_cndmask_b32_e64 v46, v5, v4, s[6:7]
	v_bitop3_b32 v4, v2, s8, v2 bitop3:0xc
	v_cmp_gt_i32_e64 s[6:7], 0, v2
	v_and_b32_e32 v2, 0x7f, v1
	s_nop 0
	v_cndmask_b32_e64 v47, v4, v3, s[6:7]
	v_bitop3_b32 v3, v1, s8, v1 bitop3:0xc
	v_cmp_gt_i32_e64 s[6:7], 0, v1
	v_and_b32_e32 v1, 0x7f, v0
	v_max_f32_e32 v4, v51, v50
	v_cndmask_b32_e64 v48, v3, v2, s[6:7]
	v_bitop3_b32 v2, v0, s8, v0 bitop3:0xc
	v_cmp_gt_i32_e64 s[6:7], 0, v0
	v_min_f32_e32 v56, v60, v61
	s_nop 0
	v_cndmask_b32_e64 v49, v2, v1, s[6:7]
	v_cmp_gt_u32_e64 s[6:7], 16, v213
	v_min_f32_e32 v58, v62, v63
	s_nop 0
	v_cndmask_b32_e64 v0, 0, v49, s[6:7]
	v_cmp_eq_u32_e64 s[6:7], 1, v214
	v_max_f32_e32 v60, v60, v61
	v_max_f32_e32 v61, v62, v63
	v_cndmask_b32_e64 v0, v0, v48, s[6:7]
	v_cmp_eq_u32_e64 s[6:7], 2, v214
	v_readlane_b32 s46, v255, 21
	v_readlane_b32 s44, v255, 19
	v_cndmask_b32_e64 v0, v0, v47, s[6:7]
	v_cmp_eq_u32_e64 s[6:7], 3, v214
	v_readlane_b32 s47, v255, 22
	v_readlane_b32 s45, v255, 20
	v_cndmask_b32_e64 v0, v0, v46, s[6:7]
	v_cmp_eq_u32_e64 s[6:7], 4, v214
	s_nop 1
	v_cndmask_b32_e64 v0, v0, v45, s[6:7]
	v_cmp_eq_u32_e64 s[6:7], 5, v214
	s_nop 1
	v_cndmask_b32_e64 v0, v0, v44, s[6:7]
	v_cmp_eq_u32_e64 s[6:7], 6, v214
	s_nop 1
	v_cndmask_b32_e64 v0, v0, v43, s[6:7]
	v_cmp_eq_u32_e64 s[6:7], 7, v214
	s_nop 1
	v_cndmask_b32_e64 v0, v0, v42, s[6:7]
	v_cmp_eq_u32_e64 s[6:7], 8, v214
	s_nop 1
	v_cndmask_b32_e64 v0, v0, v41, s[6:7]
	v_cmp_eq_u32_e64 s[6:7], 9, v214
	s_nop 1
	v_cndmask_b32_e64 v0, v0, v40, s[6:7]
	v_cmp_eq_u32_e64 s[6:7], 10, v214
	s_nop 1
	v_cndmask_b32_e64 v0, v0, v39, s[6:7]
	v_cmp_eq_u32_e64 s[6:7], 11, v214
	s_nop 1
	v_cndmask_b32_e64 v0, v0, v38, s[6:7]
	v_cmp_eq_u32_e64 s[6:7], 12, v214
	s_nop 1
	v_cndmask_b32_e64 v0, v0, v37, s[6:7]
	v_cmp_eq_u32_e64 s[6:7], 13, v214
	s_nop 1
	v_cndmask_b32_e64 v0, v0, v36, s[6:7]
	v_cmp_eq_u32_e64 s[6:7], 14, v214
	s_nop 1
	v_cndmask_b32_e64 v0, v0, v35, s[6:7]
	v_cmp_eq_u32_e64 s[6:7], 15, v214
	s_nop 1
	v_cndmask_b32_e64 v3, v0, v34, s[6:7]
	v_max_f32_e32 v0, v220, v212
	v_and_b32_e32 v1, 0xff, v0
	v_bitop3_b32 v2, v0, s10, v0 bitop3:0xc
	v_cmp_gt_i32_e64 s[6:7], 0, v0
	v_and_b32_e32 v12, 0xffffff00, v0
	v_lshl_add_u32 v3, v3, 7, v16
	v_cndmask_b32_e64 v0, v2, v1, s[6:7]
	v_lshrrev_b32_e32 v1, 4, v0
	v_cmp_gt_u32_e64 s[6:7], 16, v0
	v_and_b32_e32 v0, 15, v0
	s_nop 0
	v_cndmask_b32_e64 v2, 0, v49, s[6:7]
	v_cmp_eq_u32_e64 s[6:7], 1, v1
	s_nop 1
	v_cndmask_b32_e64 v2, v2, v48, s[6:7]
	v_cmp_eq_u32_e64 s[6:7], 2, v1
	s_nop 1
	v_cndmask_b32_e64 v2, v2, v47, s[6:7]
	v_cmp_eq_u32_e64 s[6:7], 3, v1
	s_nop 1
	v_cndmask_b32_e64 v2, v2, v46, s[6:7]
	v_cmp_eq_u32_e64 s[6:7], 4, v1
	s_nop 1
	v_cndmask_b32_e64 v2, v2, v45, s[6:7]
	v_cmp_eq_u32_e64 s[6:7], 5, v1
	s_nop 1
	v_cndmask_b32_e64 v2, v2, v44, s[6:7]
	v_cmp_eq_u32_e64 s[6:7], 6, v1
	s_nop 1
	v_cndmask_b32_e64 v2, v2, v43, s[6:7]
	v_cmp_eq_u32_e64 s[6:7], 7, v1
	s_nop 1
	v_cndmask_b32_e64 v2, v2, v42, s[6:7]
	v_cmp_eq_u32_e64 s[6:7], 8, v1
	s_nop 1
	v_cndmask_b32_e64 v2, v2, v41, s[6:7]
	v_cmp_eq_u32_e64 s[6:7], 9, v1
	s_nop 1
	v_cndmask_b32_e64 v2, v2, v40, s[6:7]
	v_cmp_eq_u32_e64 s[6:7], 10, v1
	s_nop 1
	v_cndmask_b32_e64 v2, v2, v39, s[6:7]
	v_cmp_eq_u32_e64 s[6:7], 11, v1
	s_nop 1
	v_cndmask_b32_e64 v2, v2, v38, s[6:7]
	v_cmp_eq_u32_e64 s[6:7], 12, v1
	s_nop 1
	v_cndmask_b32_e64 v2, v2, v37, s[6:7]
	v_cmp_eq_u32_e64 s[6:7], 13, v1
	s_nop 1
	v_cndmask_b32_e64 v2, v2, v36, s[6:7]
	v_cmp_eq_u32_e64 s[6:7], 14, v1
	s_nop 1
	v_cndmask_b32_e64 v2, v2, v35, s[6:7]
	v_cmp_eq_u32_e64 s[6:7], 15, v1
	s_nop 1
	v_cndmask_b32_e64 v1, v2, v34, s[6:7]
	v_cmp_eq_u32_e64 s[6:7], 0, v0
	s_nop 1
	v_cndmask_b32_e64 v2, 0, v33, s[6:7]
	v_cmp_eq_u32_e64 s[6:7], 1, v0
	s_nop 1
	v_cndmask_b32_e64 v2, v2, v17, s[6:7]
	v_cmp_eq_u32_e64 s[6:7], 2, v0
	s_nop 1
	v_cndmask_b32_e64 v2, v2, v18, s[6:7]
	v_cmp_eq_u32_e64 s[6:7], 3, v0
	s_nop 1
	v_cndmask_b32_e64 v2, v2, v19, s[6:7]
	v_cmp_eq_u32_e64 s[6:7], 4, v0
	s_nop 1
	v_cndmask_b32_e64 v2, v2, v20, s[6:7]
	v_cmp_eq_u32_e64 s[6:7], 5, v0
	s_nop 1
	v_cndmask_b32_e64 v2, v2, v21, s[6:7]
	v_cmp_eq_u32_e64 s[6:7], 6, v0
	s_nop 1
	v_cndmask_b32_e64 v2, v2, v22, s[6:7]
	v_cmp_eq_u32_e64 s[6:7], 7, v0
	s_nop 1
	v_cndmask_b32_e64 v2, v2, v23, s[6:7]
	v_cmp_eq_u32_e64 s[6:7], 8, v0
	s_nop 1
	v_cndmask_b32_e64 v2, v2, v24, s[6:7]
	v_cmp_eq_u32_e64 s[6:7], 9, v0
	s_nop 1
	v_cndmask_b32_e64 v2, v2, v25, s[6:7]
	v_cmp_eq_u32_e64 s[6:7], 10, v0
	s_nop 1
	v_cndmask_b32_e64 v2, v2, v26, s[6:7]
	v_cmp_eq_u32_e64 s[6:7], 11, v0
	s_nop 1
	v_cndmask_b32_e64 v2, v2, v27, s[6:7]
	v_cmp_eq_u32_e64 s[6:7], 12, v0
	s_nop 1
	v_cndmask_b32_e64 v2, v2, v28, s[6:7]
	v_cmp_eq_u32_e64 s[6:7], 13, v0
	s_nop 1
	v_cndmask_b32_e64 v2, v2, v29, s[6:7]
	v_cmp_eq_u32_e64 s[6:7], 14, v0
	s_nop 1
	v_cndmask_b32_e64 v2, v2, v30, s[6:7]
	v_cmp_eq_u32_e64 s[6:7], 15, v0
	s_nop 1
	v_cndmask_b32_e64 v0, v2, v31, s[6:7]
	v_lshl_add_u32 v2, v1, 7, v0
	v_max_f32_e32 v0, v216, v215
	v_min_f32_e32 v1, v0, v4
	v_and_b32_e32 v5, 0xff, v1
	v_bitop3_b32 v6, v1, s10, v1 bitop3:0xc
	v_cmp_gt_i32_e64 s[8:9], 0, v1
	v_and_b32_e32 v50, 0xffffff00, v1
	v_max_f32_e32 v0, v0, v4
	v_cndmask_b32_e64 v1, v6, v5, s[8:9]
	v_lshrrev_b32_e32 v5, 4, v1
	v_cmp_gt_u32_e64 s[8:9], 16, v1
	v_and_b32_e32 v1, 15, v1
	v_and_b32_e32 v4, 0xff, v0
	v_cndmask_b32_e64 v6, 0, v49, s[8:9]
	v_cmp_eq_u32_e64 s[8:9], 1, v5
	v_cmp_gt_i32_e64 s[6:7], 0, v0
	v_and_b32_e32 v51, 0xffffff00, v0
	v_cndmask_b32_e64 v6, v6, v48, s[8:9]
	v_cmp_eq_u32_e64 s[8:9], 2, v5
	s_nop 1
	v_cndmask_b32_e64 v6, v6, v47, s[8:9]
	v_cmp_eq_u32_e64 s[8:9], 3, v5
	s_nop 1
	v_cndmask_b32_e64 v6, v6, v46, s[8:9]
	v_cmp_eq_u32_e64 s[8:9], 4, v5
	s_nop 1
	v_cndmask_b32_e64 v6, v6, v45, s[8:9]
	v_cmp_eq_u32_e64 s[8:9], 5, v5
	s_nop 1
	v_cndmask_b32_e64 v6, v6, v44, s[8:9]
	v_cmp_eq_u32_e64 s[8:9], 6, v5
	s_nop 1
	v_cndmask_b32_e64 v6, v6, v43, s[8:9]
	v_cmp_eq_u32_e64 s[8:9], 7, v5
	s_nop 1
	v_cndmask_b32_e64 v6, v6, v42, s[8:9]
	v_cmp_eq_u32_e64 s[8:9], 8, v5
	s_nop 1
	v_cndmask_b32_e64 v6, v6, v41, s[8:9]
	v_cmp_eq_u32_e64 s[8:9], 9, v5
	s_nop 1
	v_cndmask_b32_e64 v6, v6, v40, s[8:9]
	v_cmp_eq_u32_e64 s[8:9], 10, v5
	s_nop 1
	v_cndmask_b32_e64 v6, v6, v39, s[8:9]
	v_cmp_eq_u32_e64 s[8:9], 11, v5
	s_nop 1
	v_cndmask_b32_e64 v6, v6, v38, s[8:9]
	v_cmp_eq_u32_e64 s[8:9], 12, v5
	s_nop 1
	v_cndmask_b32_e64 v6, v6, v37, s[8:9]
	v_cmp_eq_u32_e64 s[8:9], 13, v5
	s_nop 1
	v_cndmask_b32_e64 v6, v6, v36, s[8:9]
	v_cmp_eq_u32_e64 s[8:9], 14, v5
	s_nop 1
	v_cndmask_b32_e64 v6, v6, v35, s[8:9]
	v_cmp_eq_u32_e64 s[8:9], 15, v5
	s_nop 1
	v_cndmask_b32_e64 v5, v6, v34, s[8:9]
	v_cmp_eq_u32_e64 s[8:9], 0, v1
	s_nop 1
	v_cndmask_b32_e64 v6, 0, v33, s[8:9]
	v_cmp_eq_u32_e64 s[8:9], 1, v1
	s_nop 1
	v_cndmask_b32_e64 v6, v6, v17, s[8:9]
	v_cmp_eq_u32_e64 s[8:9], 2, v1
	s_nop 1
	v_cndmask_b32_e64 v6, v6, v18, s[8:9]
	v_cmp_eq_u32_e64 s[8:9], 3, v1
	s_nop 1
	v_cndmask_b32_e64 v6, v6, v19, s[8:9]
	v_cmp_eq_u32_e64 s[8:9], 4, v1
	s_nop 1
	v_cndmask_b32_e64 v6, v6, v20, s[8:9]
	v_cmp_eq_u32_e64 s[8:9], 5, v1
	s_nop 1
	v_cndmask_b32_e64 v6, v6, v21, s[8:9]
	v_cmp_eq_u32_e64 s[8:9], 6, v1
	s_nop 1
	v_cndmask_b32_e64 v6, v6, v22, s[8:9]
	v_cmp_eq_u32_e64 s[8:9], 7, v1
	s_nop 1
	v_cndmask_b32_e64 v6, v6, v23, s[8:9]
	v_cmp_eq_u32_e64 s[8:9], 8, v1
	s_nop 1
	v_cndmask_b32_e64 v6, v6, v24, s[8:9]
	v_cmp_eq_u32_e64 s[8:9], 9, v1
	s_nop 1
	v_cndmask_b32_e64 v6, v6, v25, s[8:9]
	v_cmp_eq_u32_e64 s[8:9], 10, v1
	s_nop 1
	v_cndmask_b32_e64 v6, v6, v26, s[8:9]
	v_cmp_eq_u32_e64 s[8:9], 11, v1
	s_nop 1
	v_cndmask_b32_e64 v6, v6, v27, s[8:9]
	v_cmp_eq_u32_e64 s[8:9], 12, v1
	s_nop 1
	v_cndmask_b32_e64 v6, v6, v28, s[8:9]
	v_cmp_eq_u32_e64 s[8:9], 13, v1
	s_nop 1
	v_cndmask_b32_e64 v6, v6, v29, s[8:9]
	v_cmp_eq_u32_e64 s[8:9], 14, v1
	s_nop 1
	v_cndmask_b32_e64 v6, v6, v30, s[8:9]
	v_cmp_eq_u32_e64 s[8:9], 15, v1
	s_nop 1
	v_cndmask_b32_e64 v1, v6, v31, s[8:9]
	v_lshl_add_u32 v1, v5, 7, v1
	v_bitop3_b32 v5, v0, s10, v0 bitop3:0xc
	v_cndmask_b32_e64 v0, v5, v4, s[6:7]
	v_lshrrev_b32_e32 v4, 4, v0
	v_cmp_gt_u32_e64 s[6:7], 16, v0
	v_and_b32_e32 v0, 15, v0
	s_nop 0
	v_cndmask_b32_e64 v5, 0, v49, s[6:7]
	v_cmp_eq_u32_e64 s[6:7], 1, v4
	s_nop 1
	v_cndmask_b32_e64 v5, v5, v48, s[6:7]
	v_cmp_eq_u32_e64 s[6:7], 2, v4
	s_nop 1
	v_cndmask_b32_e64 v5, v5, v47, s[6:7]
	v_cmp_eq_u32_e64 s[6:7], 3, v4
	s_nop 1
	v_cndmask_b32_e64 v5, v5, v46, s[6:7]
	v_cmp_eq_u32_e64 s[6:7], 4, v4
	s_nop 1
	v_cndmask_b32_e64 v5, v5, v45, s[6:7]
	v_cmp_eq_u32_e64 s[6:7], 5, v4
	s_nop 1
	v_cndmask_b32_e64 v5, v5, v44, s[6:7]
	v_cmp_eq_u32_e64 s[6:7], 6, v4
	s_nop 1
	v_cndmask_b32_e64 v5, v5, v43, s[6:7]
	v_cmp_eq_u32_e64 s[6:7], 7, v4
	s_nop 1
	v_cndmask_b32_e64 v5, v5, v42, s[6:7]
	v_cmp_eq_u32_e64 s[6:7], 8, v4
	s_nop 1
	v_cndmask_b32_e64 v5, v5, v41, s[6:7]
	v_cmp_eq_u32_e64 s[6:7], 9, v4
	s_nop 1
	v_cndmask_b32_e64 v5, v5, v40, s[6:7]
	v_cmp_eq_u32_e64 s[6:7], 10, v4
	s_nop 1
	v_cndmask_b32_e64 v5, v5, v39, s[6:7]
	v_cmp_eq_u32_e64 s[6:7], 11, v4
	s_nop 1
	v_cndmask_b32_e64 v5, v5, v38, s[6:7]
	v_cmp_eq_u32_e64 s[6:7], 12, v4
	s_nop 1
	v_cndmask_b32_e64 v5, v5, v37, s[6:7]
	v_cmp_eq_u32_e64 s[6:7], 13, v4
	s_nop 1
	v_cndmask_b32_e64 v5, v5, v36, s[6:7]
	v_cmp_eq_u32_e64 s[6:7], 14, v4
	s_nop 1
	v_cndmask_b32_e64 v5, v5, v35, s[6:7]
	v_cmp_eq_u32_e64 s[6:7], 15, v4
	s_nop 1
	v_cndmask_b32_e64 v4, v5, v34, s[6:7]
	v_cmp_eq_u32_e64 s[6:7], 0, v0
	s_nop 1
	v_cndmask_b32_e64 v5, 0, v33, s[6:7]
	v_cmp_eq_u32_e64 s[6:7], 1, v0
	s_nop 1
	v_cndmask_b32_e64 v5, v5, v17, s[6:7]
	v_cmp_eq_u32_e64 s[6:7], 2, v0
	s_nop 1
	v_cndmask_b32_e64 v5, v5, v18, s[6:7]
	v_cmp_eq_u32_e64 s[6:7], 3, v0
	s_nop 1
	v_cndmask_b32_e64 v5, v5, v19, s[6:7]
	v_cmp_eq_u32_e64 s[6:7], 4, v0
	s_nop 1
	v_cndmask_b32_e64 v5, v5, v20, s[6:7]
	v_cmp_eq_u32_e64 s[6:7], 5, v0
	s_nop 1
	v_cndmask_b32_e64 v5, v5, v21, s[6:7]
	v_cmp_eq_u32_e64 s[6:7], 6, v0
	s_nop 1
	v_cndmask_b32_e64 v5, v5, v22, s[6:7]
	v_cmp_eq_u32_e64 s[6:7], 7, v0
	s_nop 1
	v_cndmask_b32_e64 v5, v5, v23, s[6:7]
	v_cmp_eq_u32_e64 s[6:7], 8, v0
	s_nop 1
	v_cndmask_b32_e64 v5, v5, v24, s[6:7]
	v_cmp_eq_u32_e64 s[6:7], 9, v0
	s_nop 1
	v_cndmask_b32_e64 v5, v5, v25, s[6:7]
	v_cmp_eq_u32_e64 s[6:7], 10, v0
	s_nop 1
	v_cndmask_b32_e64 v5, v5, v26, s[6:7]
	v_cmp_eq_u32_e64 s[6:7], 11, v0
	s_nop 1
	v_cndmask_b32_e64 v5, v5, v27, s[6:7]
	v_cmp_eq_u32_e64 s[6:7], 12, v0
	s_nop 1
	v_cndmask_b32_e64 v5, v5, v28, s[6:7]
	v_cmp_eq_u32_e64 s[6:7], 13, v0
	s_nop 1
	v_cndmask_b32_e64 v5, v5, v29, s[6:7]
	v_cmp_eq_u32_e64 s[6:7], 14, v0
	s_nop 1
	v_cndmask_b32_e64 v5, v5, v30, s[6:7]
	v_cmp_eq_u32_e64 s[6:7], 15, v0
	s_nop 1
	v_cndmask_b32_e64 v0, v5, v31, s[6:7]
	v_lshl_add_u32 v0, v4, 7, v0
	v_max_f32_e32 v4, v52, v190
	v_max_f32_e32 v5, v53, v57
	v_min_f32_e32 v6, v4, v5
	v_min_f32_e32 v10, v8, v9
	v_max_f32_e32 v4, v4, v5
	v_max_f32_e32 v8, v8, v9
	v_min_f32_e32 v7, v6, v10
	v_and_b32_e32 v11, 0xff, v7
	v_bitop3_b32 v13, v7, s10, v7 bitop3:0xc
	v_cmp_gt_i32_e64 s[8:9], 0, v7
	v_and_b32_e32 v52, 0xffffff00, v7
	v_max_f32_e32 v6, v6, v10
	v_cndmask_b32_e64 v7, v13, v11, s[8:9]
	v_lshrrev_b32_e32 v11, 4, v7
	v_cmp_gt_u32_e64 s[8:9], 16, v7
	v_and_b32_e32 v7, 15, v7
	v_and_b32_e32 v10, 0xff, v6
	v_cndmask_b32_e64 v13, 0, v49, s[8:9]
	v_cmp_eq_u32_e64 s[8:9], 1, v11
	v_cmp_gt_i32_e64 s[6:7], 0, v6
	v_and_b32_e32 v53, 0xffffff00, v6
	v_cndmask_b32_e64 v13, v13, v48, s[8:9]
	v_cmp_eq_u32_e64 s[8:9], 2, v11
	s_nop 1
	v_cndmask_b32_e64 v13, v13, v47, s[8:9]
	v_cmp_eq_u32_e64 s[8:9], 3, v11
	s_nop 1
	v_cndmask_b32_e64 v13, v13, v46, s[8:9]
	v_cmp_eq_u32_e64 s[8:9], 4, v11
	s_nop 1
	v_cndmask_b32_e64 v13, v13, v45, s[8:9]
	v_cmp_eq_u32_e64 s[8:9], 5, v11
	s_nop 1
	v_cndmask_b32_e64 v13, v13, v44, s[8:9]
	v_cmp_eq_u32_e64 s[8:9], 6, v11
	s_nop 1
	v_cndmask_b32_e64 v13, v13, v43, s[8:9]
	v_cmp_eq_u32_e64 s[8:9], 7, v11
	s_nop 1
	v_cndmask_b32_e64 v13, v13, v42, s[8:9]
	v_cmp_eq_u32_e64 s[8:9], 8, v11
	s_nop 1
	v_cndmask_b32_e64 v13, v13, v41, s[8:9]
	v_cmp_eq_u32_e64 s[8:9], 9, v11
	s_nop 1
	v_cndmask_b32_e64 v13, v13, v40, s[8:9]
	v_cmp_eq_u32_e64 s[8:9], 10, v11
	s_nop 1
	v_cndmask_b32_e64 v13, v13, v39, s[8:9]
	v_cmp_eq_u32_e64 s[8:9], 11, v11
	s_nop 1
	v_cndmask_b32_e64 v13, v13, v38, s[8:9]
	v_cmp_eq_u32_e64 s[8:9], 12, v11
	s_nop 1
	v_cndmask_b32_e64 v13, v13, v37, s[8:9]
	v_cmp_eq_u32_e64 s[8:9], 13, v11
	s_nop 1
	v_cndmask_b32_e64 v13, v13, v36, s[8:9]
	v_cmp_eq_u32_e64 s[8:9], 14, v11
	s_nop 1
	v_cndmask_b32_e64 v13, v13, v35, s[8:9]
	v_cmp_eq_u32_e64 s[8:9], 15, v11
	s_nop 1
	v_cndmask_b32_e64 v11, v13, v34, s[8:9]
	v_cmp_eq_u32_e64 s[8:9], 0, v7
	s_nop 1
	v_cndmask_b32_e64 v13, 0, v33, s[8:9]
	v_cmp_eq_u32_e64 s[8:9], 1, v7
	s_nop 1
	v_cndmask_b32_e64 v13, v13, v17, s[8:9]
	v_cmp_eq_u32_e64 s[8:9], 2, v7
	s_nop 1
	v_cndmask_b32_e64 v13, v13, v18, s[8:9]
	v_cmp_eq_u32_e64 s[8:9], 3, v7
	s_nop 1
	v_cndmask_b32_e64 v13, v13, v19, s[8:9]
	v_cmp_eq_u32_e64 s[8:9], 4, v7
	s_nop 1
	v_cndmask_b32_e64 v13, v13, v20, s[8:9]
	v_cmp_eq_u32_e64 s[8:9], 5, v7
	s_nop 1
	v_cndmask_b32_e64 v13, v13, v21, s[8:9]
	v_cmp_eq_u32_e64 s[8:9], 6, v7
	s_nop 1
	v_cndmask_b32_e64 v13, v13, v22, s[8:9]
	v_cmp_eq_u32_e64 s[8:9], 7, v7
	s_nop 1
	v_cndmask_b32_e64 v13, v13, v23, s[8:9]
	v_cmp_eq_u32_e64 s[8:9], 8, v7
	s_nop 1
	v_cndmask_b32_e64 v13, v13, v24, s[8:9]
	v_cmp_eq_u32_e64 s[8:9], 9, v7
	s_nop 1
	v_cndmask_b32_e64 v13, v13, v25, s[8:9]
	v_cmp_eq_u32_e64 s[8:9], 10, v7
	s_nop 1
	v_cndmask_b32_e64 v13, v13, v26, s[8:9]
	v_cmp_eq_u32_e64 s[8:9], 11, v7
	s_nop 1
	v_cndmask_b32_e64 v13, v13, v27, s[8:9]
	v_cmp_eq_u32_e64 s[8:9], 12, v7
	s_nop 1
	v_cndmask_b32_e64 v13, v13, v28, s[8:9]
	v_cmp_eq_u32_e64 s[8:9], 13, v7
	s_nop 1
	v_cndmask_b32_e64 v13, v13, v29, s[8:9]
	v_cmp_eq_u32_e64 s[8:9], 14, v7
	s_nop 1
	v_cndmask_b32_e64 v13, v13, v30, s[8:9]
	v_cmp_eq_u32_e64 s[8:9], 15, v7
	s_nop 1
	v_cndmask_b32_e64 v7, v13, v31, s[8:9]
	v_lshl_add_u32 v7, v11, 7, v7
	v_bitop3_b32 v11, v6, s10, v6 bitop3:0xc
	v_cndmask_b32_e64 v6, v11, v10, s[6:7]
	v_lshrrev_b32_e32 v10, 4, v6
	v_cmp_gt_u32_e64 s[6:7], 16, v6
	v_and_b32_e32 v6, 15, v6
	v_max_f32_e32 v13, v54, v55
	v_cndmask_b32_e64 v11, 0, v49, s[6:7]
	v_cmp_eq_u32_e64 s[6:7], 1, v10
	v_min_f32_e32 v55, v56, v58
	s_nop 0
	v_cndmask_b32_e64 v11, v11, v48, s[6:7]
	v_cmp_eq_u32_e64 s[6:7], 2, v10
	v_max_f32_e32 v58, v56, v58
	s_nop 0
	v_cndmask_b32_e64 v11, v11, v47, s[6:7]
	v_cmp_eq_u32_e64 s[6:7], 3, v10
	s_nop 1
	v_cndmask_b32_e64 v11, v11, v46, s[6:7]
	v_cmp_eq_u32_e64 s[6:7], 4, v10
	s_nop 1
	v_cndmask_b32_e64 v11, v11, v45, s[6:7]
	v_cmp_eq_u32_e64 s[6:7], 5, v10
	s_nop 1
	v_cndmask_b32_e64 v11, v11, v44, s[6:7]
	v_cmp_eq_u32_e64 s[6:7], 6, v10
	s_nop 1
	v_cndmask_b32_e64 v11, v11, v43, s[6:7]
	v_cmp_eq_u32_e64 s[6:7], 7, v10
	s_nop 1
	v_cndmask_b32_e64 v11, v11, v42, s[6:7]
	v_cmp_eq_u32_e64 s[6:7], 8, v10
	s_nop 1
	v_cndmask_b32_e64 v11, v11, v41, s[6:7]
	v_cmp_eq_u32_e64 s[6:7], 9, v10
	s_nop 1
	v_cndmask_b32_e64 v11, v11, v40, s[6:7]
	v_cmp_eq_u32_e64 s[6:7], 10, v10
	s_nop 1
	v_cndmask_b32_e64 v11, v11, v39, s[6:7]
	v_cmp_eq_u32_e64 s[6:7], 11, v10
	s_nop 1
	v_cndmask_b32_e64 v11, v11, v38, s[6:7]
	v_cmp_eq_u32_e64 s[6:7], 12, v10
	s_nop 1
	v_cndmask_b32_e64 v11, v11, v37, s[6:7]
	v_cmp_eq_u32_e64 s[6:7], 13, v10
	s_nop 1
	v_cndmask_b32_e64 v11, v11, v36, s[6:7]
	v_cmp_eq_u32_e64 s[6:7], 14, v10
	s_nop 1
	v_cndmask_b32_e64 v11, v11, v35, s[6:7]
	v_cmp_eq_u32_e64 s[6:7], 15, v10
	s_nop 1
	v_cndmask_b32_e64 v10, v11, v34, s[6:7]
	v_cmp_eq_u32_e64 s[6:7], 0, v6
	s_nop 1
	v_cndmask_b32_e64 v11, 0, v33, s[6:7]
	v_cmp_eq_u32_e64 s[6:7], 1, v6
	s_nop 1
	v_cndmask_b32_e64 v11, v11, v17, s[6:7]
	v_cmp_eq_u32_e64 s[6:7], 2, v6
	s_nop 1
	v_cndmask_b32_e64 v11, v11, v18, s[6:7]
	v_cmp_eq_u32_e64 s[6:7], 3, v6
	s_nop 1
	v_cndmask_b32_e64 v11, v11, v19, s[6:7]
	v_cmp_eq_u32_e64 s[6:7], 4, v6
	s_nop 1
	v_cndmask_b32_e64 v11, v11, v20, s[6:7]
	v_cmp_eq_u32_e64 s[6:7], 5, v6
	s_nop 1
	v_cndmask_b32_e64 v11, v11, v21, s[6:7]
	v_cmp_eq_u32_e64 s[6:7], 6, v6
	s_nop 1
	v_cndmask_b32_e64 v11, v11, v22, s[6:7]
	v_cmp_eq_u32_e64 s[6:7], 7, v6
	s_nop 1
	v_cndmask_b32_e64 v11, v11, v23, s[6:7]
	v_cmp_eq_u32_e64 s[6:7], 8, v6
	s_nop 1
	v_cndmask_b32_e64 v11, v11, v24, s[6:7]
	v_cmp_eq_u32_e64 s[6:7], 9, v6
	s_nop 1
	v_cndmask_b32_e64 v11, v11, v25, s[6:7]
	v_cmp_eq_u32_e64 s[6:7], 10, v6
	s_nop 1
	v_cndmask_b32_e64 v11, v11, v26, s[6:7]
	v_cmp_eq_u32_e64 s[6:7], 11, v6
	s_nop 1
	v_cndmask_b32_e64 v11, v11, v27, s[6:7]
	v_cmp_eq_u32_e64 s[6:7], 12, v6
	s_nop 1
	v_cndmask_b32_e64 v11, v11, v28, s[6:7]
	v_cmp_eq_u32_e64 s[6:7], 13, v6
	s_nop 1
	v_cndmask_b32_e64 v11, v11, v29, s[6:7]
	v_cmp_eq_u32_e64 s[6:7], 14, v6
	s_nop 1
	v_cndmask_b32_e64 v11, v11, v30, s[6:7]
	v_cmp_eq_u32_e64 s[6:7], 15, v6
	s_nop 1
	v_cndmask_b32_e64 v6, v11, v31, s[6:7]
	v_lshl_add_u32 v6, v10, 7, v6
	v_min_f32_e32 v5, v4, v8
	v_and_b32_e32 v9, 0xff, v5
	v_bitop3_b32 v10, v5, s10, v5 bitop3:0xc
	v_cmp_gt_i32_e64 s[8:9], 0, v5
	v_and_b32_e32 v57, 0xffffff00, v5
	v_max_f32_e32 v4, v4, v8
	v_cndmask_b32_e64 v5, v10, v9, s[8:9]
	v_lshrrev_b32_e32 v9, 4, v5
	v_cmp_gt_u32_e64 s[8:9], 16, v5
	v_and_b32_e32 v5, 15, v5
	v_and_b32_e32 v8, 0xff, v4
	v_cndmask_b32_e64 v10, 0, v49, s[8:9]
	v_cmp_eq_u32_e64 s[8:9], 1, v9
	v_cmp_gt_i32_e64 s[6:7], 0, v4
	v_and_b32_e32 v209, 0xffffff00, v4
	v_cndmask_b32_e64 v10, v10, v48, s[8:9]
	v_cmp_eq_u32_e64 s[8:9], 2, v9
	s_nop 1
	v_cndmask_b32_e64 v10, v10, v47, s[8:9]
	v_cmp_eq_u32_e64 s[8:9], 3, v9
	s_nop 1
	v_cndmask_b32_e64 v10, v10, v46, s[8:9]
	v_cmp_eq_u32_e64 s[8:9], 4, v9
	s_nop 1
	v_cndmask_b32_e64 v10, v10, v45, s[8:9]
	v_cmp_eq_u32_e64 s[8:9], 5, v9
	s_nop 1
	v_cndmask_b32_e64 v10, v10, v44, s[8:9]
	v_cmp_eq_u32_e64 s[8:9], 6, v9
	s_nop 1
	v_cndmask_b32_e64 v10, v10, v43, s[8:9]
	v_cmp_eq_u32_e64 s[8:9], 7, v9
	s_nop 1
	v_cndmask_b32_e64 v10, v10, v42, s[8:9]
	v_cmp_eq_u32_e64 s[8:9], 8, v9
	s_nop 1
	v_cndmask_b32_e64 v10, v10, v41, s[8:9]
	v_cmp_eq_u32_e64 s[8:9], 9, v9
	s_nop 1
	v_cndmask_b32_e64 v10, v10, v40, s[8:9]
	v_cmp_eq_u32_e64 s[8:9], 10, v9
	s_nop 1
	v_cndmask_b32_e64 v10, v10, v39, s[8:9]
	v_cmp_eq_u32_e64 s[8:9], 11, v9
	s_nop 1
	v_cndmask_b32_e64 v10, v10, v38, s[8:9]
	v_cmp_eq_u32_e64 s[8:9], 12, v9
	s_nop 1
	v_cndmask_b32_e64 v10, v10, v37, s[8:9]
	v_cmp_eq_u32_e64 s[8:9], 13, v9
	s_nop 1
	v_cndmask_b32_e64 v10, v10, v36, s[8:9]
	v_cmp_eq_u32_e64 s[8:9], 14, v9
	s_nop 1
	v_cndmask_b32_e64 v10, v10, v35, s[8:9]
	v_cmp_eq_u32_e64 s[8:9], 15, v9
	s_nop 1
	v_cndmask_b32_e64 v9, v10, v34, s[8:9]
	v_cmp_eq_u32_e64 s[8:9], 0, v5
	s_nop 1
	v_cndmask_b32_e64 v10, 0, v33, s[8:9]
	v_cmp_eq_u32_e64 s[8:9], 1, v5
	s_nop 1
	v_cndmask_b32_e64 v10, v10, v17, s[8:9]
	v_cmp_eq_u32_e64 s[8:9], 2, v5
	s_nop 1
	v_cndmask_b32_e64 v10, v10, v18, s[8:9]
	v_cmp_eq_u32_e64 s[8:9], 3, v5
	s_nop 1
	v_cndmask_b32_e64 v10, v10, v19, s[8:9]
	v_cmp_eq_u32_e64 s[8:9], 4, v5
	s_nop 1
	v_cndmask_b32_e64 v10, v10, v20, s[8:9]
	v_cmp_eq_u32_e64 s[8:9], 5, v5
	s_nop 1
	v_cndmask_b32_e64 v10, v10, v21, s[8:9]
	v_cmp_eq_u32_e64 s[8:9], 6, v5
	s_nop 1
	v_cndmask_b32_e64 v10, v10, v22, s[8:9]
	v_cmp_eq_u32_e64 s[8:9], 7, v5
	s_nop 1
	v_cndmask_b32_e64 v10, v10, v23, s[8:9]
	v_cmp_eq_u32_e64 s[8:9], 8, v5
	s_nop 1
	v_cndmask_b32_e64 v10, v10, v24, s[8:9]
	v_cmp_eq_u32_e64 s[8:9], 9, v5
	s_nop 1
	v_cndmask_b32_e64 v10, v10, v25, s[8:9]
	v_cmp_eq_u32_e64 s[8:9], 10, v5
	s_nop 1
	v_cndmask_b32_e64 v10, v10, v26, s[8:9]
	v_cmp_eq_u32_e64 s[8:9], 11, v5
	s_nop 1
	v_cndmask_b32_e64 v10, v10, v27, s[8:9]
	v_cmp_eq_u32_e64 s[8:9], 12, v5
	s_nop 1
	v_cndmask_b32_e64 v10, v10, v28, s[8:9]
	v_cmp_eq_u32_e64 s[8:9], 13, v5
	s_nop 1
	v_cndmask_b32_e64 v10, v10, v29, s[8:9]
	v_cmp_eq_u32_e64 s[8:9], 14, v5
	s_nop 1
	v_cndmask_b32_e64 v10, v10, v30, s[8:9]
	v_cmp_eq_u32_e64 s[8:9], 15, v5
	s_nop 1
	v_cndmask_b32_e64 v5, v10, v31, s[8:9]
	v_lshl_add_u32 v5, v9, 7, v5
	v_bitop3_b32 v9, v4, s10, v4 bitop3:0xc
	v_cndmask_b32_e64 v4, v9, v8, s[6:7]
	v_lshrrev_b32_e32 v8, 4, v4
	v_cmp_gt_u32_e64 s[6:7], 16, v4
	v_and_b32_e32 v4, 15, v4
	s_nop 0
	v_cndmask_b32_e64 v9, 0, v49, s[6:7]
	v_cmp_eq_u32_e64 s[6:7], 1, v8
	s_nop 1
	v_cndmask_b32_e64 v9, v9, v48, s[6:7]
	v_cmp_eq_u32_e64 s[6:7], 2, v8
	s_nop 1
	v_cndmask_b32_e64 v9, v9, v47, s[6:7]
	v_cmp_eq_u32_e64 s[6:7], 3, v8
	s_nop 1
	v_cndmask_b32_e64 v9, v9, v46, s[6:7]
	v_cmp_eq_u32_e64 s[6:7], 4, v8
	s_nop 1
	v_cndmask_b32_e64 v9, v9, v45, s[6:7]
	v_cmp_eq_u32_e64 s[6:7], 5, v8
	s_nop 1
	v_cndmask_b32_e64 v9, v9, v44, s[6:7]
	v_cmp_eq_u32_e64 s[6:7], 6, v8
	s_nop 1
	v_cndmask_b32_e64 v9, v9, v43, s[6:7]
	v_cmp_eq_u32_e64 s[6:7], 7, v8
	s_nop 1
	v_cndmask_b32_e64 v9, v9, v42, s[6:7]
	v_cmp_eq_u32_e64 s[6:7], 8, v8
	s_nop 1
	v_cndmask_b32_e64 v9, v9, v41, s[6:7]
	v_cmp_eq_u32_e64 s[6:7], 9, v8
	s_nop 1
	v_cndmask_b32_e64 v9, v9, v40, s[6:7]
	v_cmp_eq_u32_e64 s[6:7], 10, v8
	s_nop 1
	v_cndmask_b32_e64 v9, v9, v39, s[6:7]
	v_cmp_eq_u32_e64 s[6:7], 11, v8
	s_nop 1
	v_cndmask_b32_e64 v9, v9, v38, s[6:7]
	v_cmp_eq_u32_e64 s[6:7], 12, v8
	s_nop 1
	v_cndmask_b32_e64 v9, v9, v37, s[6:7]
	v_cmp_eq_u32_e64 s[6:7], 13, v8
	s_nop 1
	v_cndmask_b32_e64 v9, v9, v36, s[6:7]
	v_cmp_eq_u32_e64 s[6:7], 14, v8
	s_nop 1
	v_cndmask_b32_e64 v9, v9, v35, s[6:7]
	v_cmp_eq_u32_e64 s[6:7], 15, v8
	s_nop 1
	v_cndmask_b32_e64 v8, v9, v34, s[6:7]
	v_cmp_eq_u32_e64 s[6:7], 0, v4
	s_nop 1
	v_cndmask_b32_e64 v9, 0, v33, s[6:7]
	v_cmp_eq_u32_e64 s[6:7], 1, v4
	s_nop 1
	v_cndmask_b32_e64 v9, v9, v17, s[6:7]
	v_cmp_eq_u32_e64 s[6:7], 2, v4
	s_nop 1
	v_cndmask_b32_e64 v9, v9, v18, s[6:7]
	v_cmp_eq_u32_e64 s[6:7], 3, v4
	s_nop 1
	v_cndmask_b32_e64 v9, v9, v19, s[6:7]
	v_cmp_eq_u32_e64 s[6:7], 4, v4
	s_nop 1
	v_cndmask_b32_e64 v9, v9, v20, s[6:7]
	v_cmp_eq_u32_e64 s[6:7], 5, v4
	s_nop 1
	v_cndmask_b32_e64 v9, v9, v21, s[6:7]
	v_cmp_eq_u32_e64 s[6:7], 6, v4
	s_nop 1
	v_cndmask_b32_e64 v9, v9, v22, s[6:7]
	v_cmp_eq_u32_e64 s[6:7], 7, v4
	s_nop 1
	v_cndmask_b32_e64 v9, v9, v23, s[6:7]
	v_cmp_eq_u32_e64 s[6:7], 8, v4
	s_nop 1
	v_cndmask_b32_e64 v9, v9, v24, s[6:7]
	v_cmp_eq_u32_e64 s[6:7], 9, v4
	s_nop 1
	v_cndmask_b32_e64 v9, v9, v25, s[6:7]
	v_cmp_eq_u32_e64 s[6:7], 10, v4
	s_nop 1
	v_cndmask_b32_e64 v9, v9, v26, s[6:7]
	v_cmp_eq_u32_e64 s[6:7], 11, v4
	s_nop 1
	v_cndmask_b32_e64 v9, v9, v27, s[6:7]
	v_cmp_eq_u32_e64 s[6:7], 12, v4
	s_nop 1
	v_cndmask_b32_e64 v9, v9, v28, s[6:7]
	v_cmp_eq_u32_e64 s[6:7], 13, v4
	s_nop 1
	v_cndmask_b32_e64 v9, v9, v29, s[6:7]
	v_cmp_eq_u32_e64 s[6:7], 14, v4
	s_nop 1
	v_cndmask_b32_e64 v9, v9, v30, s[6:7]
	v_cmp_eq_u32_e64 s[6:7], 15, v4
	s_nop 1
	v_cndmask_b32_e64 v4, v9, v31, s[6:7]
	v_lshl_add_u32 v4, v8, 7, v4
	v_min_f32_e32 v8, v13, v14
	v_min_f32_e32 v9, v15, v59
	v_max_f32_e32 v13, v13, v14
	v_max_f32_e32 v59, v15, v59
	v_min_f32_e32 v10, v8, v9
	v_max_f32_e32 v8, v8, v9
	v_min_f32_e32 v11, v10, v55
	v_and_b32_e32 v173, 0xff, v11
	v_bitop3_b32 v178, v11, s10, v11 bitop3:0xc
	v_cmp_gt_i32_e64 s[8:9], 0, v11
	v_and_b32_e32 v54, 0xffffff00, v11
	v_max_f32_e32 v10, v10, v55
	v_cndmask_b32_e64 v11, v178, v173, s[8:9]
	v_lshrrev_b32_e32 v173, 4, v11
	v_cmp_gt_u32_e64 s[8:9], 16, v11
	v_and_b32_e32 v11, 15, v11
	v_cmp_gt_i32_e64 s[6:7], 0, v10
	v_cndmask_b32_e64 v178, 0, v49, s[8:9]
	v_cmp_eq_u32_e64 s[8:9], 1, v173
	v_and_b32_e32 v55, 0xffffff00, v10
	s_nop 0
	v_cndmask_b32_e64 v178, v178, v48, s[8:9]
	v_cmp_eq_u32_e64 s[8:9], 2, v173
	v_min_f32_e32 v14, v13, v59
	v_min_f32_e32 v62, v60, v61
	v_cndmask_b32_e64 v178, v178, v47, s[8:9]
	v_cmp_eq_u32_e64 s[8:9], 3, v173
	v_max_f32_e32 v59, v13, v59
	v_max_f32_e32 v60, v60, v61
	v_cndmask_b32_e64 v178, v178, v46, s[8:9]
	v_cmp_eq_u32_e64 s[8:9], 4, v173
	s_nop 0
	s_nop 0
	v_cndmask_b32_e64 v178, v178, v45, s[8:9]
	v_cmp_eq_u32_e64 s[8:9], 5, v173
	v_min_f32_e32 v13, v59, v60
	v_and_b32_e32 v61, 0xffffff00, v13
	v_cndmask_b32_e64 v178, v178, v44, s[8:9]
	v_cmp_eq_u32_e64 s[8:9], 6, v173
	v_max_f32_e32 v59, v59, v60
	v_cmp_gt_i32_e32 vcc, 0, v59
	v_cndmask_b32_e64 v178, v178, v43, s[8:9]
	v_cmp_eq_u32_e64 s[8:9], 7, v173
	v_and_b32_e32 v60, 0xffffff00, v59
	v_sub_f32_e32 v12, v12, v60
	v_cndmask_b32_e64 v178, v178, v42, s[8:9]
	v_cmp_eq_u32_e64 s[8:9], 8, v173
	v_mul_f32_e32 v12, 0x3fb8aa3b, v12
	s_nop 0
	v_cndmask_b32_e64 v178, v178, v41, s[8:9]
	v_cmp_eq_u32_e64 s[8:9], 9, v173
	s_nop 1
	v_cndmask_b32_e64 v178, v178, v40, s[8:9]
	v_cmp_eq_u32_e64 s[8:9], 10, v173
	s_nop 1
	v_cndmask_b32_e64 v178, v178, v39, s[8:9]
	v_cmp_eq_u32_e64 s[8:9], 11, v173
	s_nop 1
	v_cndmask_b32_e64 v178, v178, v38, s[8:9]
	v_cmp_eq_u32_e64 s[8:9], 12, v173
	s_nop 1
	v_cndmask_b32_e64 v178, v178, v37, s[8:9]
	v_cmp_eq_u32_e64 s[8:9], 13, v173
	s_nop 1
	v_cndmask_b32_e64 v178, v178, v36, s[8:9]
	v_cmp_eq_u32_e64 s[8:9], 14, v173
	s_nop 1
	v_cndmask_b32_e64 v178, v178, v35, s[8:9]
	v_cmp_eq_u32_e64 s[8:9], 15, v173
	s_nop 1
	v_cndmask_b32_e64 v173, v178, v34, s[8:9]
	v_cmp_eq_u32_e64 s[8:9], 0, v11
	s_nop 1
	v_cndmask_b32_e64 v178, 0, v33, s[8:9]
	v_cmp_eq_u32_e64 s[8:9], 1, v11
	s_nop 1
	v_cndmask_b32_e64 v178, v178, v17, s[8:9]
	v_cmp_eq_u32_e64 s[8:9], 2, v11
	s_nop 1
	v_cndmask_b32_e64 v178, v178, v18, s[8:9]
	v_cmp_eq_u32_e64 s[8:9], 3, v11
	s_nop 1
	v_cndmask_b32_e64 v178, v178, v19, s[8:9]
	v_cmp_eq_u32_e64 s[8:9], 4, v11
	s_nop 1
	v_cndmask_b32_e64 v178, v178, v20, s[8:9]
	v_cmp_eq_u32_e64 s[8:9], 5, v11
	s_nop 1
	v_cndmask_b32_e64 v178, v178, v21, s[8:9]
	v_cmp_eq_u32_e64 s[8:9], 6, v11
	s_nop 1
	v_cndmask_b32_e64 v178, v178, v22, s[8:9]
	v_cmp_eq_u32_e64 s[8:9], 7, v11
	s_nop 1
	v_cndmask_b32_e64 v178, v178, v23, s[8:9]
	v_cmp_eq_u32_e64 s[8:9], 8, v11
	s_nop 1
	v_cndmask_b32_e64 v178, v178, v24, s[8:9]
	v_cmp_eq_u32_e64 s[8:9], 9, v11
	s_nop 1
	v_cndmask_b32_e64 v178, v178, v25, s[8:9]
	v_cmp_eq_u32_e64 s[8:9], 10, v11
	s_nop 1
	v_cndmask_b32_e64 v178, v178, v26, s[8:9]
	v_cmp_eq_u32_e64 s[8:9], 11, v11
	s_nop 1
	v_cndmask_b32_e64 v178, v178, v27, s[8:9]
	v_cmp_eq_u32_e64 s[8:9], 12, v11
	s_nop 1
	v_cndmask_b32_e64 v178, v178, v28, s[8:9]
	v_cmp_eq_u32_e64 s[8:9], 13, v11
	s_nop 1
	v_cndmask_b32_e64 v178, v178, v29, s[8:9]
	v_cmp_eq_u32_e64 s[8:9], 14, v11
	s_nop 1
	v_cndmask_b32_e64 v178, v178, v30, s[8:9]
	v_cmp_eq_u32_e64 s[8:9], 15, v11
	s_nop 1
	v_cndmask_b32_e64 v11, v178, v31, s[8:9]
	v_lshl_add_u32 v11, v173, 7, v11
	v_and_b32_e32 v173, 0xff, v10
	v_bitop3_b32 v178, v10, s10, v10 bitop3:0xc
	v_cndmask_b32_e64 v10, v178, v173, s[6:7]
	v_lshrrev_b32_e32 v173, 4, v10
	v_cmp_gt_u32_e64 s[6:7], 16, v10
	v_and_b32_e32 v10, 15, v10
	s_nop 0
	v_cndmask_b32_e64 v178, 0, v49, s[6:7]
	v_cmp_eq_u32_e64 s[6:7], 1, v173
	s_nop 1
	v_cndmask_b32_e64 v178, v178, v48, s[6:7]
	v_cmp_eq_u32_e64 s[6:7], 2, v173
	s_nop 1
	v_cndmask_b32_e64 v178, v178, v47, s[6:7]
	v_cmp_eq_u32_e64 s[6:7], 3, v173
	s_nop 1
	v_cndmask_b32_e64 v178, v178, v46, s[6:7]
	v_cmp_eq_u32_e64 s[6:7], 4, v173
	s_nop 1
	v_cndmask_b32_e64 v178, v178, v45, s[6:7]
	v_cmp_eq_u32_e64 s[6:7], 5, v173
	s_nop 1
	v_cndmask_b32_e64 v178, v178, v44, s[6:7]
	v_cmp_eq_u32_e64 s[6:7], 6, v173
	s_nop 1
	v_cndmask_b32_e64 v178, v178, v43, s[6:7]
	v_cmp_eq_u32_e64 s[6:7], 7, v173
	s_nop 1
	v_cndmask_b32_e64 v178, v178, v42, s[6:7]
	v_cmp_eq_u32_e64 s[6:7], 8, v173
	s_nop 1
	v_cndmask_b32_e64 v178, v178, v41, s[6:7]
	v_cmp_eq_u32_e64 s[6:7], 9, v173
	s_nop 1
	v_cndmask_b32_e64 v178, v178, v40, s[6:7]
	v_cmp_eq_u32_e64 s[6:7], 10, v173
	s_nop 1
	v_cndmask_b32_e64 v178, v178, v39, s[6:7]
	v_cmp_eq_u32_e64 s[6:7], 11, v173
	s_nop 1
	v_cndmask_b32_e64 v178, v178, v38, s[6:7]
	v_cmp_eq_u32_e64 s[6:7], 12, v173
	s_nop 1
	v_cndmask_b32_e64 v178, v178, v37, s[6:7]
	v_cmp_eq_u32_e64 s[6:7], 13, v173
	s_nop 1
	v_cndmask_b32_e64 v178, v178, v36, s[6:7]
	v_cmp_eq_u32_e64 s[6:7], 14, v173
	s_nop 1
	v_cndmask_b32_e64 v178, v178, v35, s[6:7]
	v_cmp_eq_u32_e64 s[6:7], 15, v173
	s_nop 1
	v_cndmask_b32_e64 v173, v178, v34, s[6:7]
	v_cmp_eq_u32_e64 s[6:7], 0, v10
	s_nop 1
	v_cndmask_b32_e64 v178, 0, v33, s[6:7]
	v_cmp_eq_u32_e64 s[6:7], 1, v10
	s_nop 1
	v_cndmask_b32_e64 v178, v178, v17, s[6:7]
	v_cmp_eq_u32_e64 s[6:7], 2, v10
	s_nop 1
	v_cndmask_b32_e64 v178, v178, v18, s[6:7]
	v_cmp_eq_u32_e64 s[6:7], 3, v10
	s_nop 1
	v_cndmask_b32_e64 v178, v178, v19, s[6:7]
	v_cmp_eq_u32_e64 s[6:7], 4, v10
	s_nop 1
	v_cndmask_b32_e64 v178, v178, v20, s[6:7]
	v_cmp_eq_u32_e64 s[6:7], 5, v10
	s_nop 1
	v_cndmask_b32_e64 v178, v178, v21, s[6:7]
	v_cmp_eq_u32_e64 s[6:7], 6, v10
	s_nop 1
	v_cndmask_b32_e64 v178, v178, v22, s[6:7]
	v_cmp_eq_u32_e64 s[6:7], 7, v10
	s_nop 1
	v_cndmask_b32_e64 v178, v178, v23, s[6:7]
	v_cmp_eq_u32_e64 s[6:7], 8, v10
	s_nop 1
	v_cndmask_b32_e64 v178, v178, v24, s[6:7]
	v_cmp_eq_u32_e64 s[6:7], 9, v10
	s_nop 1
	v_cndmask_b32_e64 v178, v178, v25, s[6:7]
	v_cmp_eq_u32_e64 s[6:7], 10, v10
	s_nop 1
	v_cndmask_b32_e64 v178, v178, v26, s[6:7]
	v_cmp_eq_u32_e64 s[6:7], 11, v10
	s_nop 1
	v_cndmask_b32_e64 v178, v178, v27, s[6:7]
	v_cmp_eq_u32_e64 s[6:7], 12, v10
	s_nop 1
	v_cndmask_b32_e64 v178, v178, v28, s[6:7]
	v_cmp_eq_u32_e64 s[6:7], 13, v10
	s_nop 1
	v_cndmask_b32_e64 v178, v178, v29, s[6:7]
	v_cmp_eq_u32_e64 s[6:7], 14, v10
	s_nop 1
	v_cndmask_b32_e64 v178, v178, v30, s[6:7]
	v_cmp_eq_u32_e64 s[6:7], 15, v10
	s_nop 1
	v_cndmask_b32_e64 v10, v178, v31, s[6:7]
	v_lshl_add_u32 v10, v173, 7, v10
	v_min_f32_e32 v9, v8, v58
	v_and_b32_e32 v173, 0xff, v9
	v_bitop3_b32 v178, v9, s10, v9 bitop3:0xc
	v_cmp_gt_i32_e64 s[8:9], 0, v9
	v_and_b32_e32 v56, 0xffffff00, v9
	v_max_f32_e32 v8, v8, v58
	v_cndmask_b32_e64 v9, v178, v173, s[8:9]
	v_lshrrev_b32_e32 v173, 4, v9
	v_cmp_gt_u32_e64 s[8:9], 16, v9
	v_and_b32_e32 v9, 15, v9
	v_cmp_gt_i32_e64 s[6:7], 0, v8
	v_cndmask_b32_e64 v178, 0, v49, s[8:9]
	v_cmp_eq_u32_e64 s[8:9], 1, v173
	v_and_b32_e32 v58, 0xffffff00, v8
	s_nop 0
	v_cndmask_b32_e64 v178, v178, v48, s[8:9]
	v_cmp_eq_u32_e64 s[8:9], 2, v173
	s_nop 1
	v_cndmask_b32_e64 v178, v178, v47, s[8:9]
	v_cmp_eq_u32_e64 s[8:9], 3, v173
	s_nop 1
	v_cndmask_b32_e64 v178, v178, v46, s[8:9]
	v_cmp_eq_u32_e64 s[8:9], 4, v173
	s_nop 1
	v_cndmask_b32_e64 v178, v178, v45, s[8:9]
	v_cmp_eq_u32_e64 s[8:9], 5, v173
	s_nop 1
	v_cndmask_b32_e64 v178, v178, v44, s[8:9]
	v_cmp_eq_u32_e64 s[8:9], 6, v173
	s_nop 1
	v_cndmask_b32_e64 v178, v178, v43, s[8:9]
	v_cmp_eq_u32_e64 s[8:9], 7, v173
	s_nop 1
	v_cndmask_b32_e64 v178, v178, v42, s[8:9]
	v_cmp_eq_u32_e64 s[8:9], 8, v173
	s_nop 1
	v_cndmask_b32_e64 v178, v178, v41, s[8:9]
	v_cmp_eq_u32_e64 s[8:9], 9, v173
	s_nop 1
	v_cndmask_b32_e64 v178, v178, v40, s[8:9]
	v_cmp_eq_u32_e64 s[8:9], 10, v173
	s_nop 1
	v_cndmask_b32_e64 v178, v178, v39, s[8:9]
	v_cmp_eq_u32_e64 s[8:9], 11, v173
	s_nop 1
	v_cndmask_b32_e64 v178, v178, v38, s[8:9]
	v_cmp_eq_u32_e64 s[8:9], 12, v173
	s_nop 1
	v_cndmask_b32_e64 v178, v178, v37, s[8:9]
	v_cmp_eq_u32_e64 s[8:9], 13, v173
	s_nop 1
	v_cndmask_b32_e64 v178, v178, v36, s[8:9]
	v_cmp_eq_u32_e64 s[8:9], 14, v173
	s_nop 1
	v_cndmask_b32_e64 v178, v178, v35, s[8:9]
	v_cmp_eq_u32_e64 s[8:9], 15, v173
	s_nop 1
	v_cndmask_b32_e64 v173, v178, v34, s[8:9]
	v_cmp_eq_u32_e64 s[8:9], 0, v9
	s_nop 1
	v_cndmask_b32_e64 v178, 0, v33, s[8:9]
	v_cmp_eq_u32_e64 s[8:9], 1, v9
	s_nop 1
	v_cndmask_b32_e64 v178, v178, v17, s[8:9]
	v_cmp_eq_u32_e64 s[8:9], 2, v9
	s_nop 1
	v_cndmask_b32_e64 v178, v178, v18, s[8:9]
	v_cmp_eq_u32_e64 s[8:9], 3, v9
	s_nop 1
	v_cndmask_b32_e64 v178, v178, v19, s[8:9]
	v_cmp_eq_u32_e64 s[8:9], 4, v9
	s_nop 1
	v_cndmask_b32_e64 v178, v178, v20, s[8:9]
	v_cmp_eq_u32_e64 s[8:9], 5, v9
	s_nop 1
	v_cndmask_b32_e64 v178, v178, v21, s[8:9]
	v_cmp_eq_u32_e64 s[8:9], 6, v9
	s_nop 1
	v_cndmask_b32_e64 v178, v178, v22, s[8:9]
	v_cmp_eq_u32_e64 s[8:9], 7, v9
	s_nop 1
	v_cndmask_b32_e64 v178, v178, v23, s[8:9]
	v_cmp_eq_u32_e64 s[8:9], 8, v9
	s_nop 1
	v_cndmask_b32_e64 v178, v178, v24, s[8:9]
	v_cmp_eq_u32_e64 s[8:9], 9, v9
	s_nop 1
	v_cndmask_b32_e64 v178, v178, v25, s[8:9]
	v_cmp_eq_u32_e64 s[8:9], 10, v9
	s_nop 1
	v_cndmask_b32_e64 v178, v178, v26, s[8:9]
	v_cmp_eq_u32_e64 s[8:9], 11, v9
	s_nop 1
	v_cndmask_b32_e64 v178, v178, v27, s[8:9]
	v_cmp_eq_u32_e64 s[8:9], 12, v9
	s_nop 1
	v_cndmask_b32_e64 v178, v178, v28, s[8:9]
	v_cmp_eq_u32_e64 s[8:9], 13, v9
	s_nop 1
	v_cndmask_b32_e64 v178, v178, v29, s[8:9]
	v_cmp_eq_u32_e64 s[8:9], 14, v9
	s_nop 1
	v_cndmask_b32_e64 v178, v178, v30, s[8:9]
	v_cmp_eq_u32_e64 s[8:9], 15, v9
	s_nop 1
	v_cndmask_b32_e64 v9, v178, v31, s[8:9]
	v_lshl_add_u32 v9, v173, 7, v9
	v_and_b32_e32 v173, 0xff, v8
	v_bitop3_b32 v178, v8, s10, v8 bitop3:0xc
	v_cndmask_b32_e64 v8, v178, v173, s[6:7]
	v_lshrrev_b32_e32 v173, 4, v8
	v_cmp_gt_u32_e64 s[6:7], 16, v8
	v_and_b32_e32 v8, 15, v8
	s_nop 0
	v_cndmask_b32_e64 v178, 0, v49, s[6:7]
	v_cmp_eq_u32_e64 s[6:7], 1, v173
	s_nop 1
	v_cndmask_b32_e64 v178, v178, v48, s[6:7]
	v_cmp_eq_u32_e64 s[6:7], 2, v173
	s_nop 1
	v_cndmask_b32_e64 v178, v178, v47, s[6:7]
	v_cmp_eq_u32_e64 s[6:7], 3, v173
	s_nop 1
	v_cndmask_b32_e64 v178, v178, v46, s[6:7]
	v_cmp_eq_u32_e64 s[6:7], 4, v173
	s_nop 1
	v_cndmask_b32_e64 v178, v178, v45, s[6:7]
	v_cmp_eq_u32_e64 s[6:7], 5, v173
	s_nop 1
	v_cndmask_b32_e64 v178, v178, v44, s[6:7]
	v_cmp_eq_u32_e64 s[6:7], 6, v173
	s_nop 1
	v_cndmask_b32_e64 v178, v178, v43, s[6:7]
	v_cmp_eq_u32_e64 s[6:7], 7, v173
	s_nop 1
	v_cndmask_b32_e64 v178, v178, v42, s[6:7]
	v_cmp_eq_u32_e64 s[6:7], 8, v173
	s_nop 1
	v_cndmask_b32_e64 v178, v178, v41, s[6:7]
	v_cmp_eq_u32_e64 s[6:7], 9, v173
	s_nop 1
	v_cndmask_b32_e64 v178, v178, v40, s[6:7]
	v_cmp_eq_u32_e64 s[6:7], 10, v173
	s_nop 1
	v_cndmask_b32_e64 v178, v178, v39, s[6:7]
	v_cmp_eq_u32_e64 s[6:7], 11, v173
	s_nop 1
	v_cndmask_b32_e64 v178, v178, v38, s[6:7]
	v_cmp_eq_u32_e64 s[6:7], 12, v173
	s_nop 1
	v_cndmask_b32_e64 v178, v178, v37, s[6:7]
	v_cmp_eq_u32_e64 s[6:7], 13, v173
	s_nop 1
	v_cndmask_b32_e64 v178, v178, v36, s[6:7]
	v_cmp_eq_u32_e64 s[6:7], 14, v173
	s_nop 1
	v_cndmask_b32_e64 v178, v178, v35, s[6:7]
	v_cmp_eq_u32_e64 s[6:7], 15, v173
	s_nop 1
	v_cndmask_b32_e64 v173, v178, v34, s[6:7]
	v_cmp_eq_u32_e64 s[6:7], 0, v8
	s_nop 1
	v_cndmask_b32_e64 v178, 0, v33, s[6:7]
	v_cmp_eq_u32_e64 s[6:7], 1, v8
	s_nop 1
	v_cndmask_b32_e64 v178, v178, v17, s[6:7]
	v_cmp_eq_u32_e64 s[6:7], 2, v8
	s_nop 1
	v_cndmask_b32_e64 v178, v178, v18, s[6:7]
	v_cmp_eq_u32_e64 s[6:7], 3, v8
	s_nop 1
	v_cndmask_b32_e64 v178, v178, v19, s[6:7]
	v_cmp_eq_u32_e64 s[6:7], 4, v8
	s_nop 1
	v_cndmask_b32_e64 v178, v178, v20, s[6:7]
	v_cmp_eq_u32_e64 s[6:7], 5, v8
	s_nop 1
	v_cndmask_b32_e64 v178, v178, v21, s[6:7]
	v_cmp_eq_u32_e64 s[6:7], 6, v8
	s_nop 1
	v_cndmask_b32_e64 v178, v178, v22, s[6:7]
	v_cmp_eq_u32_e64 s[6:7], 7, v8
	s_nop 1
	v_cndmask_b32_e64 v178, v178, v23, s[6:7]
	v_cmp_eq_u32_e64 s[6:7], 8, v8
	s_nop 1
	v_cndmask_b32_e64 v178, v178, v24, s[6:7]
	v_cmp_eq_u32_e64 s[6:7], 9, v8
	s_nop 1
	v_cndmask_b32_e64 v178, v178, v25, s[6:7]
	v_cmp_eq_u32_e64 s[6:7], 10, v8
	s_nop 1
	v_cndmask_b32_e64 v178, v178, v26, s[6:7]
	v_cmp_eq_u32_e64 s[6:7], 11, v8
	s_nop 1
	v_cndmask_b32_e64 v178, v178, v27, s[6:7]
	v_cmp_eq_u32_e64 s[6:7], 12, v8
	s_nop 1
	v_cndmask_b32_e64 v178, v178, v28, s[6:7]
	v_cmp_eq_u32_e64 s[6:7], 13, v8
	s_nop 1
	v_cndmask_b32_e64 v178, v178, v29, s[6:7]
	v_cmp_eq_u32_e64 s[6:7], 14, v8
	s_nop 1
	v_cndmask_b32_e64 v178, v178, v30, s[6:7]
	v_cmp_eq_u32_e64 s[6:7], 15, v8
	s_nop 1
	v_cndmask_b32_e64 v8, v178, v31, s[6:7]
	v_lshl_add_u32 v8, v173, 7, v8
	v_min_f32_e32 v15, v14, v62
	v_and_b32_e32 v173, 0xff, v15
	v_bitop3_b32 v178, v15, s10, v15 bitop3:0xc
	v_cmp_gt_i32_e64 s[8:9], 0, v15
	v_and_b32_e32 v63, 0xffffff00, v15
	v_max_f32_e32 v14, v14, v62
	v_cndmask_b32_e64 v15, v178, v173, s[8:9]
	v_lshrrev_b32_e32 v173, 4, v15
	v_cmp_gt_u32_e64 s[8:9], 16, v15
	v_and_b32_e32 v15, 15, v15
	v_cmp_gt_i32_e64 s[6:7], 0, v14
	v_cndmask_b32_e64 v178, 0, v49, s[8:9]
	v_cmp_eq_u32_e64 s[8:9], 1, v173
	v_and_b32_e32 v62, 0xffffff00, v14
	s_nop 0
	v_cndmask_b32_e64 v178, v178, v48, s[8:9]
	v_cmp_eq_u32_e64 s[8:9], 2, v173
	s_nop 1
	v_cndmask_b32_e64 v178, v178, v47, s[8:9]
	v_cmp_eq_u32_e64 s[8:9], 3, v173
	s_nop 1
	v_cndmask_b32_e64 v178, v178, v46, s[8:9]
	v_cmp_eq_u32_e64 s[8:9], 4, v173
	s_nop 1
	v_cndmask_b32_e64 v178, v178, v45, s[8:9]
	v_cmp_eq_u32_e64 s[8:9], 5, v173
	s_nop 1
	v_cndmask_b32_e64 v178, v178, v44, s[8:9]
	v_cmp_eq_u32_e64 s[8:9], 6, v173
	s_nop 1
	v_cndmask_b32_e64 v178, v178, v43, s[8:9]
	v_cmp_eq_u32_e64 s[8:9], 7, v173
	s_nop 1
	v_cndmask_b32_e64 v178, v178, v42, s[8:9]
	v_cmp_eq_u32_e64 s[8:9], 8, v173
	s_nop 1
	v_cndmask_b32_e64 v178, v178, v41, s[8:9]
	v_cmp_eq_u32_e64 s[8:9], 9, v173
	s_nop 1
	v_cndmask_b32_e64 v178, v178, v40, s[8:9]
	v_cmp_eq_u32_e64 s[8:9], 10, v173
	s_nop 1
	v_cndmask_b32_e64 v178, v178, v39, s[8:9]
	v_cmp_eq_u32_e64 s[8:9], 11, v173
	s_nop 1
	v_cndmask_b32_e64 v178, v178, v38, s[8:9]
	v_cmp_eq_u32_e64 s[8:9], 12, v173
	s_nop 1
	v_cndmask_b32_e64 v178, v178, v37, s[8:9]
	v_cmp_eq_u32_e64 s[8:9], 13, v173
	s_nop 1
	v_cndmask_b32_e64 v178, v178, v36, s[8:9]
	v_cmp_eq_u32_e64 s[8:9], 14, v173
	s_nop 1
	v_cndmask_b32_e64 v178, v178, v35, s[8:9]
	v_cmp_eq_u32_e64 s[8:9], 15, v173
	s_nop 1
	v_cndmask_b32_e64 v173, v178, v34, s[8:9]
	v_cmp_eq_u32_e64 s[8:9], 0, v15
	s_nop 1
	v_cndmask_b32_e64 v178, 0, v33, s[8:9]
	v_cmp_eq_u32_e64 s[8:9], 1, v15
	s_nop 1
	v_cndmask_b32_e64 v178, v178, v17, s[8:9]
	v_cmp_eq_u32_e64 s[8:9], 2, v15
	s_nop 1
	v_cndmask_b32_e64 v178, v178, v18, s[8:9]
	v_cmp_eq_u32_e64 s[8:9], 3, v15
	s_nop 1
	v_cndmask_b32_e64 v178, v178, v19, s[8:9]
	v_cmp_eq_u32_e64 s[8:9], 4, v15
	s_nop 1
	v_cndmask_b32_e64 v178, v178, v20, s[8:9]
	v_cmp_eq_u32_e64 s[8:9], 5, v15
	s_nop 1
	v_cndmask_b32_e64 v178, v178, v21, s[8:9]
	v_cmp_eq_u32_e64 s[8:9], 6, v15
	s_nop 1
	v_cndmask_b32_e64 v178, v178, v22, s[8:9]
	v_cmp_eq_u32_e64 s[8:9], 7, v15
	s_nop 1
	v_cndmask_b32_e64 v178, v178, v23, s[8:9]
	v_cmp_eq_u32_e64 s[8:9], 8, v15
	s_nop 1
	v_cndmask_b32_e64 v178, v178, v24, s[8:9]
	v_cmp_eq_u32_e64 s[8:9], 9, v15
	s_nop 1
	v_cndmask_b32_e64 v178, v178, v25, s[8:9]
	v_cmp_eq_u32_e64 s[8:9], 10, v15
	s_nop 1
	v_cndmask_b32_e64 v178, v178, v26, s[8:9]
	v_cmp_eq_u32_e64 s[8:9], 11, v15
	s_nop 1
	v_cndmask_b32_e64 v178, v178, v27, s[8:9]
	v_cmp_eq_u32_e64 s[8:9], 12, v15
	s_nop 1
	v_cndmask_b32_e64 v178, v178, v28, s[8:9]
	v_cmp_eq_u32_e64 s[8:9], 13, v15
	s_nop 1
	v_cndmask_b32_e64 v178, v178, v29, s[8:9]
	v_cmp_eq_u32_e64 s[8:9], 14, v15
	s_nop 1
	v_cndmask_b32_e64 v178, v178, v30, s[8:9]
	v_cmp_eq_u32_e64 s[8:9], 15, v15
	s_nop 1
	v_cndmask_b32_e64 v15, v178, v31, s[8:9]
	v_lshl_add_u32 v15, v173, 7, v15
	v_and_b32_e32 v173, 0xff, v14
	v_bitop3_b32 v178, v14, s10, v14 bitop3:0xc
	v_cndmask_b32_e64 v14, v178, v173, s[6:7]
	v_lshrrev_b32_e32 v173, 4, v14
	v_cmp_gt_u32_e64 s[6:7], 16, v14
	v_and_b32_e32 v14, 15, v14
	v_readlane_b32 s8, v253, 23
	v_cndmask_b32_e64 v178, 0, v49, s[6:7]
	v_cmp_eq_u32_e64 s[6:7], 1, v173
	v_readlane_b32 s9, v253, 24
	s_nop 0
	v_cndmask_b32_e64 v178, v178, v48, s[6:7]
	v_cmp_eq_u32_e64 s[6:7], 2, v173
	s_nop 1
	v_cndmask_b32_e64 v178, v178, v47, s[6:7]
	v_cmp_eq_u32_e64 s[6:7], 3, v173
	s_nop 1
	v_cndmask_b32_e64 v178, v178, v46, s[6:7]
	v_cmp_eq_u32_e64 s[6:7], 4, v173
	s_nop 1
	v_cndmask_b32_e64 v178, v178, v45, s[6:7]
	v_cmp_eq_u32_e64 s[6:7], 5, v173
	s_nop 1
	v_cndmask_b32_e64 v178, v178, v44, s[6:7]
	v_cmp_eq_u32_e64 s[6:7], 6, v173
	s_nop 1
	v_cndmask_b32_e64 v178, v178, v43, s[6:7]
	v_cmp_eq_u32_e64 s[6:7], 7, v173
	s_nop 1
	v_cndmask_b32_e64 v178, v178, v42, s[6:7]
	v_cmp_eq_u32_e64 s[6:7], 8, v173
	s_nop 1
	v_cndmask_b32_e64 v178, v178, v41, s[6:7]
	v_cmp_eq_u32_e64 s[6:7], 9, v173
	s_nop 1
	v_cndmask_b32_e64 v178, v178, v40, s[6:7]
	v_cmp_eq_u32_e64 s[6:7], 10, v173
	s_nop 1
	v_cndmask_b32_e64 v178, v178, v39, s[6:7]
	v_cmp_eq_u32_e64 s[6:7], 11, v173
	s_nop 1
	v_cndmask_b32_e64 v178, v178, v38, s[6:7]
	v_cmp_eq_u32_e64 s[6:7], 12, v173
	s_nop 1
	v_cndmask_b32_e64 v178, v178, v37, s[6:7]
	v_cmp_eq_u32_e64 s[6:7], 13, v173
	s_nop 1
	v_cndmask_b32_e64 v178, v178, v36, s[6:7]
	v_cmp_eq_u32_e64 s[6:7], 14, v173
	s_nop 1
	v_cndmask_b32_e64 v178, v178, v35, s[6:7]
	v_cmp_eq_u32_e64 s[6:7], 15, v173
	s_nop 1
	v_cndmask_b32_e64 v173, v178, v34, s[6:7]
	v_cmp_eq_u32_e64 s[6:7], 0, v14
	s_nop 1
	v_cndmask_b32_e64 v178, 0, v33, s[6:7]
	v_cmp_eq_u32_e64 s[6:7], 1, v14
	s_nop 1
	v_cndmask_b32_e64 v178, v178, v17, s[6:7]
	v_cmp_eq_u32_e64 s[6:7], 2, v14
	s_nop 1
	v_cndmask_b32_e64 v178, v178, v18, s[6:7]
	v_cmp_eq_u32_e64 s[6:7], 3, v14
	s_nop 1
	v_cndmask_b32_e64 v178, v178, v19, s[6:7]
	v_cmp_eq_u32_e64 s[6:7], 4, v14
	s_nop 1
	v_cndmask_b32_e64 v178, v178, v20, s[6:7]
	v_cmp_eq_u32_e64 s[6:7], 5, v14
	s_nop 1
	v_cndmask_b32_e64 v178, v178, v21, s[6:7]
	v_cmp_eq_u32_e64 s[6:7], 6, v14
	s_nop 1
	v_cndmask_b32_e64 v178, v178, v22, s[6:7]
	v_cmp_eq_u32_e64 s[6:7], 7, v14
	s_nop 1
	v_cndmask_b32_e64 v178, v178, v23, s[6:7]
	v_cmp_eq_u32_e64 s[6:7], 8, v14
	s_nop 1
	v_cndmask_b32_e64 v178, v178, v24, s[6:7]
	v_cmp_eq_u32_e64 s[6:7], 9, v14
	s_nop 1
	v_cndmask_b32_e64 v178, v178, v25, s[6:7]
	v_cmp_eq_u32_e64 s[6:7], 10, v14
	s_nop 1
	v_cndmask_b32_e64 v178, v178, v26, s[6:7]
	v_cmp_eq_u32_e64 s[6:7], 11, v14
	s_nop 1
	v_cndmask_b32_e64 v178, v178, v27, s[6:7]
	v_cmp_eq_u32_e64 s[6:7], 12, v14
	s_nop 1
	v_cndmask_b32_e64 v178, v178, v28, s[6:7]
	v_cmp_eq_u32_e64 s[6:7], 13, v14
	s_nop 1
	v_cndmask_b32_e64 v178, v178, v29, s[6:7]
	v_cmp_eq_u32_e64 s[6:7], 14, v14
	s_nop 1
	v_cndmask_b32_e64 v178, v178, v30, s[6:7]
	v_cmp_eq_u32_e64 s[6:7], 15, v14
	s_nop 1
	v_cndmask_b32_e64 v14, v178, v31, s[6:7]
	v_lshl_add_u32 v14, v173, 7, v14
	v_and_b32_e32 v173, 0xff, v13
	v_bitop3_b32 v178, v13, s10, v13 bitop3:0xc
	v_cmp_gt_i32_e64 s[6:7], 0, v13
	s_nop 1
	v_cndmask_b32_e64 v13, v178, v173, s[6:7]
	v_lshrrev_b32_e32 v173, 4, v13
	v_cmp_gt_u32_e64 s[6:7], 16, v13
	v_and_b32_e32 v13, 15, v13
	s_nop 0
	v_cndmask_b32_e64 v178, 0, v49, s[6:7]
	v_cmp_eq_u32_e64 s[6:7], 1, v173
	s_nop 1
	v_cndmask_b32_e64 v178, v178, v48, s[6:7]
	v_cmp_eq_u32_e64 s[6:7], 2, v173
	s_nop 1
	v_cndmask_b32_e64 v178, v178, v47, s[6:7]
	v_cmp_eq_u32_e64 s[6:7], 3, v173
	s_nop 1
	v_cndmask_b32_e64 v178, v178, v46, s[6:7]
	v_cmp_eq_u32_e64 s[6:7], 4, v173
	s_nop 1
	v_cndmask_b32_e64 v178, v178, v45, s[6:7]
	v_cmp_eq_u32_e64 s[6:7], 5, v173
	s_nop 1
	v_cndmask_b32_e64 v178, v178, v44, s[6:7]
	v_cmp_eq_u32_e64 s[6:7], 6, v173
	s_nop 1
	v_cndmask_b32_e64 v178, v178, v43, s[6:7]
	v_cmp_eq_u32_e64 s[6:7], 7, v173
	s_nop 1
	v_cndmask_b32_e64 v178, v178, v42, s[6:7]
	v_cmp_eq_u32_e64 s[6:7], 8, v173
	s_nop 1
	v_cndmask_b32_e64 v178, v178, v41, s[6:7]
	v_cmp_eq_u32_e64 s[6:7], 9, v173
	s_nop 1
	v_cndmask_b32_e64 v178, v178, v40, s[6:7]
	v_cmp_eq_u32_e64 s[6:7], 10, v173
	s_nop 1
	v_cndmask_b32_e64 v178, v178, v39, s[6:7]
	v_cmp_eq_u32_e64 s[6:7], 11, v173
	s_nop 1
	v_cndmask_b32_e64 v178, v178, v38, s[6:7]
	v_cmp_eq_u32_e64 s[6:7], 12, v173
	s_nop 1
	v_cndmask_b32_e64 v178, v178, v37, s[6:7]
	v_cmp_eq_u32_e64 s[6:7], 13, v173
	s_nop 1
	v_cndmask_b32_e64 v178, v178, v36, s[6:7]
	v_cmp_eq_u32_e64 s[6:7], 14, v173
	s_nop 1
	v_cndmask_b32_e64 v178, v178, v35, s[6:7]
	v_cmp_eq_u32_e64 s[6:7], 15, v173
	s_nop 1
	v_cndmask_b32_e64 v173, v178, v34, s[6:7]
	v_cmp_eq_u32_e64 s[6:7], 0, v13
	s_nop 1
	v_cndmask_b32_e64 v178, 0, v33, s[6:7]
	v_cmp_eq_u32_e64 s[6:7], 1, v13
	s_nop 1
	v_cndmask_b32_e64 v178, v178, v17, s[6:7]
	v_cmp_eq_u32_e64 s[6:7], 2, v13
	s_nop 1
	v_cndmask_b32_e64 v178, v178, v18, s[6:7]
	v_cmp_eq_u32_e64 s[6:7], 3, v13
	s_nop 1
	v_cndmask_b32_e64 v178, v178, v19, s[6:7]
	v_cmp_eq_u32_e64 s[6:7], 4, v13
	s_nop 1
	v_cndmask_b32_e64 v178, v178, v20, s[6:7]
	v_cmp_eq_u32_e64 s[6:7], 5, v13
	s_nop 1
	v_cndmask_b32_e64 v178, v178, v21, s[6:7]
	v_cmp_eq_u32_e64 s[6:7], 6, v13
	s_nop 1
	v_cndmask_b32_e64 v178, v178, v22, s[6:7]
	v_cmp_eq_u32_e64 s[6:7], 7, v13
	s_nop 1
	v_cndmask_b32_e64 v178, v178, v23, s[6:7]
	v_cmp_eq_u32_e64 s[6:7], 8, v13
	s_nop 1
	v_cndmask_b32_e64 v178, v178, v24, s[6:7]
	v_cmp_eq_u32_e64 s[6:7], 9, v13
	s_nop 1
	v_cndmask_b32_e64 v178, v178, v25, s[6:7]
	v_cmp_eq_u32_e64 s[6:7], 10, v13
	s_nop 1
	v_cndmask_b32_e64 v178, v178, v26, s[6:7]
	v_cmp_eq_u32_e64 s[6:7], 11, v13
	s_nop 1
	v_cndmask_b32_e64 v178, v178, v27, s[6:7]
	v_cmp_eq_u32_e64 s[6:7], 12, v13
	s_nop 1
	v_cndmask_b32_e64 v178, v178, v28, s[6:7]
	v_cmp_eq_u32_e64 s[6:7], 13, v13
	s_nop 1
	v_cndmask_b32_e64 v178, v178, v29, s[6:7]
	v_cmp_eq_u32_e64 s[6:7], 14, v13
	s_nop 1
	v_cndmask_b32_e64 v178, v178, v30, s[6:7]
	v_cmp_eq_u32_e64 s[6:7], 15, v13
	s_nop 1
	v_cndmask_b32_e64 v13, v178, v31, s[6:7]
	v_lshl_add_u32 v13, v173, 7, v13
	v_and_b32_e32 v173, 0xff, v59
	v_bitop3_b32 v178, v59, s10, v59 bitop3:0xc
	v_cndmask_b32_e32 v59, v178, v173, vcc
	v_lshrrev_b32_e32 v173, 4, v59
	v_cmp_gt_u32_e32 vcc, 16, v59
	s_nop 1
	v_cndmask_b32_e32 v49, 0, v49, vcc
	v_cmp_eq_u32_e32 vcc, 1, v173
	s_nop 1
	v_cndmask_b32_e32 v48, v49, v48, vcc
	v_cmp_eq_u32_e32 vcc, 2, v173
	s_nop 1
	v_cndmask_b32_e32 v47, v48, v47, vcc
	v_cmp_eq_u32_e32 vcc, 3, v173
	s_nop 1
	v_cndmask_b32_e32 v46, v47, v46, vcc
	v_cmp_eq_u32_e32 vcc, 4, v173
	s_nop 1
	v_cndmask_b32_e32 v45, v46, v45, vcc
	v_cmp_eq_u32_e32 vcc, 5, v173
	s_nop 1
	v_cndmask_b32_e32 v44, v45, v44, vcc
	v_cmp_eq_u32_e32 vcc, 6, v173
	s_nop 1
	v_cndmask_b32_e32 v43, v44, v43, vcc
	v_cmp_eq_u32_e32 vcc, 7, v173
	s_nop 1
	v_cndmask_b32_e32 v42, v43, v42, vcc
	v_cmp_eq_u32_e32 vcc, 8, v173
	s_nop 1
	v_cndmask_b32_e32 v41, v42, v41, vcc
	v_cmp_eq_u32_e32 vcc, 9, v173
	s_nop 1
	v_cndmask_b32_e32 v40, v41, v40, vcc
	v_cmp_eq_u32_e32 vcc, 10, v173
	s_nop 1
	v_cndmask_b32_e32 v39, v40, v39, vcc
	v_cmp_eq_u32_e32 vcc, 11, v173
	s_nop 1
	v_cndmask_b32_e32 v38, v39, v38, vcc
	v_cmp_eq_u32_e32 vcc, 12, v173
	v_and_b32_e32 v39, 15, v59
	s_nop 0
	v_cndmask_b32_e32 v37, v38, v37, vcc
	v_cmp_eq_u32_e32 vcc, 13, v173
	s_nop 1
	v_cndmask_b32_e32 v36, v37, v36, vcc
	v_cmp_eq_u32_e32 vcc, 14, v173
	s_nop 1
	v_cndmask_b32_e32 v35, v36, v35, vcc
	v_cmp_eq_u32_e32 vcc, 15, v173
	v_exp_f32_e32 v36, v12
	v_and_b32_e32 v12, 0xffffff00, v32
	v_cndmask_b32_e32 v38, v35, v34, vcc
	v_cmp_eq_u32_e32 vcc, 0, v39
	v_sub_f32_e32 v12, v12, v60
	v_mul_f32_e32 v12, 0x3fb8aa3b, v12
	v_cndmask_b32_e32 v33, 0, v33, vcc
	v_cmp_eq_u32_e32 vcc, 1, v39
	v_exp_f32_e32 v37, v12
	s_nop 0
	v_cndmask_b32_e32 v17, v33, v17, vcc
	v_cmp_eq_u32_e32 vcc, 2, v39
	v_sub_f32_e32 v33, v51, v60
	v_mul_f32_e32 v33, 0x3fb8aa3b, v33
	v_cndmask_b32_e32 v17, v17, v18, vcc
	v_cmp_eq_u32_e32 vcc, 3, v39
	v_sub_f32_e32 v18, v60, v60
	v_mul_f32_e32 v18, 0x3fb8aa3b, v18
	v_cndmask_b32_e32 v17, v17, v19, vcc
	v_cmp_eq_u32_e32 vcc, 4, v39
	v_sub_f32_e32 v19, v61, v60
	v_exp_f32_e32 v18, v18
	v_cndmask_b32_e32 v17, v17, v20, vcc
	v_cmp_eq_u32_e32 vcc, 5, v39
	v_mul_f32_e32 v19, 0x3fb8aa3b, v19
	v_sub_f32_e32 v20, v62, v60
	v_cndmask_b32_e32 v17, v17, v21, vcc
	v_exp_f32_e32 v19, v19
	v_mul_f32_e32 v20, 0x3fb8aa3b, v20
	v_sub_f32_e32 v21, v63, v60
	v_cmp_eq_u32_e32 vcc, 6, v39
	v_exp_f32_e32 v20, v20
	v_mul_f32_e32 v21, 0x3fb8aa3b, v21
	v_cndmask_b32_e32 v17, v17, v22, vcc
	v_cmp_eq_u32_e32 vcc, 7, v39
	v_exp_f32_e32 v21, v21
	v_add_f32_e32 v22, 0, v18
	v_cndmask_b32_e32 v17, v17, v23, vcc
	v_cmp_eq_u32_e32 vcc, 8, v39
	v_add_f32_e32 v22, v19, v22
	v_add_f32_e32 v22, v20, v22
	v_cndmask_b32_e32 v17, v17, v24, vcc
	v_cmp_eq_u32_e32 vcc, 9, v39
	v_sub_f32_e32 v23, v56, v60
	v_mul_f32_e32 v23, 0x3fb8aa3b, v23
	v_cndmask_b32_e32 v17, v17, v25, vcc
	v_cmp_eq_u32_e32 vcc, 10, v39
	v_sub_f32_e32 v24, v55, v60
	v_exp_f32_e32 v23, v23
	v_cndmask_b32_e32 v17, v17, v26, vcc
	v_add_f32_e32 v26, v21, v22
	v_sub_f32_e32 v22, v58, v60
	v_mul_f32_e32 v22, 0x3fb8aa3b, v22
	v_exp_f32_e32 v22, v22
	v_mul_f32_e32 v24, 0x3fb8aa3b, v24
	v_sub_f32_e32 v25, v54, v60
	v_exp_f32_e32 v24, v24
	v_mul_f32_e32 v25, 0x3fb8aa3b, v25
	v_cmp_eq_u32_e32 vcc, 11, v39
	v_exp_f32_e32 v25, v25
	v_add_f32_e32 v26, v22, v26
	v_cndmask_b32_e32 v17, v17, v27, vcc
	v_cmp_eq_u32_e32 vcc, 12, v39
	v_add_f32_e32 v26, v23, v26
	v_add_f32_e32 v26, v24, v26
	v_cndmask_b32_e32 v17, v17, v28, vcc
	v_cmp_eq_u32_e32 vcc, 13, v39
	v_sub_f32_e32 v27, v57, v60
	v_mul_f32_e32 v27, 0x3fb8aa3b, v27
	v_cndmask_b32_e32 v17, v17, v29, vcc
	v_cmp_eq_u32_e32 vcc, 14, v39
	v_sub_f32_e32 v28, v53, v60
	v_exp_f32_e32 v27, v27
	v_cndmask_b32_e32 v17, v17, v30, vcc
	v_add_f32_e32 v30, v25, v26
	v_sub_f32_e32 v26, v209, v60
	v_mul_f32_e32 v26, 0x3fb8aa3b, v26
	v_exp_f32_e32 v26, v26
	v_mul_f32_e32 v28, 0x3fb8aa3b, v28
	v_sub_f32_e32 v29, v52, v60
	v_exp_f32_e32 v28, v28
	v_mul_f32_e32 v29, 0x3fb8aa3b, v29
	v_exp_f32_e32 v29, v29
	v_exp_f32_e32 v34, v33
	v_sub_f32_e32 v33, v50, v60
	v_add_f32_e32 v30, v26, v30
	v_mul_f32_e32 v33, 0x3fb8aa3b, v33
	v_add_f32_e32 v30, v27, v30
	v_exp_f32_e32 v35, v33
	v_add_f32_e32 v30, v28, v30
	v_add_f32_e32 v30, v29, v30
	v_add_f32_e32 v12, v34, v30
	v_add_f32_e32 v12, v35, v12
	v_add_f32_e32 v12, v36, v12
	v_add_f32_e32 v30, v37, v12
	v_div_scale_f32 v32, s[6:7], v30, v30, 1.0
	v_rcp_f32_e32 v33, v32
	v_cmp_eq_u32_e32 vcc, 15, v39
	v_readlane_b32 s6, v255, 46
	s_lshl_b32 s6, s6, 4
	v_cndmask_b32_e32 v12, v17, v31, vcc
	v_fma_f32 v17, -v32, v33, 1.0
	v_fmac_f32_e32 v33, v17, v33
	v_div_scale_f32 v17, vcc, 1.0, v30, 1.0
	v_mul_f32_e32 v31, v17, v33
	v_lshl_add_u32 v12, v38, 7, v12
	v_fma_f32 v38, -v32, v31, v17
	v_fmac_f32_e32 v31, v38, v33
	v_fma_f32 v17, -v32, v31, v17
	v_div_fmas_f32 v17, v17, v33, v31
	v_div_fixup_f32 v30, v17, v30, 1.0
	v_lshlrev_b64 v[16:17], 9, v[176:177]
	s_ashr_i32 s7, s6, 31
	v_lshl_add_u64 v[32:33], s[94:95], 0, v[16:17]
	s_lshl_b64 s[6:7], s[6:7], 2
	v_lshl_add_u64 v[32:33], v[32:33], 0, s[6:7]
	v_lshl_add_u64 v[16:17], s[8:9], 0, v[16:17]
	v_lshl_add_u64 v[16:17], v[16:17], 0, s[6:7]
	global_store_dwordx4 v[32:33], v[12:15], off
	v_readlane_b32 s8, v255, 44
	v_readlane_b32 s9, v255, 45
	v_pk_mul_f32 v[12:13], v[18:19], v[30:31] op_sel_hi:[1,0]
	v_pk_mul_f32 v[14:15], v[20:21], v[30:31] op_sel_hi:[1,0]
	global_store_dwordx4 v[16:17], v[12:15], off
	global_store_dwordx4 v[32:33], v[8:11], off offset:16
	s_nop 1
	v_pk_mul_f32 v[8:9], v[22:23], v[30:31] op_sel_hi:[1,0]
	v_pk_mul_f32 v[10:11], v[24:25], v[30:31] op_sel_hi:[1,0]
	global_store_dwordx4 v[16:17], v[8:11], off offset:16
	global_store_dwordx4 v[32:33], v[4:7], off offset:32
	s_nop 1
	v_pk_mul_f32 v[4:5], v[26:27], v[30:31] op_sel_hi:[1,0]
	v_pk_mul_f32 v[6:7], v[28:29], v[30:31] op_sel_hi:[1,0]
	global_store_dwordx4 v[16:17], v[4:7], off offset:32
	global_store_dwordx4 v[32:33], v[0:3], off offset:48
	s_nop 1
	v_pk_mul_f32 v[0:1], v[34:35], v[30:31] op_sel_hi:[1,0]
	v_pk_mul_f32 v[2:3], v[36:37], v[30:31] op_sel_hi:[1,0]
	global_store_dwordx4 v[16:17], v[0:3], off offset:48
	s_branch .LBB0_696
